# speedup vs baseline: 1.0400x; 1.0400x over previous
_Z6prep_kPKfS0_S0_S0_PDF16_S1_S1_PfS2_:
	s_cmpk_ge_u32 s2, 0x800
	s_cbranch_scc1 .Lpk_nomap
	s_lshr_b32 s4, s2, 3
	s_and_b32 s5, s2, 7
	s_and_b32 s6, s4, 3
	s_lshr_b32 s7, s4, 3
	s_lshl_b32 s7, s7, 2
	s_or_b32 s6, s6, s7
	s_lshl_b32 s6, s6, 3
	s_or_b32 s6, s6, s5
	s_lshr_b32 s7, s4, 2
	s_lshr_b32 s5, s4, 5
	s_xor_b32 s7, s7, s5
	s_and_b32 s7, s7, 1
	s_lshl_b32 s7, s7, 10
	s_or_b32 s2, s6, s7
.Lpk_nomap:
	s_cmpk_lt_i32 s2, 0xc00
	s_mov_b64 s[4:5], -1
	s_cbranch_scc1 .LBB0_3
	s_andn2_b64 vcc, exec, s[4:5]
	s_cbranch_vccz .LBB0_16

.LBB0_11:
	s_andn2_b64 vcc, exec, s[4:5]
	s_cbranch_vccnz .LBB0_15
	s_load_dwordx2 s[8:9], s[0:1], 0x0
	s_load_dwordx2 s[4:5], s[0:1], 0x20
	s_lshl_b32 s11, s2, 5
	s_and_b32 s11, s11, 0x3e0
	v_and_b32_e32 v1, 31, v0
	v_mov_b32_e32 v27, 0
	v_or_b32_e32 v1, s11, v1
	s_waitcnt lgkmcnt(0)
	s_and_b32 s3, s2, 0xffffffe0
	s_lshl_b32 s10, s3, 12
	s_add_u32 s12, s6, s10
	s_addc_u32 s13, s7, 0
	s_lshl_b32 s10, s11, 12
	s_add_u32 s14, s8, s10
	s_addc_u32 s15, s9, 0
	v_lshrrev_b32_e32 v12, 4, v0
	v_and_b32_e32 v13, 15, v0
	v_lshlrev_b32_e32 v2, 12, v12
	v_lshl_add_u32 v2, v13, 4, v2
	v_add_u32_e32 v3, 16384, v2
	v_add_u32_e32 v4, 32768, v2
	v_add_u32_e32 v5, 49152, v2
	v_add_u32_e32 v6, 65536, v2
	v_add_u32_e32 v7, 81920, v2
	v_add_u32_e32 v8, 98304, v2
	v_add_u32_e32 v9, 114688, v2
	v_mul_u32_u24_e32 v10, 144, v12
	v_lshl_add_u32 v10, v13, 3, v10
	v_and_b32_e32 v11, 31, v0
	v_mul_u32_u24_e32 v11, 144, v11
	v_lshrrev_b32_e32 v14, 5, v0
	v_lshl_add_u32 v11, v14, 4, v11
	s_mov_b32 s6, 0x42000000
	s_mov_b32 s7, 0
	s_mov_b32 s10, 15
	global_load_dwordx4 v[24:27], v2, s[12:13]
	global_load_dwordx4 v[28:31], v3, s[12:13]
	global_load_dwordx4 v[32:35], v4, s[12:13]
	global_load_dwordx4 v[36:39], v5, s[12:13]
	global_load_dwordx4 v[40:43], v6, s[12:13]
	global_load_dwordx4 v[44:47], v7, s[12:13]
	global_load_dwordx4 v[48:51], v8, s[12:13]
	global_load_dwordx4 v[52:55], v9, s[12:13]
	global_load_dwordx4 v[56:59], v2, s[14:15]
	global_load_dwordx4 v[60:63], v3, s[14:15]
	global_load_dwordx4 v[64:67], v4, s[14:15]
	global_load_dwordx4 v[68:71], v5, s[14:15]
	global_load_dwordx4 v[72:75], v6, s[14:15]
	global_load_dwordx4 v[76:79], v7, s[14:15]
	global_load_dwordx4 v[80:83], v8, s[14:15]
	global_load_dwordx4 v[84:87], v9, s[14:15]
	v_accvgpr_write_b32 a0, 0
	v_accvgpr_write_b32 a1, 0
	v_accvgpr_write_b32 a2, 0
	v_accvgpr_write_b32 a3, 0
	v_accvgpr_write_b32 a4, 0
	v_accvgpr_write_b32 a5, 0
	v_accvgpr_write_b32 a6, 0
	v_accvgpr_write_b32 a7, 0
	v_accvgpr_write_b32 a8, 0
	v_accvgpr_write_b32 a9, 0
	v_accvgpr_write_b32 a10, 0
	v_accvgpr_write_b32 a11, 0
	v_accvgpr_write_b32 a12, 0
	v_accvgpr_write_b32 a13, 0
	v_accvgpr_write_b32 a14, 0
	v_accvgpr_write_b32 a15, 0
	v_mov_b32_e32 v88, 0
	v_mov_b32_e32 v89, 0
	v_mov_b32_e32 v90, 0
	v_mov_b32_e32 v91, 0
	v_mov_b32_e32 v92, 0
	v_mov_b32_e32 v93, 0
	v_mov_b32_e32 v94, 0
	v_mov_b32_e32 v95, 0
	v_mov_b32_e32 v96, 0
	v_mov_b32_e32 v97, 0
	v_mov_b32_e32 v98, 0
	v_mov_b32_e32 v99, 0
	v_mov_b32_e32 v100, 0
	v_mov_b32_e32 v101, 0
	v_mov_b32_e32 v102, 0
	v_mov_b32_e32 v103, 0
	v_mov_b32_e32 v104, 0
	v_mov_b32_e32 v105, 0
	v_mov_b32_e32 v106, 0
	v_mov_b32_e32 v107, 0
	v_mov_b32_e32 v108, 0
	v_mov_b32_e32 v109, 0
	v_mov_b32_e32 v110, 0
	v_mov_b32_e32 v111, 0
	v_mov_b32_e32 v112, 0
	v_mov_b32_e32 v113, 0
	v_mov_b32_e32 v114, 0
	v_mov_b32_e32 v115, 0
	v_mov_b32_e32 v116, 0
	v_mov_b32_e32 v117, 0
	v_mov_b32_e32 v118, 0
	v_mov_b32_e32 v119, 0
	v_mov_b32_e32 v120, 0
	v_mov_b32_e32 v121, 0
	v_mov_b32_e32 v122, 0
	v_mov_b32_e32 v123, 0
	v_mov_b32_e32 v124, 0
	v_mov_b32_e32 v125, 0
	v_mov_b32_e32 v126, 0
	v_mov_b32_e32 v127, 0
	v_mov_b32_e32 v128, 0
	v_mov_b32_e32 v129, 0
	v_mov_b32_e32 v130, 0
	v_mov_b32_e32 v131, 0
	v_mov_b32_e32 v132, 0
	v_mov_b32_e32 v133, 0
	v_mov_b32_e32 v134, 0
	v_mov_b32_e32 v135, 0
	v_mov_b32_e32 v136, 0
	v_mov_b32_e32 v137, 0
	v_mov_b32_e32 v138, 0
	v_mov_b32_e32 v139, 0
	v_mov_b32_e32 v140, 0
	v_mov_b32_e32 v141, 0
	v_mov_b32_e32 v142, 0
	v_mov_b32_e32 v143, 0
	v_mov_b32_e32 v144, 0
	v_mov_b32_e32 v145, 0
	v_mov_b32_e32 v146, 0
	v_mov_b32_e32 v147, 0
	v_mov_b32_e32 v148, 0
	v_mov_b32_e32 v149, 0
	v_mov_b32_e32 v150, 0
	v_mov_b32_e32 v151, 0
.Lpk_loop:
	s_add_u32 s12, s12, 0x100
	s_addc_u32 s13, s13, 0
	s_add_u32 s14, s14, 0x100
	s_addc_u32 s15, s15, 0
	s_waitcnt vmcnt(15)
	v_pk_mul_f32 v[12:13], v[24:25], s[6:7] op_sel_hi:[1,0]
	v_pk_mul_f32 v[16:17], v[26:27], s[6:7] op_sel_hi:[1,0]
	v_cvt_pk_f16_f32 v20, v12, v13
	v_cvt_pk_f16_f32 v21, v16, v17
	v_cvt_f32_f16_e32 v14, v20
	v_cvt_f32_f16_sdwa v15, v20 dst_sel:DWORD dst_unused:UNUSED_PAD src0_sel:WORD_1
	v_cvt_f32_f16_e32 v18, v21
	v_cvt_f32_f16_sdwa v19, v21 dst_sel:DWORD dst_unused:UNUSED_PAD src0_sel:WORD_1
	v_pk_fma_f32 v[12:13], v[24:25], s[6:7], v[14:15] op_sel_hi:[1,0,1] neg_lo:[0,0,1] neg_hi:[0,0,1]
	v_pk_fma_f32 v[16:17], v[26:27], s[6:7], v[18:19] op_sel_hi:[1,0,1] neg_lo:[0,0,1] neg_hi:[0,0,1]
	v_cvt_pk_f16_f32 v22, v12, v13
	v_cvt_pk_f16_f32 v23, v16, v17
	ds_write_b64 v10, v[20:21] offset:0
	ds_write_b64 v10, v[22:23] offset:4608
	global_load_dwordx4 v[24:27], v2, s[12:13]
	s_waitcnt lgkmcnt(2)
	v_mfma_f32_32x32x16_f16 a[0:15], v[92:95], v[96:99], a[0:15]
	s_waitcnt vmcnt(15)
	v_pk_mul_f32 v[12:13], v[28:29], s[6:7] op_sel_hi:[1,0]
	v_pk_mul_f32 v[16:17], v[30:31], s[6:7] op_sel_hi:[1,0]
	v_cvt_pk_f16_f32 v20, v12, v13
	v_cvt_pk_f16_f32 v21, v16, v17
	v_cvt_f32_f16_e32 v14, v20
	v_cvt_f32_f16_sdwa v15, v20 dst_sel:DWORD dst_unused:UNUSED_PAD src0_sel:WORD_1
	v_cvt_f32_f16_e32 v18, v21
	v_cvt_f32_f16_sdwa v19, v21 dst_sel:DWORD dst_unused:UNUSED_PAD src0_sel:WORD_1
	v_pk_fma_f32 v[12:13], v[28:29], s[6:7], v[14:15] op_sel_hi:[1,0,1] neg_lo:[0,0,1] neg_hi:[0,0,1]
	v_pk_fma_f32 v[16:17], v[30:31], s[6:7], v[18:19] op_sel_hi:[1,0,1] neg_lo:[0,0,1] neg_hi:[0,0,1]
	v_cvt_pk_f16_f32 v22, v12, v13
	v_cvt_pk_f16_f32 v23, v16, v17
	ds_write_b64 v10, v[20:21] offset:576
	ds_write_b64 v10, v[22:23] offset:5184
	global_load_dwordx4 v[28:31], v3, s[12:13]
	v_mfma_f32_32x32x16_f16 a[0:15], v[88:91], v[100:103], a[0:15]
	s_waitcnt vmcnt(15)
	v_pk_mul_f32 v[12:13], v[32:33], s[6:7] op_sel_hi:[1,0]
	v_pk_mul_f32 v[16:17], v[34:35], s[6:7] op_sel_hi:[1,0]
	v_cvt_pk_f16_f32 v20, v12, v13
	v_cvt_pk_f16_f32 v21, v16, v17
	v_cvt_f32_f16_e32 v14, v20
	v_cvt_f32_f16_sdwa v15, v20 dst_sel:DWORD dst_unused:UNUSED_PAD src0_sel:WORD_1
	v_cvt_f32_f16_e32 v18, v21
	v_cvt_f32_f16_sdwa v19, v21 dst_sel:DWORD dst_unused:UNUSED_PAD src0_sel:WORD_1
	v_pk_fma_f32 v[12:13], v[32:33], s[6:7], v[14:15] op_sel_hi:[1,0,1] neg_lo:[0,0,1] neg_hi:[0,0,1]
	v_pk_fma_f32 v[16:17], v[34:35], s[6:7], v[18:19] op_sel_hi:[1,0,1] neg_lo:[0,0,1] neg_hi:[0,0,1]
	v_cvt_pk_f16_f32 v22, v12, v13
	v_cvt_pk_f16_f32 v23, v16, v17
	ds_write_b64 v10, v[20:21] offset:1152
	ds_write_b64 v10, v[22:23] offset:5760
	global_load_dwordx4 v[32:35], v4, s[12:13]
	v_mfma_f32_32x32x16_f16 a[0:15], v[88:91], v[96:99], a[0:15]
	s_waitcnt vmcnt(15)
	v_pk_mul_f32 v[12:13], v[36:37], s[6:7] op_sel_hi:[1,0]
	v_pk_mul_f32 v[16:17], v[38:39], s[6:7] op_sel_hi:[1,0]
	v_cvt_pk_f16_f32 v20, v12, v13
	v_cvt_pk_f16_f32 v21, v16, v17
	v_cvt_f32_f16_e32 v14, v20
	v_cvt_f32_f16_sdwa v15, v20 dst_sel:DWORD dst_unused:UNUSED_PAD src0_sel:WORD_1
	v_cvt_f32_f16_e32 v18, v21
	v_cvt_f32_f16_sdwa v19, v21 dst_sel:DWORD dst_unused:UNUSED_PAD src0_sel:WORD_1
	v_pk_fma_f32 v[12:13], v[36:37], s[6:7], v[14:15] op_sel_hi:[1,0,1] neg_lo:[0,0,1] neg_hi:[0,0,1]
	v_pk_fma_f32 v[16:17], v[38:39], s[6:7], v[18:19] op_sel_hi:[1,0,1] neg_lo:[0,0,1] neg_hi:[0,0,1]
	v_cvt_pk_f16_f32 v22, v12, v13
	v_cvt_pk_f16_f32 v23, v16, v17
	ds_write_b64 v10, v[20:21] offset:1728
	ds_write_b64 v10, v[22:23] offset:6336
	global_load_dwordx4 v[36:39], v5, s[12:13]
	v_mfma_f32_32x32x16_f16 a[0:15], v[108:111], v[112:115], a[0:15]
	s_waitcnt vmcnt(15)
	v_pk_mul_f32 v[12:13], v[40:41], s[6:7] op_sel_hi:[1,0]
	v_pk_mul_f32 v[16:17], v[42:43], s[6:7] op_sel_hi:[1,0]
	v_cvt_pk_f16_f32 v20, v12, v13
	v_cvt_pk_f16_f32 v21, v16, v17
	v_cvt_f32_f16_e32 v14, v20
	v_cvt_f32_f16_sdwa v15, v20 dst_sel:DWORD dst_unused:UNUSED_PAD src0_sel:WORD_1
	v_cvt_f32_f16_e32 v18, v21
	v_cvt_f32_f16_sdwa v19, v21 dst_sel:DWORD dst_unused:UNUSED_PAD src0_sel:WORD_1
	v_pk_fma_f32 v[12:13], v[40:41], s[6:7], v[14:15] op_sel_hi:[1,0,1] neg_lo:[0,0,1] neg_hi:[0,0,1]
	v_pk_fma_f32 v[16:17], v[42:43], s[6:7], v[18:19] op_sel_hi:[1,0,1] neg_lo:[0,0,1] neg_hi:[0,0,1]
	v_cvt_pk_f16_f32 v22, v12, v13
	v_cvt_pk_f16_f32 v23, v16, v17
	ds_write_b64 v10, v[20:21] offset:2304
	ds_write_b64 v10, v[22:23] offset:6912
	global_load_dwordx4 v[40:43], v6, s[12:13]
	v_mfma_f32_32x32x16_f16 a[0:15], v[104:107], v[116:119], a[0:15]
	s_waitcnt vmcnt(15)
	v_pk_mul_f32 v[12:13], v[44:45], s[6:7] op_sel_hi:[1,0]
	v_pk_mul_f32 v[16:17], v[46:47], s[6:7] op_sel_hi:[1,0]
	v_cvt_pk_f16_f32 v20, v12, v13
	v_cvt_pk_f16_f32 v21, v16, v17
	v_cvt_f32_f16_e32 v14, v20
	v_cvt_f32_f16_sdwa v15, v20 dst_sel:DWORD dst_unused:UNUSED_PAD src0_sel:WORD_1
	v_cvt_f32_f16_e32 v18, v21
	v_cvt_f32_f16_sdwa v19, v21 dst_sel:DWORD dst_unused:UNUSED_PAD src0_sel:WORD_1
	v_pk_fma_f32 v[12:13], v[44:45], s[6:7], v[14:15] op_sel_hi:[1,0,1] neg_lo:[0,0,1] neg_hi:[0,0,1]
	v_pk_fma_f32 v[16:17], v[46:47], s[6:7], v[18:19] op_sel_hi:[1,0,1] neg_lo:[0,0,1] neg_hi:[0,0,1]
	v_cvt_pk_f16_f32 v22, v12, v13
	v_cvt_pk_f16_f32 v23, v16, v17
	ds_write_b64 v10, v[20:21] offset:2880
	ds_write_b64 v10, v[22:23] offset:7488
	global_load_dwordx4 v[44:47], v7, s[12:13]
	v_mfma_f32_32x32x16_f16 a[0:15], v[104:107], v[112:115], a[0:15]
	s_waitcnt vmcnt(15)
	v_pk_mul_f32 v[12:13], v[48:49], s[6:7] op_sel_hi:[1,0]
	v_pk_mul_f32 v[16:17], v[50:51], s[6:7] op_sel_hi:[1,0]
	v_cvt_pk_f16_f32 v20, v12, v13
	v_cvt_pk_f16_f32 v21, v16, v17
	v_cvt_f32_f16_e32 v14, v20
	v_cvt_f32_f16_sdwa v15, v20 dst_sel:DWORD dst_unused:UNUSED_PAD src0_sel:WORD_1
	v_cvt_f32_f16_e32 v18, v21
	v_cvt_f32_f16_sdwa v19, v21 dst_sel:DWORD dst_unused:UNUSED_PAD src0_sel:WORD_1
	v_pk_fma_f32 v[12:13], v[48:49], s[6:7], v[14:15] op_sel_hi:[1,0,1] neg_lo:[0,0,1] neg_hi:[0,0,1]
	v_pk_fma_f32 v[16:17], v[50:51], s[6:7], v[18:19] op_sel_hi:[1,0,1] neg_lo:[0,0,1] neg_hi:[0,0,1]
	v_cvt_pk_f16_f32 v22, v12, v13
	v_cvt_pk_f16_f32 v23, v16, v17
	ds_write_b64 v10, v[20:21] offset:3456
	ds_write_b64 v10, v[22:23] offset:8064
	global_load_dwordx4 v[48:51], v8, s[12:13]
	v_mfma_f32_32x32x16_f16 a[0:15], v[124:127], v[128:131], a[0:15]
	s_waitcnt vmcnt(15)
	v_pk_mul_f32 v[12:13], v[52:53], s[6:7] op_sel_hi:[1,0]
	v_pk_mul_f32 v[16:17], v[54:55], s[6:7] op_sel_hi:[1,0]
	v_cvt_pk_f16_f32 v20, v12, v13
	v_cvt_pk_f16_f32 v21, v16, v17
	v_cvt_f32_f16_e32 v14, v20
	v_cvt_f32_f16_sdwa v15, v20 dst_sel:DWORD dst_unused:UNUSED_PAD src0_sel:WORD_1
	v_cvt_f32_f16_e32 v18, v21
	v_cvt_f32_f16_sdwa v19, v21 dst_sel:DWORD dst_unused:UNUSED_PAD src0_sel:WORD_1
	v_pk_fma_f32 v[12:13], v[52:53], s[6:7], v[14:15] op_sel_hi:[1,0,1] neg_lo:[0,0,1] neg_hi:[0,0,1]
	v_pk_fma_f32 v[16:17], v[54:55], s[6:7], v[18:19] op_sel_hi:[1,0,1] neg_lo:[0,0,1] neg_hi:[0,0,1]
	v_cvt_pk_f16_f32 v22, v12, v13
	v_cvt_pk_f16_f32 v23, v16, v17
	ds_write_b64 v10, v[20:21] offset:4032
	ds_write_b64 v10, v[22:23] offset:8640
	global_load_dwordx4 v[52:55], v9, s[12:13]
	v_mfma_f32_32x32x16_f16 a[0:15], v[120:123], v[132:135], a[0:15]
	s_waitcnt vmcnt(15)
	v_pk_mul_f32 v[12:13], v[56:57], s[6:7] op_sel_hi:[1,0]
	v_pk_mul_f32 v[16:17], v[58:59], s[6:7] op_sel_hi:[1,0]
	v_cvt_pk_f16_f32 v20, v12, v13
	v_cvt_pk_f16_f32 v21, v16, v17
	v_cvt_f32_f16_e32 v14, v20
	v_cvt_f32_f16_sdwa v15, v20 dst_sel:DWORD dst_unused:UNUSED_PAD src0_sel:WORD_1
	v_cvt_f32_f16_e32 v18, v21
	v_cvt_f32_f16_sdwa v19, v21 dst_sel:DWORD dst_unused:UNUSED_PAD src0_sel:WORD_1
	v_pk_fma_f32 v[12:13], v[56:57], s[6:7], v[14:15] op_sel_hi:[1,0,1] neg_lo:[0,0,1] neg_hi:[0,0,1]
	v_pk_fma_f32 v[16:17], v[58:59], s[6:7], v[18:19] op_sel_hi:[1,0,1] neg_lo:[0,0,1] neg_hi:[0,0,1]
	v_cvt_pk_f16_f32 v22, v12, v13
	v_cvt_pk_f16_f32 v23, v16, v17
	ds_write_b64 v10, v[20:21] offset:9216
	ds_write_b64 v10, v[22:23] offset:13824
	global_load_dwordx4 v[56:59], v2, s[14:15]
	v_mfma_f32_32x32x16_f16 a[0:15], v[120:123], v[128:131], a[0:15]
	s_waitcnt vmcnt(15)
	v_pk_mul_f32 v[12:13], v[60:61], s[6:7] op_sel_hi:[1,0]
	v_pk_mul_f32 v[16:17], v[62:63], s[6:7] op_sel_hi:[1,0]
	v_cvt_pk_f16_f32 v20, v12, v13
	v_cvt_pk_f16_f32 v21, v16, v17
	v_cvt_f32_f16_e32 v14, v20
	v_cvt_f32_f16_sdwa v15, v20 dst_sel:DWORD dst_unused:UNUSED_PAD src0_sel:WORD_1
	v_cvt_f32_f16_e32 v18, v21
	v_cvt_f32_f16_sdwa v19, v21 dst_sel:DWORD dst_unused:UNUSED_PAD src0_sel:WORD_1
	v_pk_fma_f32 v[12:13], v[60:61], s[6:7], v[14:15] op_sel_hi:[1,0,1] neg_lo:[0,0,1] neg_hi:[0,0,1]
	v_pk_fma_f32 v[16:17], v[62:63], s[6:7], v[18:19] op_sel_hi:[1,0,1] neg_lo:[0,0,1] neg_hi:[0,0,1]
	v_cvt_pk_f16_f32 v22, v12, v13
	v_cvt_pk_f16_f32 v23, v16, v17
	ds_write_b64 v10, v[20:21] offset:9792
	ds_write_b64 v10, v[22:23] offset:14400
	global_load_dwordx4 v[60:63], v3, s[14:15]
	v_mfma_f32_32x32x16_f16 a[0:15], v[140:143], v[144:147], a[0:15]
	s_waitcnt vmcnt(15)
	v_pk_mul_f32 v[12:13], v[64:65], s[6:7] op_sel_hi:[1,0]
	v_pk_mul_f32 v[16:17], v[66:67], s[6:7] op_sel_hi:[1,0]
	v_cvt_pk_f16_f32 v20, v12, v13
	v_cvt_pk_f16_f32 v21, v16, v17
	v_cvt_f32_f16_e32 v14, v20
	v_cvt_f32_f16_sdwa v15, v20 dst_sel:DWORD dst_unused:UNUSED_PAD src0_sel:WORD_1
	v_cvt_f32_f16_e32 v18, v21
	v_cvt_f32_f16_sdwa v19, v21 dst_sel:DWORD dst_unused:UNUSED_PAD src0_sel:WORD_1
	v_pk_fma_f32 v[12:13], v[64:65], s[6:7], v[14:15] op_sel_hi:[1,0,1] neg_lo:[0,0,1] neg_hi:[0,0,1]
	v_pk_fma_f32 v[16:17], v[66:67], s[6:7], v[18:19] op_sel_hi:[1,0,1] neg_lo:[0,0,1] neg_hi:[0,0,1]
	v_cvt_pk_f16_f32 v22, v12, v13
	v_cvt_pk_f16_f32 v23, v16, v17
	ds_write_b64 v10, v[20:21] offset:10368
	ds_write_b64 v10, v[22:23] offset:14976
	global_load_dwordx4 v[64:67], v4, s[14:15]
	v_mfma_f32_32x32x16_f16 a[0:15], v[136:139], v[148:151], a[0:15]
	s_waitcnt vmcnt(15)
	v_pk_mul_f32 v[12:13], v[68:69], s[6:7] op_sel_hi:[1,0]
	v_pk_mul_f32 v[16:17], v[70:71], s[6:7] op_sel_hi:[1,0]
	v_cvt_pk_f16_f32 v20, v12, v13
	v_cvt_pk_f16_f32 v21, v16, v17
	v_cvt_f32_f16_e32 v14, v20
	v_cvt_f32_f16_sdwa v15, v20 dst_sel:DWORD dst_unused:UNUSED_PAD src0_sel:WORD_1
	v_cvt_f32_f16_e32 v18, v21
	v_cvt_f32_f16_sdwa v19, v21 dst_sel:DWORD dst_unused:UNUSED_PAD src0_sel:WORD_1
	v_pk_fma_f32 v[12:13], v[68:69], s[6:7], v[14:15] op_sel_hi:[1,0,1] neg_lo:[0,0,1] neg_hi:[0,0,1]
	v_pk_fma_f32 v[16:17], v[70:71], s[6:7], v[18:19] op_sel_hi:[1,0,1] neg_lo:[0,0,1] neg_hi:[0,0,1]
	v_cvt_pk_f16_f32 v22, v12, v13
	v_cvt_pk_f16_f32 v23, v16, v17
	ds_write_b64 v10, v[20:21] offset:10944
	ds_write_b64 v10, v[22:23] offset:15552
	global_load_dwordx4 v[68:71], v5, s[14:15]
	v_mfma_f32_32x32x16_f16 a[0:15], v[136:139], v[144:147], a[0:15]
	s_waitcnt vmcnt(15)
	v_pk_mul_f32 v[12:13], v[72:73], s[6:7] op_sel_hi:[1,0]
	v_pk_mul_f32 v[16:17], v[74:75], s[6:7] op_sel_hi:[1,0]
	v_cvt_pk_f16_f32 v20, v12, v13
	v_cvt_pk_f16_f32 v21, v16, v17
	v_cvt_f32_f16_e32 v14, v20
	v_cvt_f32_f16_sdwa v15, v20 dst_sel:DWORD dst_unused:UNUSED_PAD src0_sel:WORD_1
	v_cvt_f32_f16_e32 v18, v21
	v_cvt_f32_f16_sdwa v19, v21 dst_sel:DWORD dst_unused:UNUSED_PAD src0_sel:WORD_1
	v_pk_fma_f32 v[12:13], v[72:73], s[6:7], v[14:15] op_sel_hi:[1,0,1] neg_lo:[0,0,1] neg_hi:[0,0,1]
	v_pk_fma_f32 v[16:17], v[74:75], s[6:7], v[18:19] op_sel_hi:[1,0,1] neg_lo:[0,0,1] neg_hi:[0,0,1]
	v_cvt_pk_f16_f32 v22, v12, v13
	v_cvt_pk_f16_f32 v23, v16, v17
	ds_write_b64 v10, v[20:21] offset:11520
	ds_write_b64 v10, v[22:23] offset:16128
	global_load_dwordx4 v[72:75], v6, s[14:15]
	s_waitcnt vmcnt(15)
	v_pk_mul_f32 v[12:13], v[76:77], s[6:7] op_sel_hi:[1,0]
	v_pk_mul_f32 v[16:17], v[78:79], s[6:7] op_sel_hi:[1,0]
	v_cvt_pk_f16_f32 v20, v12, v13
	v_cvt_pk_f16_f32 v21, v16, v17
	v_cvt_f32_f16_e32 v14, v20
	v_cvt_f32_f16_sdwa v15, v20 dst_sel:DWORD dst_unused:UNUSED_PAD src0_sel:WORD_1
	v_cvt_f32_f16_e32 v18, v21
	v_cvt_f32_f16_sdwa v19, v21 dst_sel:DWORD dst_unused:UNUSED_PAD src0_sel:WORD_1
	v_pk_fma_f32 v[12:13], v[76:77], s[6:7], v[14:15] op_sel_hi:[1,0,1] neg_lo:[0,0,1] neg_hi:[0,0,1]
	v_pk_fma_f32 v[16:17], v[78:79], s[6:7], v[18:19] op_sel_hi:[1,0,1] neg_lo:[0,0,1] neg_hi:[0,0,1]
	v_cvt_pk_f16_f32 v22, v12, v13
	v_cvt_pk_f16_f32 v23, v16, v17
	ds_write_b64 v10, v[20:21] offset:12096
	ds_write_b64 v10, v[22:23] offset:16704
	global_load_dwordx4 v[76:79], v7, s[14:15]
	s_waitcnt vmcnt(15)
	v_pk_mul_f32 v[12:13], v[80:81], s[6:7] op_sel_hi:[1,0]
	v_pk_mul_f32 v[16:17], v[82:83], s[6:7] op_sel_hi:[1,0]
	v_cvt_pk_f16_f32 v20, v12, v13
	v_cvt_pk_f16_f32 v21, v16, v17
	v_cvt_f32_f16_e32 v14, v20
	v_cvt_f32_f16_sdwa v15, v20 dst_sel:DWORD dst_unused:UNUSED_PAD src0_sel:WORD_1
	v_cvt_f32_f16_e32 v18, v21
	v_cvt_f32_f16_sdwa v19, v21 dst_sel:DWORD dst_unused:UNUSED_PAD src0_sel:WORD_1
	v_pk_fma_f32 v[12:13], v[80:81], s[6:7], v[14:15] op_sel_hi:[1,0,1] neg_lo:[0,0,1] neg_hi:[0,0,1]
	v_pk_fma_f32 v[16:17], v[82:83], s[6:7], v[18:19] op_sel_hi:[1,0,1] neg_lo:[0,0,1] neg_hi:[0,0,1]
	v_cvt_pk_f16_f32 v22, v12, v13
	v_cvt_pk_f16_f32 v23, v16, v17
	ds_write_b64 v10, v[20:21] offset:12672
	ds_write_b64 v10, v[22:23] offset:17280
	global_load_dwordx4 v[80:83], v8, s[14:15]
	s_waitcnt vmcnt(15)
	v_pk_mul_f32 v[12:13], v[84:85], s[6:7] op_sel_hi:[1,0]
	v_pk_mul_f32 v[16:17], v[86:87], s[6:7] op_sel_hi:[1,0]
	v_cvt_pk_f16_f32 v20, v12, v13
	v_cvt_pk_f16_f32 v21, v16, v17
	v_cvt_f32_f16_e32 v14, v20
	v_cvt_f32_f16_sdwa v15, v20 dst_sel:DWORD dst_unused:UNUSED_PAD src0_sel:WORD_1
	v_cvt_f32_f16_e32 v18, v21
	v_cvt_f32_f16_sdwa v19, v21 dst_sel:DWORD dst_unused:UNUSED_PAD src0_sel:WORD_1
	v_pk_fma_f32 v[12:13], v[84:85], s[6:7], v[14:15] op_sel_hi:[1,0,1] neg_lo:[0,0,1] neg_hi:[0,0,1]
	v_pk_fma_f32 v[16:17], v[86:87], s[6:7], v[18:19] op_sel_hi:[1,0,1] neg_lo:[0,0,1] neg_hi:[0,0,1]
	v_cvt_pk_f16_f32 v22, v12, v13
	v_cvt_pk_f16_f32 v23, v16, v17
	ds_write_b64 v10, v[20:21] offset:13248
	ds_write_b64 v10, v[22:23] offset:17856
	global_load_dwordx4 v[84:87], v9, s[14:15]
	ds_read_b128 v[88:91], v11 offset:0
	ds_read_b128 v[92:95], v11 offset:4608
	ds_read_b128 v[96:99], v11 offset:9216
	ds_read_b128 v[100:103], v11 offset:13824
	ds_read_b128 v[104:107], v11 offset:32
	ds_read_b128 v[108:111], v11 offset:4640
	ds_read_b128 v[112:115], v11 offset:9248
	ds_read_b128 v[116:119], v11 offset:13856
	ds_read_b128 v[120:123], v11 offset:64
	ds_read_b128 v[124:127], v11 offset:4672
	ds_read_b128 v[128:131], v11 offset:9280
	ds_read_b128 v[132:135], v11 offset:13888
	ds_read_b128 v[136:139], v11 offset:96
	ds_read_b128 v[140:143], v11 offset:4704
	ds_read_b128 v[144:147], v11 offset:9312
	ds_read_b128 v[148:151], v11 offset:13920
	s_sub_i32 s10, s10, 1
	s_cmp_lg_u32 s10, 0
	s_cbranch_scc1 .Lpk_loop
	s_waitcnt vmcnt(15)
	v_pk_mul_f32 v[12:13], v[24:25], s[6:7] op_sel_hi:[1,0]
	v_pk_mul_f32 v[16:17], v[26:27], s[6:7] op_sel_hi:[1,0]
	v_cvt_pk_f16_f32 v20, v12, v13
	v_cvt_pk_f16_f32 v21, v16, v17
	v_cvt_f32_f16_e32 v14, v20
	v_cvt_f32_f16_sdwa v15, v20 dst_sel:DWORD dst_unused:UNUSED_PAD src0_sel:WORD_1
	v_cvt_f32_f16_e32 v18, v21
	v_cvt_f32_f16_sdwa v19, v21 dst_sel:DWORD dst_unused:UNUSED_PAD src0_sel:WORD_1
	v_pk_fma_f32 v[12:13], v[24:25], s[6:7], v[14:15] op_sel_hi:[1,0,1] neg_lo:[0,0,1] neg_hi:[0,0,1]
	v_pk_fma_f32 v[16:17], v[26:27], s[6:7], v[18:19] op_sel_hi:[1,0,1] neg_lo:[0,0,1] neg_hi:[0,0,1]
	v_cvt_pk_f16_f32 v22, v12, v13
	v_cvt_pk_f16_f32 v23, v16, v17
	ds_write_b64 v10, v[20:21] offset:0
	ds_write_b64 v10, v[22:23] offset:4608
	s_waitcnt lgkmcnt(2)
	v_mfma_f32_32x32x16_f16 a[0:15], v[92:95], v[96:99], a[0:15]
	s_waitcnt vmcnt(14)
	v_pk_mul_f32 v[12:13], v[28:29], s[6:7] op_sel_hi:[1,0]
	v_pk_mul_f32 v[16:17], v[30:31], s[6:7] op_sel_hi:[1,0]
	v_cvt_pk_f16_f32 v20, v12, v13
	v_cvt_pk_f16_f32 v21, v16, v17
	v_cvt_f32_f16_e32 v14, v20
	v_cvt_f32_f16_sdwa v15, v20 dst_sel:DWORD dst_unused:UNUSED_PAD src0_sel:WORD_1
	v_cvt_f32_f16_e32 v18, v21
	v_cvt_f32_f16_sdwa v19, v21 dst_sel:DWORD dst_unused:UNUSED_PAD src0_sel:WORD_1
	v_pk_fma_f32 v[12:13], v[28:29], s[6:7], v[14:15] op_sel_hi:[1,0,1] neg_lo:[0,0,1] neg_hi:[0,0,1]
	v_pk_fma_f32 v[16:17], v[30:31], s[6:7], v[18:19] op_sel_hi:[1,0,1] neg_lo:[0,0,1] neg_hi:[0,0,1]
	v_cvt_pk_f16_f32 v22, v12, v13
	v_cvt_pk_f16_f32 v23, v16, v17
	ds_write_b64 v10, v[20:21] offset:576
	ds_write_b64 v10, v[22:23] offset:5184
	v_mfma_f32_32x32x16_f16 a[0:15], v[88:91], v[100:103], a[0:15]
	s_waitcnt vmcnt(13)
	v_pk_mul_f32 v[12:13], v[32:33], s[6:7] op_sel_hi:[1,0]
	v_pk_mul_f32 v[16:17], v[34:35], s[6:7] op_sel_hi:[1,0]
	v_cvt_pk_f16_f32 v20, v12, v13
	v_cvt_pk_f16_f32 v21, v16, v17
	v_cvt_f32_f16_e32 v14, v20
	v_cvt_f32_f16_sdwa v15, v20 dst_sel:DWORD dst_unused:UNUSED_PAD src0_sel:WORD_1
	v_cvt_f32_f16_e32 v18, v21
	v_cvt_f32_f16_sdwa v19, v21 dst_sel:DWORD dst_unused:UNUSED_PAD src0_sel:WORD_1
	v_pk_fma_f32 v[12:13], v[32:33], s[6:7], v[14:15] op_sel_hi:[1,0,1] neg_lo:[0,0,1] neg_hi:[0,0,1]
	v_pk_fma_f32 v[16:17], v[34:35], s[6:7], v[18:19] op_sel_hi:[1,0,1] neg_lo:[0,0,1] neg_hi:[0,0,1]
	v_cvt_pk_f16_f32 v22, v12, v13
	v_cvt_pk_f16_f32 v23, v16, v17
	ds_write_b64 v10, v[20:21] offset:1152
	ds_write_b64 v10, v[22:23] offset:5760
	v_mfma_f32_32x32x16_f16 a[0:15], v[88:91], v[96:99], a[0:15]
	s_waitcnt vmcnt(12)
	v_pk_mul_f32 v[12:13], v[36:37], s[6:7] op_sel_hi:[1,0]
	v_pk_mul_f32 v[16:17], v[38:39], s[6:7] op_sel_hi:[1,0]
	v_cvt_pk_f16_f32 v20, v12, v13
	v_cvt_pk_f16_f32 v21, v16, v17
	v_cvt_f32_f16_e32 v14, v20
	v_cvt_f32_f16_sdwa v15, v20 dst_sel:DWORD dst_unused:UNUSED_PAD src0_sel:WORD_1
	v_cvt_f32_f16_e32 v18, v21
	v_cvt_f32_f16_sdwa v19, v21 dst_sel:DWORD dst_unused:UNUSED_PAD src0_sel:WORD_1
	v_pk_fma_f32 v[12:13], v[36:37], s[6:7], v[14:15] op_sel_hi:[1,0,1] neg_lo:[0,0,1] neg_hi:[0,0,1]
	v_pk_fma_f32 v[16:17], v[38:39], s[6:7], v[18:19] op_sel_hi:[1,0,1] neg_lo:[0,0,1] neg_hi:[0,0,1]
	v_cvt_pk_f16_f32 v22, v12, v13
	v_cvt_pk_f16_f32 v23, v16, v17
	ds_write_b64 v10, v[20:21] offset:1728
	ds_write_b64 v10, v[22:23] offset:6336
	v_mfma_f32_32x32x16_f16 a[0:15], v[108:111], v[112:115], a[0:15]
	s_waitcnt vmcnt(11)
	v_pk_mul_f32 v[12:13], v[40:41], s[6:7] op_sel_hi:[1,0]
	v_pk_mul_f32 v[16:17], v[42:43], s[6:7] op_sel_hi:[1,0]
	v_cvt_pk_f16_f32 v20, v12, v13
	v_cvt_pk_f16_f32 v21, v16, v17
	v_cvt_f32_f16_e32 v14, v20
	v_cvt_f32_f16_sdwa v15, v20 dst_sel:DWORD dst_unused:UNUSED_PAD src0_sel:WORD_1
	v_cvt_f32_f16_e32 v18, v21
	v_cvt_f32_f16_sdwa v19, v21 dst_sel:DWORD dst_unused:UNUSED_PAD src0_sel:WORD_1
	v_pk_fma_f32 v[12:13], v[40:41], s[6:7], v[14:15] op_sel_hi:[1,0,1] neg_lo:[0,0,1] neg_hi:[0,0,1]
	v_pk_fma_f32 v[16:17], v[42:43], s[6:7], v[18:19] op_sel_hi:[1,0,1] neg_lo:[0,0,1] neg_hi:[0,0,1]
	v_cvt_pk_f16_f32 v22, v12, v13
	v_cvt_pk_f16_f32 v23, v16, v17
	ds_write_b64 v10, v[20:21] offset:2304
	ds_write_b64 v10, v[22:23] offset:6912
	v_mfma_f32_32x32x16_f16 a[0:15], v[104:107], v[116:119], a[0:15]
	s_waitcnt vmcnt(10)
	v_pk_mul_f32 v[12:13], v[44:45], s[6:7] op_sel_hi:[1,0]
	v_pk_mul_f32 v[16:17], v[46:47], s[6:7] op_sel_hi:[1,0]
	v_cvt_pk_f16_f32 v20, v12, v13
	v_cvt_pk_f16_f32 v21, v16, v17
	v_cvt_f32_f16_e32 v14, v20
	v_cvt_f32_f16_sdwa v15, v20 dst_sel:DWORD dst_unused:UNUSED_PAD src0_sel:WORD_1
	v_cvt_f32_f16_e32 v18, v21
	v_cvt_f32_f16_sdwa v19, v21 dst_sel:DWORD dst_unused:UNUSED_PAD src0_sel:WORD_1
	v_pk_fma_f32 v[12:13], v[44:45], s[6:7], v[14:15] op_sel_hi:[1,0,1] neg_lo:[0,0,1] neg_hi:[0,0,1]
	v_pk_fma_f32 v[16:17], v[46:47], s[6:7], v[18:19] op_sel_hi:[1,0,1] neg_lo:[0,0,1] neg_hi:[0,0,1]
	v_cvt_pk_f16_f32 v22, v12, v13
	v_cvt_pk_f16_f32 v23, v16, v17
	ds_write_b64 v10, v[20:21] offset:2880
	ds_write_b64 v10, v[22:23] offset:7488
	v_mfma_f32_32x32x16_f16 a[0:15], v[104:107], v[112:115], a[0:15]
	s_waitcnt vmcnt(9)
	v_pk_mul_f32 v[12:13], v[48:49], s[6:7] op_sel_hi:[1,0]
	v_pk_mul_f32 v[16:17], v[50:51], s[6:7] op_sel_hi:[1,0]
	v_cvt_pk_f16_f32 v20, v12, v13
	v_cvt_pk_f16_f32 v21, v16, v17
	v_cvt_f32_f16_e32 v14, v20
	v_cvt_f32_f16_sdwa v15, v20 dst_sel:DWORD dst_unused:UNUSED_PAD src0_sel:WORD_1
	v_cvt_f32_f16_e32 v18, v21
	v_cvt_f32_f16_sdwa v19, v21 dst_sel:DWORD dst_unused:UNUSED_PAD src0_sel:WORD_1
	v_pk_fma_f32 v[12:13], v[48:49], s[6:7], v[14:15] op_sel_hi:[1,0,1] neg_lo:[0,0,1] neg_hi:[0,0,1]
	v_pk_fma_f32 v[16:17], v[50:51], s[6:7], v[18:19] op_sel_hi:[1,0,1] neg_lo:[0,0,1] neg_hi:[0,0,1]
	v_cvt_pk_f16_f32 v22, v12, v13
	v_cvt_pk_f16_f32 v23, v16, v17
	ds_write_b64 v10, v[20:21] offset:3456
	ds_write_b64 v10, v[22:23] offset:8064
	v_mfma_f32_32x32x16_f16 a[0:15], v[124:127], v[128:131], a[0:15]
	s_waitcnt vmcnt(8)
	v_pk_mul_f32 v[12:13], v[52:53], s[6:7] op_sel_hi:[1,0]
	v_pk_mul_f32 v[16:17], v[54:55], s[6:7] op_sel_hi:[1,0]
	v_cvt_pk_f16_f32 v20, v12, v13
	v_cvt_pk_f16_f32 v21, v16, v17
	v_cvt_f32_f16_e32 v14, v20
	v_cvt_f32_f16_sdwa v15, v20 dst_sel:DWORD dst_unused:UNUSED_PAD src0_sel:WORD_1
	v_cvt_f32_f16_e32 v18, v21
	v_cvt_f32_f16_sdwa v19, v21 dst_sel:DWORD dst_unused:UNUSED_PAD src0_sel:WORD_1
	v_pk_fma_f32 v[12:13], v[52:53], s[6:7], v[14:15] op_sel_hi:[1,0,1] neg_lo:[0,0,1] neg_hi:[0,0,1]
	v_pk_fma_f32 v[16:17], v[54:55], s[6:7], v[18:19] op_sel_hi:[1,0,1] neg_lo:[0,0,1] neg_hi:[0,0,1]
	v_cvt_pk_f16_f32 v22, v12, v13
	v_cvt_pk_f16_f32 v23, v16, v17
	ds_write_b64 v10, v[20:21] offset:4032
	ds_write_b64 v10, v[22:23] offset:8640
	v_mfma_f32_32x32x16_f16 a[0:15], v[120:123], v[132:135], a[0:15]
	s_waitcnt vmcnt(7)
	v_pk_mul_f32 v[12:13], v[56:57], s[6:7] op_sel_hi:[1,0]
	v_pk_mul_f32 v[16:17], v[58:59], s[6:7] op_sel_hi:[1,0]
	v_cvt_pk_f16_f32 v20, v12, v13
	v_cvt_pk_f16_f32 v21, v16, v17
	v_cvt_f32_f16_e32 v14, v20
	v_cvt_f32_f16_sdwa v15, v20 dst_sel:DWORD dst_unused:UNUSED_PAD src0_sel:WORD_1
	v_cvt_f32_f16_e32 v18, v21
	v_cvt_f32_f16_sdwa v19, v21 dst_sel:DWORD dst_unused:UNUSED_PAD src0_sel:WORD_1
	v_pk_fma_f32 v[12:13], v[56:57], s[6:7], v[14:15] op_sel_hi:[1,0,1] neg_lo:[0,0,1] neg_hi:[0,0,1]
	v_pk_fma_f32 v[16:17], v[58:59], s[6:7], v[18:19] op_sel_hi:[1,0,1] neg_lo:[0,0,1] neg_hi:[0,0,1]
	v_cvt_pk_f16_f32 v22, v12, v13
	v_cvt_pk_f16_f32 v23, v16, v17
	ds_write_b64 v10, v[20:21] offset:9216
	ds_write_b64 v10, v[22:23] offset:13824
	v_mfma_f32_32x32x16_f16 a[0:15], v[120:123], v[128:131], a[0:15]
	s_waitcnt vmcnt(6)
	v_pk_mul_f32 v[12:13], v[60:61], s[6:7] op_sel_hi:[1,0]
	v_pk_mul_f32 v[16:17], v[62:63], s[6:7] op_sel_hi:[1,0]
	v_cvt_pk_f16_f32 v20, v12, v13
	v_cvt_pk_f16_f32 v21, v16, v17
	v_cvt_f32_f16_e32 v14, v20
	v_cvt_f32_f16_sdwa v15, v20 dst_sel:DWORD dst_unused:UNUSED_PAD src0_sel:WORD_1
	v_cvt_f32_f16_e32 v18, v21
	v_cvt_f32_f16_sdwa v19, v21 dst_sel:DWORD dst_unused:UNUSED_PAD src0_sel:WORD_1
	v_pk_fma_f32 v[12:13], v[60:61], s[6:7], v[14:15] op_sel_hi:[1,0,1] neg_lo:[0,0,1] neg_hi:[0,0,1]
	v_pk_fma_f32 v[16:17], v[62:63], s[6:7], v[18:19] op_sel_hi:[1,0,1] neg_lo:[0,0,1] neg_hi:[0,0,1]
	v_cvt_pk_f16_f32 v22, v12, v13
	v_cvt_pk_f16_f32 v23, v16, v17
	ds_write_b64 v10, v[20:21] offset:9792
	ds_write_b64 v10, v[22:23] offset:14400
	v_mfma_f32_32x32x16_f16 a[0:15], v[140:143], v[144:147], a[0:15]
	s_waitcnt vmcnt(5)
	v_pk_mul_f32 v[12:13], v[64:65], s[6:7] op_sel_hi:[1,0]
	v_pk_mul_f32 v[16:17], v[66:67], s[6:7] op_sel_hi:[1,0]
	v_cvt_pk_f16_f32 v20, v12, v13
	v_cvt_pk_f16_f32 v21, v16, v17
	v_cvt_f32_f16_e32 v14, v20
	v_cvt_f32_f16_sdwa v15, v20 dst_sel:DWORD dst_unused:UNUSED_PAD src0_sel:WORD_1
	v_cvt_f32_f16_e32 v18, v21
	v_cvt_f32_f16_sdwa v19, v21 dst_sel:DWORD dst_unused:UNUSED_PAD src0_sel:WORD_1
	v_pk_fma_f32 v[12:13], v[64:65], s[6:7], v[14:15] op_sel_hi:[1,0,1] neg_lo:[0,0,1] neg_hi:[0,0,1]
	v_pk_fma_f32 v[16:17], v[66:67], s[6:7], v[18:19] op_sel_hi:[1,0,1] neg_lo:[0,0,1] neg_hi:[0,0,1]
	v_cvt_pk_f16_f32 v22, v12, v13
	v_cvt_pk_f16_f32 v23, v16, v17
	ds_write_b64 v10, v[20:21] offset:10368
	ds_write_b64 v10, v[22:23] offset:14976
	v_mfma_f32_32x32x16_f16 a[0:15], v[136:139], v[148:151], a[0:15]
	s_waitcnt vmcnt(4)
	v_pk_mul_f32 v[12:13], v[68:69], s[6:7] op_sel_hi:[1,0]
	v_pk_mul_f32 v[16:17], v[70:71], s[6:7] op_sel_hi:[1,0]
	v_cvt_pk_f16_f32 v20, v12, v13
	v_cvt_pk_f16_f32 v21, v16, v17
	v_cvt_f32_f16_e32 v14, v20
	v_cvt_f32_f16_sdwa v15, v20 dst_sel:DWORD dst_unused:UNUSED_PAD src0_sel:WORD_1
	v_cvt_f32_f16_e32 v18, v21
	v_cvt_f32_f16_sdwa v19, v21 dst_sel:DWORD dst_unused:UNUSED_PAD src0_sel:WORD_1
	v_pk_fma_f32 v[12:13], v[68:69], s[6:7], v[14:15] op_sel_hi:[1,0,1] neg_lo:[0,0,1] neg_hi:[0,0,1]
	v_pk_fma_f32 v[16:17], v[70:71], s[6:7], v[18:19] op_sel_hi:[1,0,1] neg_lo:[0,0,1] neg_hi:[0,0,1]
	v_cvt_pk_f16_f32 v22, v12, v13
	v_cvt_pk_f16_f32 v23, v16, v17
	ds_write_b64 v10, v[20:21] offset:10944
	ds_write_b64 v10, v[22:23] offset:15552
	v_mfma_f32_32x32x16_f16 a[0:15], v[136:139], v[144:147], a[0:15]
	s_waitcnt vmcnt(3)
	v_pk_mul_f32 v[12:13], v[72:73], s[6:7] op_sel_hi:[1,0]
	v_pk_mul_f32 v[16:17], v[74:75], s[6:7] op_sel_hi:[1,0]
	v_cvt_pk_f16_f32 v20, v12, v13
	v_cvt_pk_f16_f32 v21, v16, v17
	v_cvt_f32_f16_e32 v14, v20
	v_cvt_f32_f16_sdwa v15, v20 dst_sel:DWORD dst_unused:UNUSED_PAD src0_sel:WORD_1
	v_cvt_f32_f16_e32 v18, v21
	v_cvt_f32_f16_sdwa v19, v21 dst_sel:DWORD dst_unused:UNUSED_PAD src0_sel:WORD_1
	v_pk_fma_f32 v[12:13], v[72:73], s[6:7], v[14:15] op_sel_hi:[1,0,1] neg_lo:[0,0,1] neg_hi:[0,0,1]
	v_pk_fma_f32 v[16:17], v[74:75], s[6:7], v[18:19] op_sel_hi:[1,0,1] neg_lo:[0,0,1] neg_hi:[0,0,1]
	v_cvt_pk_f16_f32 v22, v12, v13
	v_cvt_pk_f16_f32 v23, v16, v17
	ds_write_b64 v10, v[20:21] offset:11520
	ds_write_b64 v10, v[22:23] offset:16128
	s_waitcnt vmcnt(2)
	v_pk_mul_f32 v[12:13], v[76:77], s[6:7] op_sel_hi:[1,0]
	v_pk_mul_f32 v[16:17], v[78:79], s[6:7] op_sel_hi:[1,0]
	v_cvt_pk_f16_f32 v20, v12, v13
	v_cvt_pk_f16_f32 v21, v16, v17
	v_cvt_f32_f16_e32 v14, v20
	v_cvt_f32_f16_sdwa v15, v20 dst_sel:DWORD dst_unused:UNUSED_PAD src0_sel:WORD_1
	v_cvt_f32_f16_e32 v18, v21
	v_cvt_f32_f16_sdwa v19, v21 dst_sel:DWORD dst_unused:UNUSED_PAD src0_sel:WORD_1
	v_pk_fma_f32 v[12:13], v[76:77], s[6:7], v[14:15] op_sel_hi:[1,0,1] neg_lo:[0,0,1] neg_hi:[0,0,1]
	v_pk_fma_f32 v[16:17], v[78:79], s[6:7], v[18:19] op_sel_hi:[1,0,1] neg_lo:[0,0,1] neg_hi:[0,0,1]
	v_cvt_pk_f16_f32 v22, v12, v13
	v_cvt_pk_f16_f32 v23, v16, v17
	ds_write_b64 v10, v[20:21] offset:12096
	ds_write_b64 v10, v[22:23] offset:16704
	s_waitcnt vmcnt(1)
	v_pk_mul_f32 v[12:13], v[80:81], s[6:7] op_sel_hi:[1,0]
	v_pk_mul_f32 v[16:17], v[82:83], s[6:7] op_sel_hi:[1,0]
	v_cvt_pk_f16_f32 v20, v12, v13
	v_cvt_pk_f16_f32 v21, v16, v17
	v_cvt_f32_f16_e32 v14, v20
	v_cvt_f32_f16_sdwa v15, v20 dst_sel:DWORD dst_unused:UNUSED_PAD src0_sel:WORD_1
	v_cvt_f32_f16_e32 v18, v21
	v_cvt_f32_f16_sdwa v19, v21 dst_sel:DWORD dst_unused:UNUSED_PAD src0_sel:WORD_1
	v_pk_fma_f32 v[12:13], v[80:81], s[6:7], v[14:15] op_sel_hi:[1,0,1] neg_lo:[0,0,1] neg_hi:[0,0,1]
	v_pk_fma_f32 v[16:17], v[82:83], s[6:7], v[18:19] op_sel_hi:[1,0,1] neg_lo:[0,0,1] neg_hi:[0,0,1]
	v_cvt_pk_f16_f32 v22, v12, v13
	v_cvt_pk_f16_f32 v23, v16, v17
	ds_write_b64 v10, v[20:21] offset:12672
	ds_write_b64 v10, v[22:23] offset:17280
	s_waitcnt vmcnt(0)
	v_pk_mul_f32 v[12:13], v[84:85], s[6:7] op_sel_hi:[1,0]
	v_pk_mul_f32 v[16:17], v[86:87], s[6:7] op_sel_hi:[1,0]
	v_cvt_pk_f16_f32 v20, v12, v13
	v_cvt_pk_f16_f32 v21, v16, v17
	v_cvt_f32_f16_e32 v14, v20
	v_cvt_f32_f16_sdwa v15, v20 dst_sel:DWORD dst_unused:UNUSED_PAD src0_sel:WORD_1
	v_cvt_f32_f16_e32 v18, v21
	v_cvt_f32_f16_sdwa v19, v21 dst_sel:DWORD dst_unused:UNUSED_PAD src0_sel:WORD_1
	v_pk_fma_f32 v[12:13], v[84:85], s[6:7], v[14:15] op_sel_hi:[1,0,1] neg_lo:[0,0,1] neg_hi:[0,0,1]
	v_pk_fma_f32 v[16:17], v[86:87], s[6:7], v[18:19] op_sel_hi:[1,0,1] neg_lo:[0,0,1] neg_hi:[0,0,1]
	v_cvt_pk_f16_f32 v22, v12, v13
	v_cvt_pk_f16_f32 v23, v16, v17
	ds_write_b64 v10, v[20:21] offset:13248
	ds_write_b64 v10, v[22:23] offset:17856
	ds_read_b128 v[88:91], v11 offset:0
	ds_read_b128 v[92:95], v11 offset:4608
	ds_read_b128 v[96:99], v11 offset:9216
	ds_read_b128 v[100:103], v11 offset:13824
	ds_read_b128 v[104:107], v11 offset:32
	ds_read_b128 v[108:111], v11 offset:4640
	ds_read_b128 v[112:115], v11 offset:9248
	ds_read_b128 v[116:119], v11 offset:13856
	ds_read_b128 v[120:123], v11 offset:64
	ds_read_b128 v[124:127], v11 offset:4672
	ds_read_b128 v[128:131], v11 offset:9280
	ds_read_b128 v[132:135], v11 offset:13888
	ds_read_b128 v[136:139], v11 offset:96
	ds_read_b128 v[140:143], v11 offset:4704
	ds_read_b128 v[144:147], v11 offset:9312
	ds_read_b128 v[148:151], v11 offset:13920
	s_waitcnt lgkmcnt(0)
	v_mfma_f32_32x32x16_f16 a[0:15], v[92:95], v[96:99], a[0:15]
	v_mfma_f32_32x32x16_f16 a[0:15], v[88:91], v[100:103], a[0:15]
	v_mfma_f32_32x32x16_f16 a[0:15], v[88:91], v[96:99], a[0:15]
	v_mfma_f32_32x32x16_f16 a[0:15], v[108:111], v[112:115], a[0:15]
	v_mfma_f32_32x32x16_f16 a[0:15], v[104:107], v[116:119], a[0:15]
	v_mfma_f32_32x32x16_f16 a[0:15], v[104:107], v[112:115], a[0:15]
	v_mfma_f32_32x32x16_f16 a[0:15], v[124:127], v[128:131], a[0:15]
	v_mfma_f32_32x32x16_f16 a[0:15], v[120:123], v[132:135], a[0:15]
	v_mfma_f32_32x32x16_f16 a[0:15], v[120:123], v[128:131], a[0:15]
	v_mfma_f32_32x32x16_f16 a[0:15], v[140:143], v[144:147], a[0:15]
	v_mfma_f32_32x32x16_f16 a[0:15], v[136:139], v[148:151], a[0:15]
	v_mfma_f32_32x32x16_f16 a[0:15], v[136:139], v[144:147], a[0:15]
	s_nop 1
	v_lshrrev_b32_e32 v18, 3, v0
	v_and_b32_e32 v18, 4, v18
	v_add_u32_e32 v18, s3, v18
	v_lshlrev_b32_e32 v20, 1, v1
	v_mov_b32_e32 v21, 0
	v_ashrrev_i32_e32 v19, 31, v18
	s_nop 4
	v_accvgpr_read_b32 v17, a0
	v_lshl_add_u64 v[20:21], s[4:5], 0, v[20:21]
	s_mov_b32 s3, 0x3d800000
	v_lshlrev_b64 v[22:23], 11, v[18:19]
	v_fma_mixlo_f16 v1, v17, s3, 0
	v_lshl_add_u64 v[22:23], v[20:21], 0, v[22:23]
	global_store_short v[22:23], v1, off
	v_or_b32_e32 v22, 1, v18
	v_accvgpr_read_b32 v16, a1
	v_ashrrev_i32_e32 v23, 31, v22
	v_fma_mixlo_f16 v1, v16, s3, 0
	v_lshlrev_b64 v[16:17], 11, v[22:23]
	v_lshl_add_u64 v[16:17], v[20:21], 0, v[16:17]
	global_store_short v[16:17], v1, off
	v_or_b32_e32 v16, 2, v18
	v_ashrrev_i32_e32 v17, 31, v16
	v_accvgpr_read_b32 v15, a2
	v_lshlrev_b64 v[16:17], 11, v[16:17]
	v_fma_mixlo_f16 v1, v15, s3, 0
	v_lshl_add_u64 v[16:17], v[20:21], 0, v[16:17]
	global_store_short v[16:17], v1, off
	v_or_b32_e32 v16, 3, v18
	v_accvgpr_read_b32 v14, a3
	v_ashrrev_i32_e32 v17, 31, v16
	v_fma_mixlo_f16 v1, v14, s3, 0
	v_lshlrev_b64 v[14:15], 11, v[16:17]
	v_lshl_add_u64 v[14:15], v[20:21], 0, v[14:15]
	global_store_short v[14:15], v1, off
	v_add_u32_e32 v14, 8, v18
	v_ashrrev_i32_e32 v15, 31, v14
	v_accvgpr_read_b32 v13, a4
	v_lshlrev_b64 v[14:15], 11, v[14:15]
	v_fma_mixlo_f16 v1, v13, s3, 0
	v_lshl_add_u64 v[14:15], v[20:21], 0, v[14:15]
	global_store_short v[14:15], v1, off
	v_add_u32_e32 v14, 9, v18
	v_accvgpr_read_b32 v12, a5
	v_ashrrev_i32_e32 v15, 31, v14
	v_fma_mixlo_f16 v1, v12, s3, 0
	v_lshlrev_b64 v[12:13], 11, v[14:15]
	v_lshl_add_u64 v[12:13], v[20:21], 0, v[12:13]
	global_store_short v[12:13], v1, off
	v_add_u32_e32 v12, 10, v18
	v_ashrrev_i32_e32 v13, 31, v12
	v_accvgpr_read_b32 v11, a6
	v_lshlrev_b64 v[12:13], 11, v[12:13]
	v_fma_mixlo_f16 v1, v11, s3, 0
	v_lshl_add_u64 v[12:13], v[20:21], 0, v[12:13]
	global_store_short v[12:13], v1, off
	v_add_u32_e32 v12, 11, v18
	v_accvgpr_read_b32 v10, a7
	v_ashrrev_i32_e32 v13, 31, v12
	v_fma_mixlo_f16 v1, v10, s3, 0
	v_lshlrev_b64 v[10:11], 11, v[12:13]
	v_lshl_add_u64 v[10:11], v[20:21], 0, v[10:11]
	global_store_short v[10:11], v1, off
	v_add_u32_e32 v10, 16, v18
	v_ashrrev_i32_e32 v11, 31, v10
	v_accvgpr_read_b32 v9, a8
	v_lshlrev_b64 v[10:11], 11, v[10:11]
	v_fma_mixlo_f16 v1, v9, s3, 0
	v_lshl_add_u64 v[10:11], v[20:21], 0, v[10:11]
	global_store_short v[10:11], v1, off
	v_add_u32_e32 v10, 17, v18
	v_accvgpr_read_b32 v8, a9
	v_ashrrev_i32_e32 v11, 31, v10
	v_fma_mixlo_f16 v1, v8, s3, 0
	v_lshlrev_b64 v[8:9], 11, v[10:11]
	v_lshl_add_u64 v[8:9], v[20:21], 0, v[8:9]
	global_store_short v[8:9], v1, off
	v_add_u32_e32 v8, 18, v18
	v_ashrrev_i32_e32 v9, 31, v8
	v_accvgpr_read_b32 v7, a10
	v_lshlrev_b64 v[8:9], 11, v[8:9]
	v_fma_mixlo_f16 v1, v7, s3, 0
	v_lshl_add_u64 v[8:9], v[20:21], 0, v[8:9]
	global_store_short v[8:9], v1, off
	v_add_u32_e32 v8, 19, v18
	v_accvgpr_read_b32 v6, a11
	v_ashrrev_i32_e32 v9, 31, v8
	v_fma_mixlo_f16 v1, v6, s3, 0
	v_lshlrev_b64 v[6:7], 11, v[8:9]
	v_lshl_add_u64 v[6:7], v[20:21], 0, v[6:7]
	global_store_short v[6:7], v1, off
	v_add_u32_e32 v6, 24, v18
	v_ashrrev_i32_e32 v7, 31, v6
	v_accvgpr_read_b32 v5, a12
	v_lshlrev_b64 v[6:7], 11, v[6:7]
	v_fma_mixlo_f16 v1, v5, s3, 0
	v_lshl_add_u64 v[6:7], v[20:21], 0, v[6:7]
	global_store_short v[6:7], v1, off
	v_add_u32_e32 v6, 25, v18
	v_accvgpr_read_b32 v4, a13
	v_ashrrev_i32_e32 v7, 31, v6
	v_fma_mixlo_f16 v1, v4, s3, 0
	v_lshlrev_b64 v[4:5], 11, v[6:7]
	v_lshl_add_u64 v[4:5], v[20:21], 0, v[4:5]
	global_store_short v[4:5], v1, off
	v_add_u32_e32 v4, 26, v18
	v_ashrrev_i32_e32 v5, 31, v4
	v_accvgpr_read_b32 v3, a14
	v_lshlrev_b64 v[4:5], 11, v[4:5]
	v_fma_mixlo_f16 v1, v3, s3, 0
	v_lshl_add_u64 v[4:5], v[20:21], 0, v[4:5]
	global_store_short v[4:5], v1, off
	v_add_u32_e32 v4, 27, v18
	v_accvgpr_read_b32 v2, a15
	v_ashrrev_i32_e32 v5, 31, v4
	v_fma_mixlo_f16 v1, v2, s3, 0
	v_lshlrev_b64 v[2:3], 11, v[4:5]
	v_lshl_add_u64 v[2:3], v[20:21], 0, v[2:3]
	global_store_short v[2:3], v1, off

	.amdhsa_kernel _Z6prep_kPKfS0_S0_S0_PDF16_S1_S1_PfS2_
		.amdhsa_group_segment_fixed_size 18432
		.amdhsa_private_segment_fixed_size 0
		.amdhsa_kernarg_size 72
		.amdhsa_user_sgpr_count 2
		.amdhsa_user_sgpr_dispatch_ptr 0
		.amdhsa_user_sgpr_queue_ptr 0
		.amdhsa_user_sgpr_kernarg_segment_ptr 1
		.amdhsa_user_sgpr_dispatch_id 0
		.amdhsa_user_sgpr_kernarg_preload_length 0
		.amdhsa_user_sgpr_kernarg_preload_offset 0
		.amdhsa_user_sgpr_private_segment_size 0
		.amdhsa_uses_dynamic_stack 0
		.amdhsa_enable_private_segment 0
		.amdhsa_system_sgpr_workgroup_id_x 1
		.amdhsa_system_sgpr_workgroup_id_y 0
		.amdhsa_system_sgpr_workgroup_id_z 0
		.amdhsa_system_sgpr_workgroup_info 0
		.amdhsa_system_vgpr_workitem_id 0
		.amdhsa_next_free_vgpr 168
		.amdhsa_next_free_sgpr 16
		.amdhsa_accum_offset 152
		.amdhsa_reserve_vcc 1
		.amdhsa_float_round_mode_32 0
		.amdhsa_float_round_mode_16_64 0
		.amdhsa_float_denorm_mode_32 3
		.amdhsa_float_denorm_mode_16_64 3
		.amdhsa_dx10_clamp 1
		.amdhsa_ieee_mode 1
		.amdhsa_fp16_overflow 0
		.amdhsa_tg_split 0
		.amdhsa_exception_fp_ieee_invalid_op 0
		.amdhsa_exception_fp_denorm_src 0
		.amdhsa_exception_fp_ieee_div_zero 0
		.amdhsa_exception_fp_ieee_overflow 0
		.amdhsa_exception_fp_ieee_underflow 0
		.amdhsa_exception_fp_ieee_inexact 0
		.amdhsa_exception_int_div_zero 0
	.end_amdhsa_kernel

.LBB2_4:
	s_add_i32 s2, s13, s2
	s_ashr_i32 s3, s2, 31
	s_lshr_b32 s3, s3, 27
	s_add_i32 s3, s2, s3
	s_ashr_i32 s12, s3, 5
	s_lshl_b32 s13, s12, 3
	s_sub_i32 s12, 0x100, s13
	s_min_i32 s12, s12, 8
	s_abs_i32 s14, s12
	v_cvt_f32_u32_e32 v1, s14
	s_sub_i32 s16, 0, s14
	s_andn2_b32 s3, s3, 31
	s_sub_i32 s2, s2, s3
	v_rcp_iflag_f32_e32 v1, v1
	s_abs_i32 s3, s2
	s_xor_b32 s15, s2, s12
	s_ashr_i32 s15, s15, 31
	v_mul_f32_e32 v1, 0x4f7ffffe, v1
	v_cvt_u32_f32_e32 v1, v1
	v_lshlrev_b32_e32 v124, 4, v0
	v_lshrrev_b32_e32 v3, 1, v0
	v_bfe_u32 v2, v0, 2, 4
	v_readfirstlane_b32 s17, v1
	s_mul_i32 s16, s16, s17
	s_mul_hi_u32 s16, s17, s16
	s_add_i32 s17, s17, s16
	s_mul_hi_u32 s16, s3, s17
	s_mul_i32 s17, s16, s14
	s_sub_i32 s3, s3, s17
	s_add_i32 s18, s16, 1
	s_sub_i32 s17, s3, s14
	s_cmp_ge_u32 s3, s14
	s_cselect_b32 s16, s18, s16
	s_cselect_b32 s3, s17, s3
	s_add_i32 s17, s16, 1
	s_cmp_ge_u32 s3, s14
	s_cselect_b32 s3, s17, s16
	s_xor_b32 s3, s3, s15
	s_sub_i32 s3, s3, s15
	s_mul_i32 s14, s3, s12
	s_sub_i32 s2, s2, s14
	s_add_i32 s13, s13, s2
	v_and_b32_e32 v1, 32, v0
	s_lshl_b32 s12, s3, 8
	s_lshl_b32 s2, s13, 8
	v_bitop3_b32 v1, v124, v1, 48 bitop3:0x6c
	s_ashr_i32 s3, s2, 31
	s_ashr_i32 s13, s12, 31
	v_lshrrev_b32_e32 v1, 1, v1
	s_lshl_b64 s[14:15], s[2:3], 12
	s_lshl_b64 s[16:17], s[12:13], 11
	v_and_or_b32 v1, v3, 32, v1
	v_lshrrev_b32_e32 v3, 3, v0
	v_or_b32_e32 v4, 64, v3
	s_movk_i32 s3, 0x70
	s_waitcnt lgkmcnt(0)
	s_add_u32 s18, s8, s14
	v_and_or_b32 v6, v3, 48, v2
	v_and_or_b32 v8, v4, s3, v2
	v_or_b32_e32 v3, 0xc0, v3
	s_movk_i32 s3, 0xf0
	s_addc_u32 s19, s9, s15
	v_and_or_b32 v10, v3, s3, v2
	s_add_u32 s10, s10, s16
	v_mov_b32_e32 v3, 0
	v_or_b32_e32 v9, 0x80, v6
	s_addc_u32 s11, s11, s17
	v_lshlrev_b32_e32 v2, 12, v6
	v_lshlrev_b32_e32 v6, 11, v6
	v_mov_b32_e32 v7, v3
	v_lshlrev_b32_e32 v106, 12, v8
	v_mov_b32_e32 v107, v3
	v_lshlrev_b32_e32 v102, 2, v1
	v_mov_b32_e32 v103, v3
	v_lshl_add_u64 v[104:105], s[10:11], 0, v[6:7]
	v_lshl_add_u64 v[6:7], s[18:19], 0, v[106:107]
	v_lshl_add_u64 v[20:21], v[6:7], 0, v[102:103]
	v_lshlrev_b32_e32 v6, 11, v8
	v_mov_b32_e32 v7, v3
	v_lshlrev_b32_e32 v110, 12, v9
	v_mov_b32_e32 v111, v3
	v_lshl_add_u64 v[108:109], s[10:11], 0, v[6:7]
	v_lshl_add_u64 v[6:7], s[18:19], 0, v[110:111]
	v_lshl_add_u64 v[28:29], v[6:7], 0, v[102:103]
	v_lshlrev_b32_e32 v6, 11, v9
	v_mov_b32_e32 v7, v3
	v_lshlrev_b32_e32 v116, 12, v10
	v_mov_b32_e32 v117, v3
	v_lshl_add_u64 v[112:113], s[10:11], 0, v[6:7]
	v_lshl_add_u64 v[6:7], s[18:19], 0, v[116:117]
	v_lshl_add_u64 v[118:119], v[6:7], 0, v[102:103]
	v_lshlrev_b32_e32 v6, 11, v10
	v_mov_b32_e32 v7, v3
	v_lshl_add_u64 v[4:5], s[18:19], 0, v[2:3]
	v_lshlrev_b32_e32 v178, 1, v1
	v_mov_b32_e32 v179, v3
	v_lshl_add_u64 v[120:121], s[10:11], 0, v[6:7]
	v_lshl_add_u64 v[4:5], v[4:5], 0, v[102:103]
	v_lshl_add_u64 v[18:19], v[104:105], 0, v[178:179]
	v_lshl_add_u64 v[26:27], v[108:109], 0, v[178:179]
	v_lshl_add_u64 v[114:115], v[112:113], 0, v[178:179]
	v_lshl_add_u64 v[122:123], v[120:121], 0, v[178:179]
	global_load_dwordx4 v[54:57], v[4:5], off
	global_load_dwordx4 v[58:61], v[4:5], off offset:16
	global_load_dwordx4 v[62:65], v[18:19], off
	global_load_dwordx4 v[66:69], v[20:21], off
	global_load_dwordx4 v[70:73], v[20:21], off offset:16
	global_load_dwordx4 v[74:77], v[26:27], off
	global_load_dwordx4 v[78:81], v[28:29], off
	global_load_dwordx4 v[82:85], v[28:29], off offset:16
	global_load_dwordx4 v[86:89], v[114:115], off
	global_load_dwordx4 v[90:93], v[118:119], off
	global_load_dwordx4 v[94:97], v[118:119], off offset:16
	global_load_dwordx4 v[98:101], v[122:123], off
	v_lshrrev_b32_e32 v1, 6, v0
	s_mov_b32 s3, 0
	v_bfe_u32 v197, v0, 6, 2
	v_lshlrev_b32_e32 v199, 10, v1
	v_lshrrev_b32_e32 v1, 2, v0
	v_lshrrev_b32_e32 v196, 8, v0
	global_load_dwordx4 v[50:53], v[4:5], off offset:272
	global_load_dwordx4 v[46:49], v[4:5], off offset:256
	global_load_dwordx4 v[10:13], v[18:19], off offset:128
	global_load_dwordx4 v[42:45], v[20:21], off offset:272
	global_load_dwordx4 v[38:41], v[20:21], off offset:256
	global_load_dwordx4 v[6:9], v[26:27], off offset:128
	global_load_dwordx4 v[34:37], v[28:29], off offset:272
	global_load_dwordx4 v[30:33], v[28:29], off offset:256
	global_load_dwordx4 v[14:17], v[114:115], off offset:128
	global_load_dwordx4 v[22:25], v[118:119], off offset:272
	s_nop 0
	global_load_dwordx4 v[26:29], v[118:119], off offset:256
	global_load_dwordx4 v[18:21], v[122:123], off offset:128
	v_and_b32_e32 v200, 0x3f0, v124
	v_or_b32_e32 v211, v199, v200
	s_waitcnt vmcnt(22)
	v_cvt_pk_f16_f32 v61, v60, v61
	v_cvt_pk_f16_f32 v60, v58, v59
	v_cvt_pk_f16_f32 v59, v56, v57
	v_cvt_pk_f16_f32 v58, v54, v55
	s_waitcnt vmcnt(19)
	v_cvt_pk_f16_f32 v57, v72, v73
	v_cvt_pk_f16_f32 v56, v70, v71
	v_cvt_pk_f16_f32 v55, v68, v69
	v_cvt_pk_f16_f32 v54, v66, v67
	ds_write_b128 v211, v[58:61]
	ds_write_b128 v211, v[62:65] offset:32768
	ds_write_b128 v211, v[54:57] offset:8192
	s_waitcnt vmcnt(18)
	ds_write_b128 v211, v[74:77] offset:40960
	s_waitcnt vmcnt(16)
	v_cvt_pk_f16_f32 v57, v84, v85
	v_cvt_pk_f16_f32 v56, v82, v83
	v_cvt_pk_f16_f32 v55, v80, v81
	v_cvt_pk_f16_f32 v54, v78, v79
	ds_write_b128 v211, v[54:57] offset:16384
	s_waitcnt vmcnt(15)
	ds_write_b128 v211, v[86:89] offset:49152
	s_waitcnt vmcnt(13)
	v_cvt_pk_f16_f32 v57, v96, v97
	v_cvt_pk_f16_f32 v56, v94, v95
	v_cvt_pk_f16_f32 v55, v92, v93
	v_cvt_pk_f16_f32 v54, v90, v91
	v_and_b32_e32 v198, 15, v0
	ds_write_b128 v211, v[54:57] offset:24576
	s_waitcnt vmcnt(12)
	ds_write_b128 v211, v[98:101] offset:57344
	v_lshlrev_b32_e32 v5, 6, v0
	v_lshlrev_b32_e32 v54, 2, v0
	v_and_b32_e32 v4, 48, v0
	v_and_b32_e32 v5, 0x3c0, v5
	v_and_b32_e32 v54, 32, v54
	v_bitop3_b32 v201, v5, v54, v4 bitop3:0x36
	v_or3_b32 v4, s14, v116, v102
	v_mov_b32_e32 v5, s15
	v_lshl_add_u64 v[188:189], s[8:9], 0, v[4:5]
	v_or_b32_e32 v4, s14, v102
	v_lshl_add_u64 v[54:55], v[4:5], 0, v[110:111]
	v_lshlrev_b32_e32 v210, 14, v196
	s_mov_b64 s[10:11], 0x100
	v_lshl_add_u64 v[190:191], s[8:9], 0, v[54:55]
	v_lshl_add_u64 v[54:55], v[4:5], 0, v[106:107]
	v_lshl_add_u64 v[4:5], v[4:5], 0, v[2:3]
	v_or_b32_e32 v208, 0x800, v210
	v_or_b32_e32 v207, 0x1000, v210
	v_or_b32_e32 v206, 0x1800, v210
	v_or_b32_e32 v205, 0x2000, v210
	v_or_b32_e32 v204, 0x2800, v210
	v_or_b32_e32 v203, 0x3000, v210
	v_or_b32_e32 v202, 0x3800, v210
	v_lshlrev_b32_e32 v209, 13, v197
	v_lshl_add_u64 v[180:181], v[120:121], 0, s[10:11]
	v_lshl_add_u64 v[182:183], v[112:113], 0, s[10:11]
	v_lshl_add_u64 v[184:185], v[108:109], 0, s[10:11]
	v_lshl_add_u64 v[186:187], v[104:105], 0, s[10:11]
	v_lshl_add_u64 v[192:193], s[8:9], 0, v[54:55]
	v_lshl_add_u64 v[194:195], s[8:9], 0, v[4:5]
	s_mov_b64 s[8:9], 0
	v_mov_b32_e32 v212, 0x10000
	s_mov_b64 s[10:11], 0x80
	v_mov_b32_e32 v2, v3
	v_mov_b32_e32 v4, v3
	v_mov_b32_e32 v5, v3
	v_mov_b32_e32 v54, v3
	v_mov_b32_e32 v55, v3
	v_mov_b32_e32 v56, v3
	v_mov_b32_e32 v57, v3
	v_mov_b32_e32 v58, v3
	v_mov_b32_e32 v59, v3
	v_mov_b32_e32 v60, v3
	v_mov_b32_e32 v61, v3
	v_mov_b32_e32 v62, v3
	v_mov_b32_e32 v63, v3
	v_mov_b32_e32 v64, v3
	v_mov_b32_e32 v65, v3
	v_mov_b32_e32 v66, v3
	v_mov_b32_e32 v67, v3
	v_mov_b32_e32 v68, v3
	v_mov_b32_e32 v69, v3
	v_mov_b32_e32 v70, v3
	v_mov_b32_e32 v71, v3
	v_mov_b32_e32 v72, v3
	v_mov_b32_e32 v73, v3
	v_mov_b32_e32 v74, v3
	v_mov_b32_e32 v75, v3
	v_mov_b32_e32 v76, v3
	v_mov_b32_e32 v77, v3
	v_mov_b32_e32 v78, v3
	v_mov_b32_e32 v79, v3
	v_mov_b32_e32 v80, v3
	v_mov_b32_e32 v81, v3
	v_mov_b32_e32 v82, v3
	v_mov_b32_e32 v83, v3
	v_mov_b32_e32 v84, v3
	v_mov_b32_e32 v85, v3
	v_mov_b32_e32 v86, v3
	v_mov_b32_e32 v87, v3
	v_mov_b32_e32 v88, v3
	v_mov_b32_e32 v89, v3
	v_mov_b32_e32 v90, v3
	v_mov_b32_e32 v91, v3
	v_mov_b32_e32 v92, v3
	v_mov_b32_e32 v93, v3
	v_mov_b32_e32 v94, v3
	v_mov_b32_e32 v95, v3
	v_mov_b32_e32 v96, v3
	v_mov_b32_e32 v97, v3
	v_mov_b32_e32 v98, v3
	v_mov_b32_e32 v99, v3
	v_mov_b32_e32 v100, v3
	v_mov_b32_e32 v101, v3
	v_mov_b32_e32 v102, v3
	v_mov_b32_e32 v104, v3
	v_mov_b32_e32 v105, v3
	v_mov_b32_e32 v106, v3
	v_mov_b32_e32 v108, v3
	v_mov_b32_e32 v109, v3
	v_mov_b32_e32 v110, v3
	v_mov_b32_e32 v112, v3
	v_mov_b32_e32 v113, v3
	v_mov_b32_e32 v114, v3
	v_mov_b32_e32 v115, v3
	v_mov_b32_e32 v116, v3
	v_mov_b32_e32 v118, v3
	v_mov_b32_e32 v119, v3
	v_mov_b32_e32 v120, v3
	v_mov_b32_e32 v121, v3
	v_mov_b32_e32 v122, v3
	v_mov_b32_e32 v123, v3
	v_mov_b32_e32 v124, v3
	v_mov_b32_e32 v125, v3
	v_mov_b32_e32 v126, v3
	v_mov_b32_e32 v127, v3
	v_mov_b32_e32 v128, v3
	v_mov_b32_e32 v129, v3
	v_mov_b32_e32 v130, v3
	v_mov_b32_e32 v131, v3
	v_mov_b32_e32 v132, v3
	v_mov_b32_e32 v133, v3
	v_mov_b32_e32 v134, v3
	v_mov_b32_e32 v135, v3
	v_mov_b32_e32 v136, v3
	v_mov_b32_e32 v137, v3
	v_mov_b32_e32 v138, v3
	v_mov_b32_e32 v139, v3
	v_mov_b32_e32 v140, v3
	v_mov_b32_e32 v141, v3
	v_mov_b32_e32 v142, v3
	v_mov_b32_e32 v143, v3
	v_mov_b32_e32 v144, v3
	v_mov_b32_e32 v145, v3
	v_mov_b32_e32 v146, v3
	v_mov_b32_e32 v147, v3
	v_mov_b32_e32 v148, v3
	v_mov_b32_e32 v149, v3
	v_mov_b32_e32 v150, v3
	v_mov_b32_e32 v151, v3
	v_mov_b32_e32 v152, v3
	v_mov_b32_e32 v153, v3
	v_mov_b32_e32 v154, v3
	v_mov_b32_e32 v155, v3
	v_mov_b32_e32 v156, v3
	v_mov_b32_e32 v157, v3
	v_mov_b32_e32 v158, v3
	v_mov_b32_e32 v159, v3
	v_mov_b32_e32 v160, v3
	v_mov_b32_e32 v161, v3
	v_mov_b32_e32 v162, v3
	v_mov_b32_e32 v163, v3
	v_mov_b32_e32 v164, v3
	v_mov_b32_e32 v165, v3
	v_mov_b32_e32 v166, v3
	v_mov_b32_e32 v167, v3
	v_mov_b32_e32 v168, v3
	v_mov_b32_e32 v169, v3
	v_mov_b32_e32 v170, v3
	v_mov_b32_e32 v171, v3
	v_mov_b32_e32 v172, v3
	v_mov_b32_e32 v173, v3
	v_mov_b32_e32 v174, v3
	v_mov_b32_e32 v175, v3
	v_mov_b32_e32 v176, v3
	v_mov_b32_e32 v177, v3
	s_waitcnt lgkmcnt(0)
	s_barrier
	v_readfirstlane_b32 s20, v0
	s_nop 3
	s_lshr_b32 s20, s20, 6
	s_cmp_ge_u32 s20, 4
	s_cbranch_scc1 .Lq2_loopB
.LBB2_5:
	s_waitcnt vmcnt(2)
	v_cvt_pk_f16_f32 v229, v24, v25
	v_cvt_pk_f16_f32 v228, v22, v23
	s_waitcnt vmcnt(1)
	v_cvt_pk_f16_f32 v227, v28, v29
	v_cvt_pk_f16_f32 v226, v26, v27
	v_lshl_add_u64 v[22:23], v[194:195], 0, s[8:9]
	v_lshl_add_u64 v[24:25], v[192:193], 0, s[8:9]
	v_lshl_add_u64 v[26:27], v[190:191], 0, s[8:9]
	v_lshl_add_u64 v[28:29], v[188:189], 0, s[8:9]
	v_cvt_pk_f16_f32 v217, v52, v53
	v_cvt_pk_f16_f32 v216, v50, v51
	v_cvt_pk_f16_f32 v215, v48, v49
	v_cvt_pk_f16_f32 v214, v46, v47
	v_cvt_pk_f16_f32 v221, v44, v45
	v_cvt_pk_f16_f32 v220, v42, v43
	v_cvt_pk_f16_f32 v219, v40, v41
	v_cvt_pk_f16_f32 v218, v38, v39
	v_cvt_pk_f16_f32 v225, v36, v37
	v_cvt_pk_f16_f32 v224, v34, v35
	v_cvt_pk_f16_f32 v223, v32, v33
	v_cvt_pk_f16_f32 v222, v30, v31
	global_load_dwordx4 v[50:53], v[22:23], off offset:528
	global_load_dwordx4 v[46:49], v[22:23], off offset:512
	global_load_dwordx4 v[42:45], v[24:25], off offset:528
	global_load_dwordx4 v[38:41], v[24:25], off offset:512
	global_load_dwordx4 v[34:37], v[26:27], off offset:528
	global_load_dwordx4 v[30:33], v[26:27], off offset:512
	s_nop 0
	global_load_dwordx4 v[22:25], v[28:29], off offset:528
	s_nop 0
	global_load_dwordx4 v[26:29], v[28:29], off offset:512
	s_lshl_b32 s14, s3, 16
	v_bitop3_b32 v213, v211, s14, v212 bitop3:0xf2
	v_lshl_add_u64 v[230:231], v[186:187], 0, v[178:179]
	ds_write_b128 v213, v[10:13] offset:32768
	ds_write_b128 v213, v[6:9] offset:40960
	ds_write_b128 v213, v[14:17] offset:49152
	s_waitcnt vmcnt(8)
	ds_write_b128 v213, v[18:21] offset:57344
	v_lshl_add_u64 v[232:233], v[184:185], 0, v[178:179]
	v_lshl_add_u64 v[234:235], v[182:183], 0, v[178:179]
	v_lshl_add_u64 v[236:237], v[180:181], 0, v[178:179]
	global_load_dwordx4 v[10:13], v[230:231], off
	global_load_dwordx4 v[6:9], v[232:233], off
	global_load_dwordx4 v[14:17], v[234:235], off
	global_load_dwordx4 v[18:21], v[236:237], off
	s_add_i32 s3, s3, 1
	s_and_b32 s14, s14, 0x10000
	ds_write_b128 v213, v[214:217]
	ds_write_b128 v213, v[218:221] offset:8192
	ds_write_b128 v213, v[222:225] offset:16384
	ds_write_b128 v213, v[226:229] offset:24576
	v_or_b32_e32 v213, s14, v201
	v_add_u32_e32 v238, v213, v210
	v_add_u32_e32 v239, v213, v209
	v_add_u32_e32 v240, v213, v208
	ds_read_b128 v[214:217], v238
	ds_read_b128 v[218:221], v239 offset:32768
	ds_read_b128 v[222:225], v240
	ds_read_b128 v[226:229], v239 offset:34816
	ds_read_b128 v[230:233], v239 offset:36864
	ds_read_b128 v[234:237], v239 offset:38912
	v_add_u32_e32 v242, v213, v206
	s_waitcnt lgkmcnt(3)
	v_mfma_f32_16x16x32_f16 v[158:161], v[222:225], v[218:221], v[158:161]
	v_add_u32_e32 v241, v213, v207
	v_add_u32_e32 v244, v213, v204
	v_add_u32_e32 v243, v213, v205
	s_waitcnt lgkmcnt(2)
	v_mfma_f32_16x16x32_f16 v[154:157], v[222:225], v[226:229], v[154:157]
	v_add_u32_e32 v245, v213, v203
	v_add_u32_e32 v213, v213, v202
	s_waitcnt lgkmcnt(1)
	v_mfma_f32_16x16x32_f16 v[150:153], v[222:225], v[230:233], v[150:153]
	s_waitcnt lgkmcnt(0)
	v_mfma_f32_16x16x32_f16 v[146:149], v[222:225], v[234:237], v[146:149]
	ds_read_b128 v[222:225], v242
	v_mfma_f32_16x16x32_f16 v[174:177], v[214:217], v[218:221], v[174:177]
	v_mfma_f32_16x16x32_f16 v[170:173], v[214:217], v[226:229], v[170:173]
	v_mfma_f32_16x16x32_f16 v[166:169], v[214:217], v[230:233], v[166:169]
	v_mfma_f32_16x16x32_f16 v[162:165], v[214:217], v[234:237], v[162:165]
	ds_read_b128 v[214:217], v241
	s_waitcnt lgkmcnt(1)
	v_mfma_f32_16x16x32_f16 v[126:129], v[222:225], v[218:221], v[126:129]
	v_mfma_f32_16x16x32_f16 v[122:125], v[222:225], v[226:229], v[122:125]
	v_mfma_f32_16x16x32_f16 v[118:121], v[222:225], v[230:233], v[118:121]
	v_mfma_f32_16x16x32_f16 v[114:117], v[222:225], v[234:237], v[114:117]
	ds_read_b128 v[222:225], v244
	s_waitcnt lgkmcnt(0)
	v_mfma_f32_16x16x32_f16 v[94:97], v[222:225], v[218:221], v[94:97]
	v_mfma_f32_16x16x32_f16 v[90:93], v[222:225], v[226:229], v[90:93]
	v_mfma_f32_16x16x32_f16 v[86:89], v[222:225], v[230:233], v[86:89]
	v_mfma_f32_16x16x32_f16 v[82:85], v[222:225], v[234:237], v[82:85]
	ds_read_b128 v[222:225], v213
	v_mfma_f32_16x16x32_f16 v[142:145], v[214:217], v[218:221], v[142:145]
	v_mfma_f32_16x16x32_f16 v[138:141], v[214:217], v[226:229], v[138:141]
	v_mfma_f32_16x16x32_f16 v[134:137], v[214:217], v[230:233], v[134:137]
	v_mfma_f32_16x16x32_f16 v[130:133], v[214:217], v[234:237], v[130:133]
	ds_read_b128 v[214:217], v243
	s_waitcnt lgkmcnt(0)
	v_mfma_f32_16x16x32_f16 v[110:113], v[214:217], v[218:221], v[110:113]
	v_mfma_f32_16x16x32_f16 v[106:109], v[214:217], v[226:229], v[106:109]
	v_mfma_f32_16x16x32_f16 v[102:105], v[214:217], v[230:233], v[102:105]
	v_mfma_f32_16x16x32_f16 v[98:101], v[214:217], v[234:237], v[98:101]
	ds_read_b128 v[214:217], v245
	s_waitcnt lgkmcnt(0)
	v_mfma_f32_16x16x32_f16 v[78:81], v[214:217], v[218:221], v[78:81]
	v_mfma_f32_16x16x32_f16 v[74:77], v[214:217], v[226:229], v[74:77]
	v_mfma_f32_16x16x32_f16 v[70:73], v[214:217], v[230:233], v[70:73]
	v_mfma_f32_16x16x32_f16 v[66:69], v[214:217], v[234:237], v[66:69]
	v_mfma_f32_16x16x32_f16 v[62:65], v[222:225], v[218:221], v[62:65]
	v_mfma_f32_16x16x32_f16 v[58:61], v[222:225], v[226:229], v[58:61]
	v_mfma_f32_16x16x32_f16 v[54:57], v[222:225], v[230:233], v[54:57]
	v_mfma_f32_16x16x32_f16 v[2:5], v[222:225], v[234:237], v[2:5]
	ds_read_b128 v[214:217], v238 offset:1024
	ds_read_b128 v[218:221], v239 offset:33792
	ds_read_b128 v[222:225], v240 offset:1024
	ds_read_b128 v[226:229], v239 offset:35840
	ds_read_b128 v[230:233], v239 offset:37888
	ds_read_b128 v[234:237], v239 offset:39936
	s_waitcnt lgkmcnt(4)
	v_mfma_f32_16x16x32_f16 v[174:177], v[214:217], v[218:221], v[174:177]
	s_waitcnt lgkmcnt(2)
	v_mfma_f32_16x16x32_f16 v[170:173], v[214:217], v[226:229], v[170:173]
	s_waitcnt lgkmcnt(1)
	v_mfma_f32_16x16x32_f16 v[166:169], v[214:217], v[230:233], v[166:169]
	s_waitcnt lgkmcnt(0)
	v_mfma_f32_16x16x32_f16 v[162:165], v[214:217], v[234:237], v[162:165]
	v_mfma_f32_16x16x32_f16 v[158:161], v[222:225], v[218:221], v[158:161]
	v_mfma_f32_16x16x32_f16 v[154:157], v[222:225], v[226:229], v[154:157]
	v_mfma_f32_16x16x32_f16 v[150:153], v[222:225], v[230:233], v[150:153]
	v_mfma_f32_16x16x32_f16 v[146:149], v[222:225], v[234:237], v[146:149]
	ds_read_b128 v[214:217], v241 offset:1024
	ds_read_b128 v[222:225], v242 offset:1024
	s_waitcnt lgkmcnt(1)
	v_mfma_f32_16x16x32_f16 v[142:145], v[214:217], v[218:221], v[142:145]
	v_mfma_f32_16x16x32_f16 v[138:141], v[214:217], v[226:229], v[138:141]
	v_mfma_f32_16x16x32_f16 v[134:137], v[214:217], v[230:233], v[134:137]
	v_mfma_f32_16x16x32_f16 v[130:133], v[214:217], v[234:237], v[130:133]
	s_waitcnt lgkmcnt(0)
	v_mfma_f32_16x16x32_f16 v[126:129], v[222:225], v[218:221], v[126:129]
	v_mfma_f32_16x16x32_f16 v[122:125], v[222:225], v[226:229], v[122:125]
	v_mfma_f32_16x16x32_f16 v[118:121], v[222:225], v[230:233], v[118:121]
	v_mfma_f32_16x16x32_f16 v[114:117], v[222:225], v[234:237], v[114:117]
	ds_read_b128 v[214:217], v243 offset:1024
	ds_read_b128 v[222:225], v244 offset:1024
	s_waitcnt lgkmcnt(1)
	v_mfma_f32_16x16x32_f16 v[110:113], v[214:217], v[218:221], v[110:113]
	v_mfma_f32_16x16x32_f16 v[106:109], v[214:217], v[226:229], v[106:109]
	v_mfma_f32_16x16x32_f16 v[102:105], v[214:217], v[230:233], v[102:105]
	v_mfma_f32_16x16x32_f16 v[98:101], v[214:217], v[234:237], v[98:101]
	s_waitcnt lgkmcnt(0)
	v_mfma_f32_16x16x32_f16 v[94:97], v[222:225], v[218:221], v[94:97]
	v_mfma_f32_16x16x32_f16 v[90:93], v[222:225], v[226:229], v[90:93]
	v_mfma_f32_16x16x32_f16 v[86:89], v[222:225], v[230:233], v[86:89]
	v_mfma_f32_16x16x32_f16 v[82:85], v[222:225], v[234:237], v[82:85]
	ds_read_b128 v[214:217], v245 offset:1024
	ds_read_b128 v[222:225], v213 offset:1024
	s_waitcnt lgkmcnt(1)
	v_mfma_f32_16x16x32_f16 v[78:81], v[214:217], v[218:221], v[78:81]
	v_mfma_f32_16x16x32_f16 v[74:77], v[214:217], v[226:229], v[74:77]
	v_mfma_f32_16x16x32_f16 v[70:73], v[214:217], v[230:233], v[70:73]
	v_mfma_f32_16x16x32_f16 v[66:69], v[214:217], v[234:237], v[66:69]
	s_waitcnt lgkmcnt(0)
	v_mfma_f32_16x16x32_f16 v[62:65], v[222:225], v[218:221], v[62:65]
	v_mfma_f32_16x16x32_f16 v[58:61], v[222:225], v[226:229], v[58:61]
	v_mfma_f32_16x16x32_f16 v[54:57], v[222:225], v[230:233], v[54:57]
	v_mfma_f32_16x16x32_f16 v[2:5], v[222:225], v[234:237], v[2:5]
	s_add_u32 s8, s8, 0x100
	s_addc_u32 s9, s9, 0
	v_lshl_add_u64 v[180:181], v[180:181], 0, s[10:11]
	v_lshl_add_u64 v[182:183], v[182:183], 0, s[10:11]
	v_lshl_add_u64 v[184:185], v[184:185], 0, s[10:11]
	v_lshl_add_u64 v[186:187], v[186:187], 0, s[10:11]
	s_cmpk_eq_i32 s8, 0xe00
	s_barrier
	s_cbranch_scc0 .LBB2_5
	s_branch .Lq2_after
.Lq2_loopB:
	s_lshl_b32 s14, s3, 16
	s_and_b32 s14, s14, 0x10000
	v_or_b32_e32 v213, s14, v201
	v_add_u32_e32 v238, v213, v210
	v_add_u32_e32 v239, v213, v209
	v_add_u32_e32 v240, v213, v208
	ds_read_b128 v[214:217], v238
	ds_read_b128 v[218:221], v239 offset:32768
	ds_read_b128 v[222:225], v240
	ds_read_b128 v[226:229], v239 offset:34816
	ds_read_b128 v[230:233], v239 offset:36864
	ds_read_b128 v[234:237], v239 offset:38912
	v_add_u32_e32 v242, v213, v206
	s_waitcnt lgkmcnt(3)
	v_mfma_f32_16x16x32_f16 v[158:161], v[222:225], v[218:221], v[158:161]
	v_add_u32_e32 v241, v213, v207
	v_add_u32_e32 v244, v213, v204
	v_add_u32_e32 v243, v213, v205
	s_waitcnt lgkmcnt(2)
	v_mfma_f32_16x16x32_f16 v[154:157], v[222:225], v[226:229], v[154:157]
	v_add_u32_e32 v245, v213, v203
	v_add_u32_e32 v213, v213, v202
	s_waitcnt lgkmcnt(1)
	v_mfma_f32_16x16x32_f16 v[150:153], v[222:225], v[230:233], v[150:153]
	s_waitcnt lgkmcnt(0)
	v_mfma_f32_16x16x32_f16 v[146:149], v[222:225], v[234:237], v[146:149]
	ds_read_b128 v[222:225], v242
	v_mfma_f32_16x16x32_f16 v[174:177], v[214:217], v[218:221], v[174:177]
	v_mfma_f32_16x16x32_f16 v[170:173], v[214:217], v[226:229], v[170:173]
	v_mfma_f32_16x16x32_f16 v[166:169], v[214:217], v[230:233], v[166:169]
	v_mfma_f32_16x16x32_f16 v[162:165], v[214:217], v[234:237], v[162:165]
	ds_read_b128 v[214:217], v241
	s_waitcnt lgkmcnt(1)
	v_mfma_f32_16x16x32_f16 v[126:129], v[222:225], v[218:221], v[126:129]
	v_mfma_f32_16x16x32_f16 v[122:125], v[222:225], v[226:229], v[122:125]
	v_mfma_f32_16x16x32_f16 v[118:121], v[222:225], v[230:233], v[118:121]
	v_mfma_f32_16x16x32_f16 v[114:117], v[222:225], v[234:237], v[114:117]
	ds_read_b128 v[222:225], v244
	s_waitcnt lgkmcnt(0)
	v_mfma_f32_16x16x32_f16 v[94:97], v[222:225], v[218:221], v[94:97]
	v_mfma_f32_16x16x32_f16 v[90:93], v[222:225], v[226:229], v[90:93]
	v_mfma_f32_16x16x32_f16 v[86:89], v[222:225], v[230:233], v[86:89]
	v_mfma_f32_16x16x32_f16 v[82:85], v[222:225], v[234:237], v[82:85]
	ds_read_b128 v[222:225], v213
	v_mfma_f32_16x16x32_f16 v[142:145], v[214:217], v[218:221], v[142:145]
	v_mfma_f32_16x16x32_f16 v[138:141], v[214:217], v[226:229], v[138:141]
	v_mfma_f32_16x16x32_f16 v[134:137], v[214:217], v[230:233], v[134:137]
	v_mfma_f32_16x16x32_f16 v[130:133], v[214:217], v[234:237], v[130:133]
	ds_read_b128 v[214:217], v243
	s_waitcnt lgkmcnt(0)
	v_mfma_f32_16x16x32_f16 v[110:113], v[214:217], v[218:221], v[110:113]
	v_mfma_f32_16x16x32_f16 v[106:109], v[214:217], v[226:229], v[106:109]
	v_mfma_f32_16x16x32_f16 v[102:105], v[214:217], v[230:233], v[102:105]
	v_mfma_f32_16x16x32_f16 v[98:101], v[214:217], v[234:237], v[98:101]
	ds_read_b128 v[214:217], v245
	s_waitcnt lgkmcnt(0)
	v_mfma_f32_16x16x32_f16 v[78:81], v[214:217], v[218:221], v[78:81]
	v_mfma_f32_16x16x32_f16 v[74:77], v[214:217], v[226:229], v[74:77]
	v_mfma_f32_16x16x32_f16 v[70:73], v[214:217], v[230:233], v[70:73]
	v_mfma_f32_16x16x32_f16 v[66:69], v[214:217], v[234:237], v[66:69]
	v_mfma_f32_16x16x32_f16 v[62:65], v[222:225], v[218:221], v[62:65]
	v_mfma_f32_16x16x32_f16 v[58:61], v[222:225], v[226:229], v[58:61]
	v_mfma_f32_16x16x32_f16 v[54:57], v[222:225], v[230:233], v[54:57]
	v_mfma_f32_16x16x32_f16 v[2:5], v[222:225], v[234:237], v[2:5]
	ds_read_b128 v[214:217], v238 offset:1024
	ds_read_b128 v[218:221], v239 offset:33792
	ds_read_b128 v[222:225], v240 offset:1024
	ds_read_b128 v[226:229], v239 offset:35840
	ds_read_b128 v[230:233], v239 offset:37888
	ds_read_b128 v[234:237], v239 offset:39936
	s_waitcnt lgkmcnt(4)
	v_mfma_f32_16x16x32_f16 v[174:177], v[214:217], v[218:221], v[174:177]
	s_waitcnt lgkmcnt(2)
	v_mfma_f32_16x16x32_f16 v[170:173], v[214:217], v[226:229], v[170:173]
	s_waitcnt lgkmcnt(1)
	v_mfma_f32_16x16x32_f16 v[166:169], v[214:217], v[230:233], v[166:169]
	s_waitcnt lgkmcnt(0)
	v_mfma_f32_16x16x32_f16 v[162:165], v[214:217], v[234:237], v[162:165]
	v_mfma_f32_16x16x32_f16 v[158:161], v[222:225], v[218:221], v[158:161]
	v_mfma_f32_16x16x32_f16 v[154:157], v[222:225], v[226:229], v[154:157]
	v_mfma_f32_16x16x32_f16 v[150:153], v[222:225], v[230:233], v[150:153]
	v_mfma_f32_16x16x32_f16 v[146:149], v[222:225], v[234:237], v[146:149]
	ds_read_b128 v[214:217], v241 offset:1024
	ds_read_b128 v[222:225], v242 offset:1024
	s_waitcnt lgkmcnt(1)
	v_mfma_f32_16x16x32_f16 v[142:145], v[214:217], v[218:221], v[142:145]
	v_mfma_f32_16x16x32_f16 v[138:141], v[214:217], v[226:229], v[138:141]
	v_mfma_f32_16x16x32_f16 v[134:137], v[214:217], v[230:233], v[134:137]
	v_mfma_f32_16x16x32_f16 v[130:133], v[214:217], v[234:237], v[130:133]
	s_waitcnt lgkmcnt(0)
	v_mfma_f32_16x16x32_f16 v[126:129], v[222:225], v[218:221], v[126:129]
	v_mfma_f32_16x16x32_f16 v[122:125], v[222:225], v[226:229], v[122:125]
	v_mfma_f32_16x16x32_f16 v[118:121], v[222:225], v[230:233], v[118:121]
	v_mfma_f32_16x16x32_f16 v[114:117], v[222:225], v[234:237], v[114:117]
	ds_read_b128 v[214:217], v243 offset:1024
	ds_read_b128 v[222:225], v244 offset:1024
	s_waitcnt lgkmcnt(1)
	v_mfma_f32_16x16x32_f16 v[110:113], v[214:217], v[218:221], v[110:113]
	v_mfma_f32_16x16x32_f16 v[106:109], v[214:217], v[226:229], v[106:109]
	v_mfma_f32_16x16x32_f16 v[102:105], v[214:217], v[230:233], v[102:105]
	v_mfma_f32_16x16x32_f16 v[98:101], v[214:217], v[234:237], v[98:101]
	s_waitcnt lgkmcnt(0)
	v_mfma_f32_16x16x32_f16 v[94:97], v[222:225], v[218:221], v[94:97]
	v_mfma_f32_16x16x32_f16 v[90:93], v[222:225], v[226:229], v[90:93]
	v_mfma_f32_16x16x32_f16 v[86:89], v[222:225], v[230:233], v[86:89]
	v_mfma_f32_16x16x32_f16 v[82:85], v[222:225], v[234:237], v[82:85]
	ds_read_b128 v[214:217], v245 offset:1024
	ds_read_b128 v[222:225], v213 offset:1024
	s_waitcnt lgkmcnt(1)
	v_mfma_f32_16x16x32_f16 v[78:81], v[214:217], v[218:221], v[78:81]
	v_mfma_f32_16x16x32_f16 v[74:77], v[214:217], v[226:229], v[74:77]
	v_mfma_f32_16x16x32_f16 v[70:73], v[214:217], v[230:233], v[70:73]
	v_mfma_f32_16x16x32_f16 v[66:69], v[214:217], v[234:237], v[66:69]
	s_waitcnt lgkmcnt(0)
	v_mfma_f32_16x16x32_f16 v[62:65], v[222:225], v[218:221], v[62:65]
	v_mfma_f32_16x16x32_f16 v[58:61], v[222:225], v[226:229], v[58:61]
	v_mfma_f32_16x16x32_f16 v[54:57], v[222:225], v[230:233], v[54:57]
	v_mfma_f32_16x16x32_f16 v[2:5], v[222:225], v[234:237], v[2:5]
	s_waitcnt vmcnt(2)
	v_cvt_pk_f16_f32 v229, v24, v25
	v_cvt_pk_f16_f32 v228, v22, v23
	s_waitcnt vmcnt(1)
	v_cvt_pk_f16_f32 v227, v28, v29
	v_cvt_pk_f16_f32 v226, v26, v27
	v_lshl_add_u64 v[22:23], v[194:195], 0, s[8:9]
	v_lshl_add_u64 v[24:25], v[192:193], 0, s[8:9]
	v_lshl_add_u64 v[26:27], v[190:191], 0, s[8:9]
	v_lshl_add_u64 v[28:29], v[188:189], 0, s[8:9]
	v_cvt_pk_f16_f32 v217, v52, v53
	v_cvt_pk_f16_f32 v216, v50, v51
	v_cvt_pk_f16_f32 v215, v48, v49
	v_cvt_pk_f16_f32 v214, v46, v47
	v_cvt_pk_f16_f32 v221, v44, v45
	v_cvt_pk_f16_f32 v220, v42, v43
	v_cvt_pk_f16_f32 v219, v40, v41
	v_cvt_pk_f16_f32 v218, v38, v39
	v_cvt_pk_f16_f32 v225, v36, v37
	v_cvt_pk_f16_f32 v224, v34, v35
	v_cvt_pk_f16_f32 v223, v32, v33
	v_cvt_pk_f16_f32 v222, v30, v31
	global_load_dwordx4 v[50:53], v[22:23], off offset:528
	global_load_dwordx4 v[46:49], v[22:23], off offset:512
	global_load_dwordx4 v[42:45], v[24:25], off offset:528
	global_load_dwordx4 v[38:41], v[24:25], off offset:512
	global_load_dwordx4 v[34:37], v[26:27], off offset:528
	global_load_dwordx4 v[30:33], v[26:27], off offset:512
	s_nop 0
	global_load_dwordx4 v[22:25], v[28:29], off offset:528
	s_nop 0
	global_load_dwordx4 v[26:29], v[28:29], off offset:512
	s_lshl_b32 s14, s3, 16
	v_bitop3_b32 v213, v211, s14, v212 bitop3:0xf2
	v_lshl_add_u64 v[230:231], v[186:187], 0, v[178:179]
	ds_write_b128 v213, v[10:13] offset:32768
	ds_write_b128 v213, v[6:9] offset:40960
	ds_write_b128 v213, v[14:17] offset:49152
	s_waitcnt vmcnt(8)
	ds_write_b128 v213, v[18:21] offset:57344
	v_lshl_add_u64 v[232:233], v[184:185], 0, v[178:179]
	v_lshl_add_u64 v[234:235], v[182:183], 0, v[178:179]
	v_lshl_add_u64 v[236:237], v[180:181], 0, v[178:179]
	global_load_dwordx4 v[10:13], v[230:231], off
	global_load_dwordx4 v[6:9], v[232:233], off
	global_load_dwordx4 v[14:17], v[234:235], off
	global_load_dwordx4 v[18:21], v[236:237], off
	s_add_i32 s3, s3, 1
	s_and_b32 s14, s14, 0x10000
	ds_write_b128 v213, v[214:217]
	ds_write_b128 v213, v[218:221] offset:8192
	ds_write_b128 v213, v[222:225] offset:16384
	ds_write_b128 v213, v[226:229] offset:24576
	s_add_u32 s8, s8, 0x100
	s_addc_u32 s9, s9, 0
	v_lshl_add_u64 v[180:181], v[180:181], 0, s[10:11]
	v_lshl_add_u64 v[182:183], v[182:183], 0, s[10:11]
	v_lshl_add_u64 v[184:185], v[184:185], 0, s[10:11]
	v_lshl_add_u64 v[186:187], v[186:187], 0, s[10:11]
	s_cmpk_eq_i32 s8, 0xe00
	s_waitcnt lgkmcnt(0)
	s_barrier
	s_cbranch_scc0 .Lq2_loopB
	s_branch .Lq2_after
.Lq2_after:
	v_add_u32_e32 v194, v201, v210
	ds_read_b128 v[178:181], v194
	v_add_u32_e32 v195, v201, v209
	v_add_u32_e32 v224, v201, v208
	ds_read_b128 v[182:185], v195 offset:32768
	ds_read_b128 v[186:189], v224
	ds_read_b128 v[190:193], v195 offset:34816
	ds_read_b128 v[208:211], v195 offset:36864
	ds_read_b128 v[212:215], v195 offset:38912
	v_add_u32_e32 v236, v201, v207
	v_add_u32_e32 v237, v201, v206
	s_waitcnt lgkmcnt(3)
	v_mfma_f32_16x16x32_f16 v[158:161], v[186:189], v[182:185], v[158:161]
	v_add_u32_e32 v238, v201, v205
	v_add_u32_e32 v239, v201, v204
	v_add_u32_e32 v199, v200, v199
	v_mfma_f32_16x16x32_f16 v[174:177], v[178:181], v[182:185], v[174:177]
	s_waitcnt vmcnt(11)
	v_cvt_pk_f16_f32 v53, v52, v53
	v_cvt_pk_f16_f32 v52, v50, v51
	s_waitcnt vmcnt(10)
	v_cvt_pk_f16_f32 v51, v48, v49
	s_waitcnt lgkmcnt(2)
	v_mfma_f32_16x16x32_f16 v[170:173], v[178:181], v[190:193], v[170:173]
	v_cvt_pk_f16_f32 v50, v46, v47
	v_add_u32_e32 v240, v201, v203
	v_add_u32_e32 v241, v201, v202
	s_waitcnt lgkmcnt(1)
	v_mfma_f32_16x16x32_f16 v[166:169], v[178:181], v[208:211], v[166:169]
	s_waitcnt lgkmcnt(0)
	v_mfma_f32_16x16x32_f16 v[162:165], v[178:181], v[212:215], v[162:165]
	ds_read_b128 v[178:181], v236
	v_mfma_f32_16x16x32_f16 v[154:157], v[186:189], v[190:193], v[154:157]
	v_mfma_f32_16x16x32_f16 v[150:153], v[186:189], v[208:211], v[150:153]
	v_mfma_f32_16x16x32_f16 v[146:149], v[186:189], v[212:215], v[146:149]
	ds_read_b128 v[186:189], v237
	s_waitcnt lgkmcnt(1)
	v_mfma_f32_16x16x32_f16 v[142:145], v[178:181], v[182:185], v[142:145]
	v_mfma_f32_16x16x32_f16 v[138:141], v[178:181], v[190:193], v[138:141]
	v_mfma_f32_16x16x32_f16 v[134:137], v[178:181], v[208:211], v[134:137]
	v_mfma_f32_16x16x32_f16 v[130:133], v[178:181], v[212:215], v[130:133]
	ds_read_b128 v[178:181], v238
	s_waitcnt lgkmcnt(1)
	v_mfma_f32_16x16x32_f16 v[126:129], v[186:189], v[182:185], v[126:129]
	v_mfma_f32_16x16x32_f16 v[122:125], v[186:189], v[190:193], v[122:125]
	v_mfma_f32_16x16x32_f16 v[118:121], v[186:189], v[208:211], v[118:121]
	v_mfma_f32_16x16x32_f16 v[114:117], v[186:189], v[212:215], v[114:117]
	ds_read_b128 v[186:189], v239
	s_waitcnt lgkmcnt(1)
	v_mfma_f32_16x16x32_f16 v[110:113], v[178:181], v[182:185], v[110:113]
	v_mfma_f32_16x16x32_f16 v[106:109], v[178:181], v[190:193], v[106:109]
	v_mfma_f32_16x16x32_f16 v[102:105], v[178:181], v[208:211], v[102:105]
	v_mfma_f32_16x16x32_f16 v[98:101], v[178:181], v[212:215], v[98:101]
	v_or_b32_e32 v178, 0x10000, v199
	v_or_b32_e32 v179, 0x18000, v199
	ds_write_b128 v178, v[50:53]
	ds_read_b128 v[50:53], v240
	s_waitcnt vmcnt(3)
	ds_write_b128 v179, v[10:13]
	v_cvt_pk_f16_f32 v13, v44, v45
	v_cvt_pk_f16_f32 v12, v42, v43
	s_waitcnt lgkmcnt(3)
	v_mfma_f32_16x16x32_f16 v[42:45], v[186:189], v[212:215], v[82:85]
	v_cvt_pk_f16_f32 v11, v40, v41
	v_cvt_pk_f16_f32 v10, v38, v39
	v_add_u32_e32 v38, 0x12000, v199
	ds_read_b128 v[82:85], v241
	ds_write_b128 v38, v[10:13]
	v_add_u32_e32 v38, 0x1a000, v199
	s_waitcnt vmcnt(2)
	ds_write_b128 v38, v[6:9]
	v_cvt_pk_f16_f32 v9, v36, v37
	v_cvt_pk_f16_f32 v8, v34, v35
	v_cvt_pk_f16_f32 v7, v32, v33
	v_cvt_pk_f16_f32 v6, v30, v31
	v_or_b32_e32 v34, 0x14000, v199
	ds_write_b128 v34, v[6:9]
	v_or_b32_e32 v34, 0x1c000, v199
	v_mfma_f32_16x16x32_f16 v[94:97], v[186:189], v[182:185], v[94:97]
	s_waitcnt vmcnt(1)
	ds_write_b128 v34, v[14:17]
	v_cvt_pk_f16_f32 v17, v24, v25
	v_cvt_pk_f16_f32 v16, v22, v23
	v_mfma_f32_16x16x32_f16 v[46:49], v[186:189], v[190:193], v[90:93]
	v_cvt_pk_f16_f32 v15, v28, v29
	v_cvt_pk_f16_f32 v14, v26, v27
	v_add_u32_e32 v34, 0x16000, v199
	v_mfma_f32_16x16x32_f16 v[86:89], v[186:189], v[208:211], v[86:89]
	ds_write_b128 v34, v[14:17]
	v_add_u32_e32 v14, 0x1e000, v199
	s_waitcnt vmcnt(0)
	ds_write_b128 v14, v[18:21]
	s_waitcnt lgkmcnt(8)
	v_mfma_f32_16x16x32_f16 v[78:81], v[50:53], v[182:185], v[78:81]
	v_mfma_f32_16x16x32_f16 v[10:13], v[50:53], v[190:193], v[74:77]
	v_mfma_f32_16x16x32_f16 v[36:39], v[50:53], v[208:211], v[70:73]
	v_mfma_f32_16x16x32_f16 v[30:33], v[50:53], v[212:215], v[66:69]
	s_waitcnt lgkmcnt(6)
	v_mfma_f32_16x16x32_f16 v[6:9], v[82:85], v[182:185], v[62:65]
	v_mfma_f32_16x16x32_f16 v[22:25], v[82:85], v[190:193], v[58:61]
	v_mfma_f32_16x16x32_f16 v[26:29], v[82:85], v[208:211], v[54:57]
	v_mfma_f32_16x16x32_f16 v[2:5], v[82:85], v[212:215], v[2:5]
	ds_read_b128 v[14:17], v194 offset:1024
	ds_read_b128 v[18:21], v195 offset:33792
	ds_read_b128 v[50:53], v224 offset:1024
	ds_read_b128 v[54:57], v195 offset:35840
	ds_read_b128 v[66:69], v195 offset:37888
	ds_read_b128 v[70:73], v195 offset:39936
	s_waitcnt lgkmcnt(4)
	v_mfma_f32_16x16x32_f16 v[58:61], v[14:17], v[18:21], v[174:177]
	s_waitcnt lgkmcnt(3)
	v_mfma_f32_16x16x32_f16 v[82:85], v[50:53], v[18:21], v[158:161]
	s_waitcnt lgkmcnt(2)
	v_mfma_f32_16x16x32_f16 v[90:93], v[50:53], v[54:57], v[154:157]
	s_waitcnt lgkmcnt(1)
	v_mfma_f32_16x16x32_f16 v[150:153], v[50:53], v[66:69], v[150:153]
	s_waitcnt lgkmcnt(0)
	v_mfma_f32_16x16x32_f16 v[50:53], v[50:53], v[70:73], v[146:149]
	s_nop 2
	ds_read_b128 v[146:149], v236 offset:1024
	ds_read_b128 v[154:157], v237 offset:1024
	s_waitcnt lgkmcnt(1)
	v_mfma_f32_16x16x32_f16 v[142:145], v[146:149], v[18:21], v[142:145]
	v_mfma_f32_16x16x32_f16 v[138:141], v[146:149], v[54:57], v[138:141]
	v_mfma_f32_16x16x32_f16 v[134:137], v[146:149], v[66:69], v[134:137]
	v_mfma_f32_16x16x32_f16 v[130:133], v[146:149], v[70:73], v[130:133]
	s_waitcnt lgkmcnt(0)
	v_mfma_f32_16x16x32_f16 v[126:129], v[154:157], v[18:21], v[126:129]
	v_mfma_f32_16x16x32_f16 v[122:125], v[154:157], v[54:57], v[122:125]
	v_mfma_f32_16x16x32_f16 v[118:121], v[154:157], v[66:69], v[118:121]
	v_mfma_f32_16x16x32_f16 v[114:117], v[154:157], v[70:73], v[114:117]
	ds_read_b128 v[146:149], v238 offset:1024
	ds_read_b128 v[154:157], v239 offset:1024
	s_waitcnt lgkmcnt(1)
	v_mfma_f32_16x16x32_f16 v[110:113], v[146:149], v[18:21], v[110:113]
	v_mfma_f32_16x16x32_f16 v[106:109], v[146:149], v[54:57], v[106:109]
	v_mfma_f32_16x16x32_f16 v[102:105], v[146:149], v[66:69], v[102:105]
	v_mfma_f32_16x16x32_f16 v[98:101], v[146:149], v[70:73], v[98:101]
	s_waitcnt lgkmcnt(0)
	v_mfma_f32_16x16x32_f16 v[94:97], v[154:157], v[18:21], v[94:97]
	v_mfma_f32_16x16x32_f16 v[46:49], v[154:157], v[54:57], v[46:49]
	v_mfma_f32_16x16x32_f16 v[86:89], v[154:157], v[66:69], v[86:89]
	v_mfma_f32_16x16x32_f16 v[40:43], v[154:157], v[70:73], v[42:45]
	ds_read_b128 v[146:149], v240 offset:1024
	ds_read_b128 v[154:157], v241 offset:1024
	v_mfma_f32_16x16x32_f16 v[62:65], v[14:17], v[54:57], v[170:173]
	v_mfma_f32_16x16x32_f16 v[74:77], v[14:17], v[66:69], v[166:169]
	v_mfma_f32_16x16x32_f16 v[14:17], v[14:17], v[70:73], v[162:165]
	s_waitcnt lgkmcnt(1)
	v_mfma_f32_16x16x32_f16 v[78:81], v[146:149], v[18:21], v[78:81]
	v_mfma_f32_16x16x32_f16 v[10:13], v[146:149], v[54:57], v[10:13]
	v_mfma_f32_16x16x32_f16 v[34:37], v[146:149], v[66:69], v[36:39]
	v_mfma_f32_16x16x32_f16 v[30:33], v[146:149], v[70:73], v[30:33]
	s_waitcnt lgkmcnt(0)
	v_mfma_f32_16x16x32_f16 v[6:9], v[154:157], v[18:21], v[6:9]
	v_mfma_f32_16x16x32_f16 v[18:21], v[154:157], v[54:57], v[22:25]
	v_mfma_f32_16x16x32_f16 v[22:25], v[154:157], v[66:69], v[26:29]
	v_mfma_f32_16x16x32_f16 v[2:5], v[154:157], v[70:73], v[2:5]
	s_nop 1
	v_or_b32_e32 v26, 0x10000, v194
	s_barrier
	ds_read_b128 v[26:29], v26
	v_add_u32_e32 v44, 0x18000, v195
	ds_read_b128 v[54:57], v44
	ds_read_b128 v[66:69], v44 offset:2048
	ds_read_b128 v[70:73], v44 offset:4096
	ds_read_b128 v[146:149], v44 offset:6144
	v_or_b32_e32 v38, 0x10000, v224
	s_waitcnt lgkmcnt(3)
	v_mfma_f32_16x16x32_f16 v[58:61], v[26:29], v[54:57], v[58:61]
	s_waitcnt lgkmcnt(2)
	v_mfma_f32_16x16x32_f16 v[62:65], v[26:29], v[66:69], v[62:65]
	s_waitcnt lgkmcnt(1)
	v_mfma_f32_16x16x32_f16 v[74:77], v[26:29], v[70:73], v[74:77]
	s_waitcnt lgkmcnt(0)
	v_mfma_f32_16x16x32_f16 v[14:17], v[26:29], v[146:149], v[14:17]
	ds_read_b128 v[26:29], v38
	v_or_b32_e32 v38, 0x10000, v236
	s_waitcnt lgkmcnt(0)
	v_mfma_f32_16x16x32_f16 v[82:85], v[26:29], v[54:57], v[82:85]
	v_mfma_f32_16x16x32_f16 v[90:93], v[26:29], v[66:69], v[90:93]
	v_mfma_f32_16x16x32_f16 v[150:153], v[26:29], v[70:73], v[150:153]
	v_mfma_f32_16x16x32_f16 v[26:29], v[26:29], v[146:149], v[50:53]
	s_nop 2
	ds_read_b128 v[50:53], v38
	v_or_b32_e32 v38, 0x10000, v237
	s_waitcnt lgkmcnt(0)
	v_mfma_f32_16x16x32_f16 v[142:145], v[50:53], v[54:57], v[142:145]
	v_mfma_f32_16x16x32_f16 v[138:141], v[50:53], v[66:69], v[138:141]
	v_mfma_f32_16x16x32_f16 v[134:137], v[50:53], v[70:73], v[134:137]
	v_mfma_f32_16x16x32_f16 v[50:53], v[50:53], v[146:149], v[130:133]
	s_nop 2
	ds_read_b128 v[130:133], v38
	v_or_b32_e32 v38, 0x10000, v238
	s_waitcnt lgkmcnt(0)
	v_mfma_f32_16x16x32_f16 v[154:157], v[130:133], v[54:57], v[126:129]
	v_mfma_f32_16x16x32_f16 v[158:161], v[130:133], v[66:69], v[122:125]
	v_mfma_f32_16x16x32_f16 v[162:165], v[130:133], v[70:73], v[118:121]
	v_mfma_f32_16x16x32_f16 v[130:133], v[130:133], v[146:149], v[114:117]
	s_nop 2
	ds_read_b128 v[114:117], v38
	v_or_b32_e32 v38, 0x10000, v239
	s_waitcnt lgkmcnt(0)
	v_mfma_f32_16x16x32_f16 v[178:181], v[114:117], v[146:149], v[98:101]
	s_nop 2
	ds_read_b128 v[98:101], v38
	v_or_b32_e32 v38, 0x10000, v240
	s_waitcnt lgkmcnt(0)
	v_mfma_f32_16x16x32_f16 v[200:203], v[98:101], v[146:149], v[40:43]
	s_nop 2
	ds_read_b128 v[38:41], v38
	s_waitcnt lgkmcnt(0)
	v_mfma_f32_16x16x32_f16 v[208:211], v[38:41], v[70:73], v[34:37]
	s_nop 2
	v_or_b32_e32 v34, 0x10000, v241
	v_mfma_f32_16x16x32_f16 v[212:215], v[38:41], v[146:149], v[30:33]
	s_nop 2
	ds_read_b128 v[30:33], v34
	v_mfma_f32_16x16x32_f16 v[10:13], v[38:41], v[66:69], v[10:13]
	s_waitcnt lgkmcnt(0)
	v_mfma_f32_16x16x32_f16 v[6:9], v[30:33], v[54:57], v[6:9]
	v_mfma_f32_16x16x32_f16 v[2:5], v[30:33], v[146:149], v[2:5]
	v_mfma_f32_16x16x32_f16 v[166:169], v[114:117], v[54:57], v[110:113]
	v_mfma_f32_16x16x32_f16 v[170:173], v[114:117], v[66:69], v[106:109]
	v_mfma_f32_16x16x32_f16 v[174:177], v[114:117], v[70:73], v[102:105]
	v_mfma_f32_16x16x32_f16 v[182:185], v[98:101], v[54:57], v[94:97]
	v_mfma_f32_16x16x32_f16 v[186:189], v[98:101], v[66:69], v[46:49]
	v_mfma_f32_16x16x32_f16 v[190:193], v[98:101], v[70:73], v[86:89]
	v_mfma_f32_16x16x32_f16 v[204:207], v[38:41], v[54:57], v[78:81]
	v_mfma_f32_16x16x32_f16 v[216:219], v[30:33], v[66:69], v[18:21]
	v_mfma_f32_16x16x32_f16 v[220:223], v[30:33], v[70:73], v[22:25]
	s_nop 1
	v_add_u32_e32 v18, 0x10400, v194
	v_add_u32_e32 v22, 0x10400, v224
	ds_read_b128 v[18:21], v18
	ds_read_b128 v[146:149], v44 offset:1024
	ds_read_b128 v[224:227], v44 offset:3072
	ds_read_b128 v[22:25], v22
	ds_read_b128 v[228:231], v44 offset:5120
	ds_read_b128 v[232:235], v44 offset:7168
	s_waitcnt lgkmcnt(3)
	v_mfma_f32_16x16x32_f16 v[126:129], v[18:21], v[224:227], v[62:65]
	v_mfma_f32_16x16x32_f16 v[122:125], v[18:21], v[146:149], v[58:61]
	s_waitcnt lgkmcnt(1)
	v_mfma_f32_16x16x32_f16 v[114:117], v[18:21], v[228:231], v[74:77]
	s_waitcnt lgkmcnt(0)
	v_mfma_f32_16x16x32_f16 v[118:121], v[18:21], v[232:235], v[14:17]
	v_add_u32_e32 v18, 0x10400, v237
	ds_read_b128 v[18:21], v18
	s_nop 0
	v_add_u32_e32 v14, 0x10400, v236
	ds_read_b128 v[14:17], v14
	v_mfma_f32_16x16x32_f16 v[102:105], v[22:25], v[146:149], v[82:85]
	v_mfma_f32_16x16x32_f16 v[110:113], v[22:25], v[224:227], v[90:93]
	s_waitcnt lgkmcnt(0)
	v_mfma_f32_16x16x32_f16 v[90:93], v[14:17], v[146:149], v[142:145]
	v_mfma_f32_16x16x32_f16 v[94:97], v[14:17], v[224:227], v[138:141]
	v_mfma_f32_16x16x32_f16 v[82:85], v[14:17], v[228:231], v[134:137]
	v_mfma_f32_16x16x32_f16 v[86:89], v[14:17], v[232:235], v[50:53]
	v_add_u32_e32 v14, 0x10400, v238
	ds_read_b128 v[14:17], v14
	v_mfma_f32_16x16x32_f16 v[70:73], v[18:21], v[146:149], v[154:157]
	v_mfma_f32_16x16x32_f16 v[78:81], v[18:21], v[224:227], v[158:161]
	v_mfma_f32_16x16x32_f16 v[66:69], v[18:21], v[228:231], v[162:165]
	v_mfma_f32_16x16x32_f16 v[74:77], v[18:21], v[232:235], v[130:133]
	v_add_u32_e32 v18, 0x10400, v239
	ds_read_b128 v[18:21], v18
	s_waitcnt lgkmcnt(1)
	v_mfma_f32_16x16x32_f16 v[62:65], v[14:17], v[146:149], v[166:169]
	v_mfma_f32_16x16x32_f16 v[58:61], v[14:17], v[224:227], v[170:173]
	v_mfma_f32_16x16x32_f16 v[54:57], v[14:17], v[228:231], v[174:177]
	v_mfma_f32_16x16x32_f16 v[50:53], v[14:17], v[232:235], v[178:181]
	v_add_u32_e32 v14, 0x10400, v240
	ds_read_b128 v[14:17], v14
	s_waitcnt lgkmcnt(1)
	v_mfma_f32_16x16x32_f16 v[46:49], v[18:21], v[146:149], v[182:185]
	v_mfma_f32_16x16x32_f16 v[42:45], v[18:21], v[224:227], v[186:189]
	v_mfma_f32_16x16x32_f16 v[38:41], v[18:21], v[228:231], v[190:193]
	v_mfma_f32_16x16x32_f16 v[34:37], v[18:21], v[232:235], v[200:203]
	v_add_u32_e32 v18, 0x10400, v241
	ds_read_b128 v[130:133], v18
	v_mfma_f32_16x16x32_f16 v[98:101], v[22:25], v[228:231], v[150:153]
	v_mfma_f32_16x16x32_f16 v[106:109], v[22:25], v[232:235], v[26:29]
	s_waitcnt lgkmcnt(1)
	v_mfma_f32_16x16x32_f16 v[30:33], v[14:17], v[146:149], v[204:207]
	v_mfma_f32_16x16x32_f16 v[26:29], v[14:17], v[224:227], v[10:13]
	v_mfma_f32_16x16x32_f16 v[22:25], v[14:17], v[228:231], v[208:211]
	v_mfma_f32_16x16x32_f16 v[18:21], v[14:17], v[232:235], v[212:215]
	s_waitcnt lgkmcnt(0)
	v_mfma_f32_16x16x32_f16 v[14:17], v[130:133], v[146:149], v[6:9]
	v_mfma_f32_16x16x32_f16 v[10:13], v[130:133], v[224:227], v[216:219]
	v_mfma_f32_16x16x32_f16 v[6:9], v[130:133], v[228:231], v[220:223]
	v_mfma_f32_16x16x32_f16 v[2:5], v[130:133], v[232:235], v[2:5]
	v_lshlrev_b32_e32 v131, 8, v197
	v_and_b32_e32 v130, 12, v1
	v_lshl_or_b32 v145, v198, 2, v131
	s_movk_i32 s3, 0x100
	v_cmp_gt_u32_e32 vcc, s3, v0
	v_lshlrev_b32_e32 v146, 10, v130
	v_add_u32_e32 v144, 64, v145
	s_barrier
	s_and_saveexec_b64 s[8:9], vcc
	s_cbranch_execz .LBB2_8
	v_or_b32_e32 v130, v145, v146
	v_add_u32_e32 v131, 0x400, v130
	v_add_u32_e32 v132, 0x800, v130
	v_add_u32_e32 v133, 0xc00, v130
	ds_write2_b32 v130, v122, v126 offset1:16
	ds_write2_b32 v131, v123, v127 offset1:16
	ds_write2_b32 v132, v124, v128 offset1:16
	ds_write2_b32 v133, v125, v129 offset1:16
	ds_write2_b32 v130, v114, v118 offset0:32 offset1:48
	ds_write2_b32 v131, v115, v119 offset0:32 offset1:48
	ds_write2_b32 v132, v116, v120 offset0:32 offset1:48
	ds_write2_b32 v133, v117, v121 offset0:32 offset1:48
	v_add_u32_e32 v131, 0x4000, v130
	v_add_u32_e32 v132, 0x4400, v130
	v_add_u32_e32 v133, 0x4800, v130
	v_add_u32_e32 v136, 0x4c00, v130
	ds_write2_b32 v131, v102, v110 offset1:16
	ds_write2_b32 v132, v103, v111 offset1:16
	ds_write2_b32 v133, v104, v112 offset1:16
	ds_write2_b32 v136, v105, v113 offset1:16
	ds_write2_b32 v131, v98, v106 offset0:32 offset1:48
	ds_write2_b32 v132, v99, v107 offset0:32 offset1:48
	ds_write2_b32 v133, v100, v108 offset0:32 offset1:48
	ds_write2_b32 v136, v101, v109 offset0:32 offset1:48
	v_add_u32_e32 v131, 0x8000, v130
	v_add_u32_e32 v132, 0x8400, v130
	v_add_u32_e32 v133, 0x8800, v130
	v_add_u32_e32 v136, 0x8c00, v130
	ds_write2_b32 v131, v90, v94 offset1:16
	ds_write2_b32 v132, v91, v95 offset1:16
	ds_write2_b32 v133, v92, v96 offset1:16
	ds_write2_b32 v136, v93, v97 offset1:16
	ds_write2_b32 v131, v82, v86 offset0:32 offset1:48
	ds_write2_b32 v132, v83, v87 offset0:32 offset1:48
	ds_write2_b32 v133, v84, v88 offset0:32 offset1:48
	ds_write2_b32 v136, v85, v89 offset0:32 offset1:48
	ds_write_b32 v130, v70 offset:49152
	ds_write_b32 v130, v71 offset:50176
	ds_write_b32 v130, v72 offset:51200
	v_lshl_or_b32 v131, v1, 10, v145
	v_or_b32_e32 v132, 0xcc00, v131
	ds_write_b32 v132, v73
	ds_write_b32 v130, v78 offset:49216
	ds_write_b32 v130, v79 offset:50240
	ds_write_b32 v130, v80 offset:51264
	ds_write_b32 v132, v81 offset:64
	ds_write_b32 v130, v66 offset:49280
	ds_write_b32 v130, v67 offset:50304
	ds_write_b32 v130, v68 offset:51328
	ds_write_b32 v132, v69 offset:128
	ds_write_b32 v130, v74 offset:49344
	ds_write_b32 v130, v75 offset:50368
	ds_write_b32 v130, v76 offset:51392
	ds_write_b32 v132, v77 offset:192
	v_or_b32_e32 v130, 0x10000, v146
	v_or_b32_e32 v132, v145, v130
	ds_write_b32 v132, v62
	v_or_b32_e32 v132, 0x10400, v146
	v_or_b32_e32 v133, v145, v132
	ds_write_b32 v133, v63
	v_or_b32_e32 v133, 0x10800, v146
	v_or_b32_e32 v136, v145, v133
	ds_write_b32 v136, v64
	v_or_b32_e32 v136, 0x10c00, v146
	v_or_b32_e32 v137, v145, v136
	ds_write_b32 v137, v65
	v_add_u32_e32 v137, v144, v130
	ds_write_b32 v137, v58
	v_add_u32_e32 v137, v144, v132
	ds_write_b32 v137, v59
	v_add_u32_e32 v137, v144, v133
	v_add_u32_e32 v134, 0x80, v145
	v_add_u32_e32 v135, 0xc0, v145
	ds_write_b32 v137, v60
	v_add_u32_e32 v137, v144, v136
	ds_write_b32 v137, v61
	v_add_u32_e32 v137, v134, v130
	v_add_u32_e32 v130, v135, v130
	ds_write_b32 v130, v50
	v_add_u32_e32 v130, v135, v132
	ds_write_b32 v130, v51
	v_add_u32_e32 v130, v135, v133
	ds_write_b32 v130, v52
	v_add_u32_e32 v130, v135, v136
	ds_write_b32 v130, v53
	v_or_b32_e32 v130, 0x14000, v146
	ds_write_b32 v137, v54
	v_add_u32_e32 v137, v134, v132
	v_or_b32_e32 v132, v145, v130
	ds_write_b32 v132, v46
	v_or_b32_e32 v132, 0x14400, v146
	ds_write_b32 v137, v55
	v_add_u32_e32 v137, v134, v133
	v_or_b32_e32 v133, v145, v132
	ds_write_b32 v133, v47
	v_or_b32_e32 v133, 0x14800, v146
	ds_write_b32 v137, v56
	v_add_u32_e32 v137, v134, v136
	v_or_b32_e32 v136, v145, v133
	ds_write_b32 v136, v48
	v_or_b32_e32 v136, 0x14c00, v146
	ds_write_b32 v137, v57
	v_or_b32_e32 v137, v145, v136
	ds_write_b32 v137, v49
	v_add_u32_e32 v137, v144, v130
	ds_write_b32 v137, v42
	v_add_u32_e32 v137, v144, v132
	ds_write_b32 v137, v43
	v_add_u32_e32 v137, v144, v133
	ds_write_b32 v137, v44
	v_add_u32_e32 v137, v144, v136
	ds_write_b32 v137, v45
	v_add_u32_e32 v137, v134, v130
	v_add_u32_e32 v130, v135, v130
	ds_write_b32 v130, v34
	v_add_u32_e32 v130, v135, v132
	ds_write_b32 v130, v35
	v_add_u32_e32 v130, v135, v133
	ds_write_b32 v130, v36
	v_add_u32_e32 v130, v135, v136
	ds_write_b32 v130, v37
	v_or_b32_e32 v130, 0x18000, v146
	ds_write_b32 v137, v38
	v_add_u32_e32 v137, v134, v132
	v_or_b32_e32 v132, v145, v130
	ds_write_b32 v132, v30
	v_or_b32_e32 v132, 0x18400, v146
	ds_write_b32 v137, v39
	v_add_u32_e32 v137, v134, v133
	v_or_b32_e32 v133, v145, v132
	ds_write_b32 v133, v31
	v_or_b32_e32 v133, 0x18800, v146
	ds_write_b32 v137, v40
	v_add_u32_e32 v137, v134, v136
	v_or_b32_e32 v136, v145, v133
	ds_write_b32 v136, v32
	v_or_b32_e32 v136, 0x18c00, v146
	ds_write_b32 v137, v41
	v_or_b32_e32 v137, v145, v136
	ds_write_b32 v137, v33
	v_add_u32_e32 v137, v144, v130
	ds_write_b32 v137, v26
	v_add_u32_e32 v137, v144, v132
	ds_write_b32 v137, v27
	v_add_u32_e32 v137, v144, v133
	ds_write_b32 v137, v28
	v_add_u32_e32 v137, v144, v136
	ds_write_b32 v137, v29
	v_add_u32_e32 v137, v134, v130
	v_add_u32_e32 v130, v135, v130
	ds_write_b32 v130, v18
	v_add_u32_e32 v130, v135, v132
	ds_write_b32 v130, v19
	v_add_u32_e32 v130, v135, v133
	ds_write_b32 v130, v20
	v_add_u32_e32 v130, v135, v136
	ds_write_b32 v130, v21
	v_or_b32_e32 v130, 0x1c000, v146
	ds_write_b32 v137, v22
	v_add_u32_e32 v137, v134, v132
	v_or_b32_e32 v132, v145, v130
	ds_write_b32 v132, v14
	v_or_b32_e32 v132, 0x1c400, v146
	ds_write_b32 v137, v23
	v_add_u32_e32 v137, v134, v133
	v_or_b32_e32 v133, v145, v132
	ds_write_b32 v133, v15
	v_or_b32_e32 v133, 0x1c800, v146
	ds_write_b32 v137, v24
	v_add_u32_e32 v137, v134, v136
	v_or_b32_e32 v136, v145, v133
	ds_write_b32 v136, v16
	v_or_b32_e32 v131, 0x1cc00, v131
	v_add_u32_e32 v136, v144, v130
	ds_write_b32 v131, v17
	ds_write_b32 v136, v10
	v_add_u32_e32 v136, v144, v132
	ds_write_b32 v136, v11
	v_add_u32_e32 v136, v144, v133
	ds_write_b32 v137, v25
	ds_write_b32 v136, v12
	ds_write_b32 v131, v13 offset:64
	v_add_u32_e32 v136, v134, v130
	ds_write_b32 v136, v6
	v_add_u32_e32 v136, v134, v132
	v_add_u32_e32 v134, v134, v133
	v_add_u32_e32 v130, v135, v130
	ds_write_b32 v136, v7
	ds_write_b32 v134, v8
	ds_write_b32 v131, v9 offset:128
	ds_write_b32 v130, v2
	v_add_u32_e32 v130, v135, v132
	ds_write_b32 v130, v3
	v_add_u32_e32 v130, v135, v133
	ds_write_b32 v130, v4
	ds_write_b32 v131, v5 offset:192

.LBB2_10:
	s_or_b64 exec, exec, s[4:5]
	s_waitcnt lgkmcnt(0)
	s_barrier
	global_load_dwordx4 v[4:7], v[142:143], off
	global_load_dwordx4 v[0:3], v[142:143], off offset:16
	v_add_u32_e32 v12, v138, v153
	v_add_u32_e32 v20, v138, v160
	v_add_u32_e32 v28, v138, v159
	v_add_u32_e32 v36, v138, v157
	ds_read_b128 v[8:11], v12
	ds_read_b128 v[12:15], v12 offset:16
	ds_read_b128 v[16:19], v20
	ds_read_b128 v[20:23], v20 offset:16
	v_add_u32_e32 v44, v138, v161
	ds_read_b128 v[24:27], v28
	ds_read_b128 v[28:31], v28 offset:16
	ds_read_b128 v[32:35], v36
	ds_read_b128 v[36:39], v36 offset:16
	s_bitset1_b32 s2, 7
	ds_read_b128 v[40:43], v44
	ds_read_b128 v[44:47], v44 offset:16
	v_or_b32_e32 v48, s2, v147
	v_or_b32_e32 v50, s2, v148
	v_or_b32_e32 v52, s2, v149
	v_or_b32_e32 v54, s2, v150
	v_ashrrev_i32_e32 v49, 31, v48
	v_or_b32_e32 v56, s2, v158
	v_ashrrev_i32_e32 v51, 31, v50
	v_ashrrev_i32_e32 v53, 31, v52
	v_ashrrev_i32_e32 v55, 31, v54
	v_lshlrev_b64 v[48:49], 11, v[48:49]
	v_ashrrev_i32_e32 v57, 31, v56
	v_lshlrev_b64 v[50:51], 11, v[50:51]
	v_lshlrev_b64 v[52:53], 11, v[52:53]
	v_lshlrev_b64 v[54:55], 11, v[54:55]
	v_lshl_add_u64 v[48:49], v[140:141], 0, v[48:49]
	v_lshl_add_u64 v[50:51], v[140:141], 0, v[50:51]
	v_lshl_add_u64 v[52:53], v[140:141], 0, v[52:53]
	v_lshl_add_u64 v[54:55], v[140:141], 0, v[54:55]
	s_waitcnt vmcnt(1) lgkmcnt(9)
	v_pk_fma_f32 v[8:9], s[0:1], v[8:9], v[4:5]
	v_pk_fma_f32 v[10:11], s[0:1], v[10:11], v[6:7]
	s_waitcnt vmcnt(0) lgkmcnt(8)
	v_pk_fma_f32 v[12:13], s[0:1], v[12:13], v[0:1]
	v_pk_fma_f32 v[14:15], s[0:1], v[14:15], v[2:3]
	s_waitcnt lgkmcnt(7)
	v_pk_fma_f32 v[16:17], s[0:1], v[16:17], v[4:5]
	v_pk_fma_f32 v[18:19], s[0:1], v[18:19], v[6:7]
	s_waitcnt lgkmcnt(6)
	v_pk_fma_f32 v[20:21], s[0:1], v[20:21], v[0:1]
	v_pk_fma_f32 v[22:23], s[0:1], v[22:23], v[2:3]
	s_waitcnt lgkmcnt(5)
	v_pk_fma_f32 v[24:25], s[0:1], v[24:25], v[4:5]
	v_pk_fma_f32 v[26:27], s[0:1], v[26:27], v[6:7]
	s_waitcnt lgkmcnt(4)
	v_pk_fma_f32 v[28:29], s[0:1], v[28:29], v[0:1]
	v_pk_fma_f32 v[30:31], s[0:1], v[30:31], v[2:3]
	s_waitcnt lgkmcnt(3)
	v_pk_fma_f32 v[32:33], s[0:1], v[32:33], v[4:5]
	v_pk_fma_f32 v[34:35], s[0:1], v[34:35], v[6:7]
	s_waitcnt lgkmcnt(2)
	v_pk_fma_f32 v[36:37], s[0:1], v[36:37], v[0:1]
	v_pk_fma_f32 v[38:39], s[0:1], v[38:39], v[2:3]
	v_cvt_pk_f16_f32 v8, v8, v9
	v_cvt_pk_f16_f32 v9, v10, v11
	v_cvt_pk_f16_f32 v10, v12, v13
	v_cvt_pk_f16_f32 v11, v14, v15
	v_cvt_pk_f16_f32 v12, v16, v17
	v_cvt_pk_f16_f32 v13, v18, v19
	v_cvt_pk_f16_f32 v14, v20, v21
	s_waitcnt lgkmcnt(1)
	v_pk_fma_f32 v[40:41], s[0:1], v[40:41], v[4:5]
	v_pk_fma_f32 v[42:43], s[0:1], v[42:43], v[6:7]
	s_waitcnt lgkmcnt(0)
	v_pk_fma_f32 v[44:45], s[0:1], v[44:45], v[0:1]
	v_pk_fma_f32 v[46:47], s[0:1], v[46:47], v[2:3]
	v_cvt_pk_f16_f32 v15, v22, v23
	v_cvt_pk_f16_f32 v16, v24, v25
	v_cvt_pk_f16_f32 v17, v26, v27
	v_cvt_pk_f16_f32 v18, v28, v29
	v_cvt_pk_f16_f32 v19, v30, v31
	v_cvt_pk_f16_f32 v20, v32, v33
	v_cvt_pk_f16_f32 v21, v34, v35
	v_cvt_pk_f16_f32 v22, v36, v37
	v_cvt_pk_f16_f32 v23, v38, v39
	global_store_dwordx4 v[48:49], v[8:11], off nt
	global_store_dwordx4 v[50:51], v[12:15], off nt
	global_store_dwordx4 v[52:53], v[16:19], off nt
	global_store_dwordx4 v[54:55], v[20:23], off nt
	v_add_u32_e32 v14, v138, v154
	v_lshlrev_b64 v[12:13], 11, v[56:57]
	v_cvt_pk_f16_f32 v24, v40, v41
	v_cvt_pk_f16_f32 v25, v42, v43
	v_cvt_pk_f16_f32 v26, v44, v45
	v_cvt_pk_f16_f32 v27, v46, v47
	ds_read_b128 v[8:11], v14
	v_lshl_add_u64 v[12:13], v[140:141], 0, v[12:13]
	global_store_dwordx4 v[12:13], v[24:27], off nt
	ds_read_b128 v[12:15], v14 offset:16
	v_or_b32_e32 v16, s2, v139
	s_waitcnt lgkmcnt(1)
	v_pk_fma_f32 v[8:9], s[0:1], v[8:9], v[4:5]
	v_pk_fma_f32 v[10:11], s[0:1], v[10:11], v[6:7]
	v_ashrrev_i32_e32 v17, 31, v16
	v_cvt_pk_f16_f32 v8, v8, v9
	v_cvt_pk_f16_f32 v9, v10, v11
	s_waitcnt lgkmcnt(0)
	v_pk_fma_f32 v[10:11], s[0:1], v[12:13], v[0:1]
	v_pk_fma_f32 v[12:13], s[0:1], v[14:15], v[2:3]
	v_lshlrev_b64 v[16:17], 11, v[16:17]
	v_cvt_pk_f16_f32 v10, v10, v11
	v_cvt_pk_f16_f32 v11, v12, v13
	v_add_u32_e32 v18, v138, v155
	v_lshl_add_u64 v[16:17], v[140:141], 0, v[16:17]
	ds_read_b128 v[12:15], v18
	global_store_dwordx4 v[16:17], v[8:11], off nt
	ds_read_b128 v[8:11], v18 offset:16
	v_or_b32_e32 v16, s2, v151
	v_ashrrev_i32_e32 v17, 31, v16
	s_waitcnt lgkmcnt(1)
	v_pk_fma_f32 v[12:13], s[0:1], v[12:13], v[4:5]
	v_pk_fma_f32 v[14:15], s[0:1], v[14:15], v[6:7]
	s_waitcnt lgkmcnt(0)
	v_pk_fma_f32 v[8:9], s[0:1], v[8:9], v[0:1]
	v_cvt_pk_f16_f32 v12, v12, v13
	v_cvt_pk_f16_f32 v13, v14, v15
	v_cvt_pk_f16_f32 v14, v8, v9
	v_pk_fma_f32 v[8:9], s[0:1], v[10:11], v[2:3]
	v_lshlrev_b64 v[16:17], 11, v[16:17]
	v_cvt_pk_f16_f32 v15, v8, v9
	v_add_u32_e32 v18, v138, v156
	v_lshl_add_u64 v[16:17], v[140:141], 0, v[16:17]
	ds_read_b128 v[8:11], v18
	global_store_dwordx4 v[16:17], v[12:15], off nt
	ds_read_b128 v[12:15], v18 offset:16
	s_waitcnt lgkmcnt(1)
	v_pk_fma_f32 v[4:5], s[0:1], v[8:9], v[4:5]
	v_pk_fma_f32 v[6:7], s[0:1], v[10:11], v[6:7]
	s_waitcnt lgkmcnt(0)
	v_pk_fma_f32 v[0:1], s[0:1], v[12:13], v[0:1]
	v_cvt_pk_f16_f32 v4, v4, v5
	v_cvt_pk_f16_f32 v5, v6, v7
	v_cvt_pk_f16_f32 v6, v0, v1
	v_pk_fma_f32 v[0:1], s[0:1], v[14:15], v[2:3]
	s_nop 0
	v_cvt_pk_f16_f32 v7, v0, v1
	v_add_u32_e32 v0, s2, v152
	v_ashrrev_i32_e32 v1, 31, v0
	v_lshlrev_b64 v[0:1], 11, v[0:1]
	v_lshl_add_u64 v[0:1], v[140:141], 0, v[0:1]
	global_store_dwordx4 v[0:1], v[4:7], off nt
	s_endpgm
	.p2align	8

_Z6gemm_kILi1ELi0ELi2ELi3EEvPKvS1_S1_S1_PvS2_PKfiiiiiilllf:
	s_load_dwordx2 s[12:13], s[0:1], 0x48
	s_load_dwordx4 s[4:7], s[0:1], 0x38
	s_load_dwordx2 s[26:27], s[0:1], 0x0
	s_load_dwordx2 s[28:29], s[0:1], 0x10
	s_load_dword s3, s[0:1], 0x70
	s_waitcnt lgkmcnt(0)
	s_mul_i32 s14, s13, s12
	s_abs_i32 s8, s14
	v_cvt_f32_u32_e32 v1, s8
	s_and_b32 s9, s2, 7
	s_ashr_i32 s3, s3, 3
	s_sub_i32 s10, 0, s8
	v_rcp_iflag_f32_e32 v1, v1
	s_mul_i32 s3, s3, s9
	s_ashr_i32 s2, s2, 3
	s_add_i32 s3, s3, s2
	v_mul_f32_e32 v1, 0x4f7ffffe, v1
	v_cvt_u32_f32_e32 v1, v1
	s_abs_i32 s9, s3
	s_xor_b32 s2, s3, s14
	s_ashr_i32 s2, s2, 31
	v_readfirstlane_b32 s11, v1
	s_mul_i32 s10, s10, s11
	s_mul_hi_u32 s10, s11, s10
	s_add_i32 s11, s11, s10
	s_mul_hi_u32 s10, s9, s11
	s_mul_i32 s11, s10, s8
	s_sub_i32 s9, s9, s11
	s_add_i32 s11, s10, 1
	s_sub_i32 s12, s9, s8
	s_cmp_ge_u32 s9, s8
	s_cselect_b32 s10, s11, s10
	s_cselect_b32 s9, s12, s9
	s_add_i32 s11, s10, 1
	s_cmp_ge_u32 s9, s8
	s_cselect_b32 s12, s11, s10
	s_abs_i32 s15, s13
	v_cvt_f32_u32_e32 v1, s15
	s_xor_b32 s12, s12, s2
	s_sub_i32 s12, s12, s2
	s_sub_i32 s16, 0, s15
	v_rcp_iflag_f32_e32 v1, v1
	s_mul_i32 s2, s12, s14
	s_sub_i32 s2, s3, s2
	s_abs_i32 s14, s2
	v_mul_f32_e32 v1, 0x4f7ffffe, v1
	v_cvt_u32_f32_e32 v1, v1
	s_xor_b32 s3, s2, s13
	s_ashr_i32 s3, s3, 31
	s_load_dwordx4 s[8:11], s[0:1], 0x50
	v_readfirstlane_b32 s17, v1
	s_mul_i32 s16, s16, s17
	s_mul_hi_u32 s16, s17, s16
	s_add_i32 s17, s17, s16
	s_mul_hi_u32 s16, s14, s17
	s_mul_i32 s17, s16, s15
	s_sub_i32 s14, s14, s17
	s_add_i32 s17, s16, 1
	s_sub_i32 s18, s14, s15
	s_cmp_ge_u32 s14, s15
	s_cselect_b32 s16, s17, s16
	s_cselect_b32 s14, s18, s14
	s_add_i32 s17, s16, 1
	s_cmp_ge_u32 s14, s15
	s_cselect_b32 s14, s17, s16
	s_xor_b32 s14, s14, s3
	s_sub_i32 s3, s14, s3
	s_mul_i32 s13, s3, s13
	s_sub_i32 s14, s2, s13
	s_ashr_i32 s13, s12, 31
	s_lshl_b32 s33, s3, 8
	s_waitcnt lgkmcnt(0)
	s_mul_i32 s2, s8, s13
	s_mul_hi_u32 s3, s8, s12
	s_add_i32 s2, s3, s2
	s_mul_i32 s3, s9, s12
	s_lshl_b32 s16, s14, 8
	s_add_i32 s3, s2, s3
	s_mul_i32 s2, s8, s12
	s_ashr_i32 s19, s4, 31
	s_mul_i32 s9, s33, s4
	s_mul_hi_i32 s8, s33, s4
	s_add_u32 s2, s9, s2
	s_addc_u32 s3, s8, s3
	s_lshl_b64 s[30:31], s[2:3], 1
	s_mul_i32 s2, s10, s13
	s_mul_hi_u32 s3, s10, s12
	s_add_i32 s2, s3, s2
	s_mul_i32 s3, s11, s12
	s_add_i32 s3, s2, s3
	s_mul_i32 s2, s10, s12
	s_ashr_i32 s35, s5, 31
	s_mul_i32 s9, s16, s5
	s_mul_hi_i32 s8, s16, s5
	s_add_u32 s2, s9, s2
	s_addc_u32 s3, s8, s3
	s_lshl_b64 s[36:37], s[2:3], 2
	s_add_u32 s2, s26, s30
	s_addc_u32 s3, s27, s31
	v_lshrrev_b32_e32 v201, 2, v0
	s_add_u32 s8, s28, s36
	s_mov_b32 s18, s4
	v_mul_lo_u32 v1, s4, v201
	v_lshlrev_b32_e32 v26, 3, v0
	s_addc_u32 s9, s29, s37
	s_ashr_i32 s4, s7, 31
	v_and_b32_e32 v2, 24, v26
	s_lshr_b32 s4, s4, 27
	v_add_lshl_u32 v144, v1, v2, 1
	s_add_i32 s4, s7, s4
	v_lshrrev_b32_e32 v1, 3, v0
	v_lshlrev_b32_e32 v10, 2, v0
	s_ashr_i32 s15, s4, 5
	s_lshl_b64 s[20:21], s[18:19], 8
	v_mul_lo_u32 v1, s5, v1
	v_and_b32_e32 v10, 28, v10
	s_add_u32 s10, s2, s20
	v_add_lshl_u32 v194, v1, v10, 2
	global_load_dwordx4 v[2:5], v144, s[2:3]
	s_addc_u32 s11, s3, s21
	global_load_dwordx4 v[10:13], v194, s[8:9] nt
	global_load_dwordx4 v[6:9], v144, s[10:11]
	s_mov_b32 s34, s5
	s_lshl_b64 s[22:23], s[34:35], 8
	s_add_u32 s4, s8, s22
	s_addc_u32 s5, s9, s23
	global_load_dwordx4 v[14:17], v194, s[4:5] nt
	s_add_u32 s4, s4, s22
	s_addc_u32 s5, s5, s23
	global_load_dwordx4 v[18:21], v194, s[4:5] nt
	s_add_u32 s4, s4, s22
	s_addc_u32 s5, s5, s23
	s_lshl_b64 s[24:25], s[34:35], 9
	s_sub_u32 s17, 0, s24
	s_subb_u32 s35, 0, s25
	global_load_dwordx4 v[22:25], v194, s[4:5] nt
	global_load_dwordx4 v[146:149], v144, s[2:3] offset:64
	global_load_dwordx4 v[150:153], v194, s[8:9] offset:128 nt
	s_add_u32 s4, s4, s17
	s_addc_u32 s5, s5, s35
	s_add_u32 s38, s4, s22
	s_addc_u32 s39, s5, s23
	global_load_dwordx4 v[154:157], v194, s[4:5] offset:128 nt
	global_load_dwordx4 v[158:161], v194, s[38:39] offset:128 nt
	s_add_u32 s4, s38, s22
	s_addc_u32 s5, s39, s23
	global_load_dwordx4 v[166:169], v144, s[2:3] offset:128
	global_load_dwordx4 v[162:165], v144, s[10:11] offset:64
	global_load_dwordx4 v[170:173], v144, s[10:11] offset:128
	global_load_dwordx4 v[174:177], v194, s[8:9] offset:256 nt
	s_add_u32 s2, s4, s17
	s_addc_u32 s3, s5, s35
	global_load_dwordx4 v[178:181], v194, s[4:5] offset:128 nt
	global_load_dwordx4 v[182:185], v194, s[2:3] offset:256 nt
	s_add_u32 s2, s2, s22
	s_addc_u32 s3, s3, s23
	s_add_u32 s4, s2, s22
	s_addc_u32 s5, s3, s23
	global_load_dwordx4 v[186:189], v194, s[2:3] offset:256 nt
	global_load_dwordx4 v[190:193], v194, s[4:5] offset:256 nt
	v_lshlrev_b32_e32 v27, 4, v0
	v_and_b32_e32 v28, 0x1fc0, v27
	v_xor_b32_e32 v27, v27, v0
	v_and_or_b32 v199, v27, 48, v28
	v_lshrrev_b32_e32 v196, 5, v0
	s_load_dwordx2 s[18:19], s[0:1], 0x60
	s_movk_i32 s4, 0xff
	s_cmp_gt_i32 s7, 31
	v_cmp_lt_u32_e32 vcc, s4, v0
	s_cselect_b64 s[4:5], -1, 0
	v_mov_b32_e32 v145, 0
	s_movk_i32 s2, 0x100
	s_waitcnt vmcnt(17)
	ds_write_b128 v199, v[2:5]
	s_waitcnt vmcnt(15)
	ds_write_b128 v199, v[6:9] offset:8192
	v_lshrrev_b32_e32 v2, 1, v0
	v_cvt_f16_f32_e32 v4, v10
	v_cvt_f16_f32_e32 v5, v11
	v_xor_b32_e32 v2, v2, v196
	v_lshlrev_b32_e32 v2, 4, v2
	v_and_b32_e32 v3, 0xfc8, v26
	v_and_or_b32 v200, v2, 48, v3
	v_cvt_pk_f16_f32 v3, v12, v13
	v_cvt_f32_f16_e32 v6, v4
	v_cvt_f32_f16_e32 v7, v5
	v_cvt_f32_f16_e32 v4, v3
	v_cvt_f32_f16_sdwa v5, v3 dst_sel:DWORD dst_unused:UNUSED_PAD src0_sel:WORD_1
	s_waitcnt vmcnt(14)
	v_cvt_f16_f32_e32 v8, v14
	v_cvt_f16_f32_e32 v9, v15
	v_sub_f32_e32 v6, v10, v6
	v_sub_f32_e32 v7, v11, v7
	v_pk_add_f32 v[4:5], v[12:13], v[4:5] neg_lo:[0,1] neg_hi:[0,1]
	v_cvt_pk_f16_f32 v6, v6, v7
	v_cvt_pk_f16_f32 v7, v4, v5
	v_cvt_pk_f16_f32 v5, v16, v17
	v_cvt_pk_f16_f32 v2, v10, v11
	v_cvt_f32_f16_e32 v10, v8
	v_cvt_f32_f16_e32 v11, v9
	v_cvt_f32_f16_e32 v8, v5
	v_cvt_f32_f16_sdwa v9, v5 dst_sel:DWORD dst_unused:UNUSED_PAD src0_sel:WORD_1
	v_cvt_pk_f16_f32 v4, v14, v15
	v_sub_f32_e32 v10, v14, v10
	v_sub_f32_e32 v11, v15, v11
	v_pk_add_f32 v[8:9], v[16:17], v[8:9] neg_lo:[0,1] neg_hi:[0,1]
	v_cvt_pk_f16_f32 v10, v10, v11
	v_cvt_pk_f16_f32 v11, v8, v9
	ds_write2st64_b64 v200, v[2:3], v[4:5] offset0:64 offset1:72
	ds_write2st64_b64 v200, v[6:7], v[10:11] offset0:96 offset1:104
	s_waitcnt vmcnt(13)
	v_cvt_f16_f32_e32 v3, v18
	v_cvt_f16_f32_e32 v4, v19
	s_waitcnt vmcnt(12)
	v_cvt_f16_f32_e32 v8, v22
	v_cvt_f16_f32_e32 v9, v23
	v_cvt_f32_f16_e32 v6, v3
	v_cvt_pk_f16_f32 v3, v20, v21
	v_cvt_f32_f16_e32 v7, v4
	v_cvt_f32_f16_e32 v4, v3
	v_cvt_f32_f16_sdwa v5, v3 dst_sel:DWORD dst_unused:UNUSED_PAD src0_sel:WORD_1
	v_sub_f32_e32 v6, v18, v6
	v_sub_f32_e32 v7, v19, v7
	v_cvt_pk_f16_f32 v6, v6, v7
	v_pk_add_f32 v[4:5], v[20:21], v[4:5] neg_lo:[0,1] neg_hi:[0,1]
	v_cvt_f32_f16_e32 v10, v8
	v_cvt_pk_f16_f32 v7, v4, v5
	v_cvt_pk_f16_f32 v5, v24, v25
	v_cvt_f32_f16_e32 v11, v9
	v_cvt_f32_f16_e32 v8, v5
	v_cvt_f32_f16_sdwa v9, v5 dst_sel:DWORD dst_unused:UNUSED_PAD src0_sel:WORD_1
	v_cvt_pk_f16_f32 v2, v18, v19
	v_cvt_pk_f16_f32 v4, v22, v23
	v_sub_f32_e32 v10, v22, v10
	v_sub_f32_e32 v11, v23, v11
	v_pk_add_f32 v[8:9], v[24:25], v[8:9] neg_lo:[0,1] neg_hi:[0,1]
	v_cvt_pk_f16_f32 v10, v10, v11
	v_cvt_pk_f16_f32 v11, v8, v9
	ds_write2st64_b64 v200, v[2:3], v[4:5] offset0:80 offset1:88
	ds_write2st64_b64 v200, v[6:7], v[10:11] offset0:112 offset1:120
	v_cndmask_b32_e64 v2, 0, 1, s[4:5]
	v_and_b32_e32 v1, 63, v0
	v_lshrrev_b32_e32 v197, 8, v0
	v_bfe_u32 v198, v0, 6, 2
	v_mov_b32_e32 v195, v145
	v_or_b32_e32 v202, 0x2000, v200
	v_cmp_gt_u32_e64 s[2:3], s2, v0
	v_cmp_ne_u32_e64 s[4:5], 1, v2
	s_waitcnt lgkmcnt(0)
	s_barrier
	s_and_saveexec_b64 s[8:9], vcc
	s_xor_b64 s[8:9], exec, s[8:9]
	s_cbranch_execz .LBB3_11
	s_and_b64 vcc, exec, s[4:5]
	v_mov_b32_e32 v128, 0
	v_mov_b32_e32 v143, 0
	v_mov_b32_e32 v142, 0
	v_mov_b32_e32 v141, 0
	v_mov_b32_e32 v140, 0
	v_mov_b32_e32 v139, 0
	v_mov_b32_e32 v138, 0
	v_mov_b32_e32 v137, 0
	v_mov_b32_e32 v136, 0
	v_mov_b32_e32 v135, 0
	v_mov_b32_e32 v134, 0
	v_mov_b32_e32 v133, 0
	v_mov_b32_e32 v132, 0
	v_mov_b32_e32 v131, 0
	v_mov_b32_e32 v130, 0
	v_mov_b32_e32 v113, 0
	v_mov_b32_e32 v112, 0
	v_mov_b32_e32 v111, 0
	v_mov_b32_e32 v110, 0
	v_mov_b32_e32 v109, 0
	v_mov_b32_e32 v108, 0
	v_mov_b32_e32 v107, 0
	v_mov_b32_e32 v106, 0
	v_mov_b32_e32 v105, 0
	v_mov_b32_e32 v104, 0
	v_mov_b32_e32 v103, 0
	v_mov_b32_e32 v102, 0
	v_mov_b32_e32 v101, 0
	v_mov_b32_e32 v100, 0
	v_mov_b32_e32 v99, 0
	v_mov_b32_e32 v98, 0
	v_mov_b32_e32 v97, 0
	v_mov_b32_e32 v96, 0
	v_mov_b32_e32 v95, 0
	v_mov_b32_e32 v94, 0
	v_mov_b32_e32 v93, 0
	v_mov_b32_e32 v92, 0
	v_mov_b32_e32 v91, 0
	v_mov_b32_e32 v90, 0
	v_mov_b32_e32 v89, 0
	v_mov_b32_e32 v88, 0
	v_mov_b32_e32 v87, 0
	v_mov_b32_e32 v86, 0
	v_mov_b32_e32 v85, 0
	v_mov_b32_e32 v84, 0
	v_mov_b32_e32 v83, 0
	v_mov_b32_e32 v82, 0
	v_mov_b32_e32 v81, 0
	v_mov_b32_e32 v80, 0
	v_mov_b32_e32 v79, 0
	v_mov_b32_e32 v78, 0
	v_mov_b32_e32 v77, 0
	v_mov_b32_e32 v76, 0
	v_mov_b32_e32 v75, 0
	v_mov_b32_e32 v74, 0
	v_mov_b32_e32 v73, 0
	v_mov_b32_e32 v72, 0
	v_mov_b32_e32 v71, 0
	v_mov_b32_e32 v70, 0
	v_mov_b32_e32 v69, 0
	v_mov_b32_e32 v68, 0
	v_mov_b32_e32 v67, 0
	v_mov_b32_e32 v66, 0
	v_mov_b32_e32 v65, 0
	v_mov_b32_e32 v64, 0
	v_mov_b32_e32 v63, 0
	v_mov_b32_e32 v62, 0
	v_mov_b32_e32 v61, 0
	v_mov_b32_e32 v60, 0
	v_mov_b32_e32 v59, 0
	v_mov_b32_e32 v58, 0
	v_mov_b32_e32 v57, 0
	v_mov_b32_e32 v56, 0
	v_mov_b32_e32 v55, 0
	v_mov_b32_e32 v54, 0
	v_mov_b32_e32 v53, 0
	v_mov_b32_e32 v52, 0
	v_mov_b32_e32 v51, 0
	v_mov_b32_e32 v50, 0
	v_mov_b32_e32 v49, 0
	v_mov_b32_e32 v48, 0
	v_mov_b32_e32 v47, 0
	v_mov_b32_e32 v46, 0
	v_mov_b32_e32 v45, 0
	v_mov_b32_e32 v44, 0
	v_mov_b32_e32 v43, 0
	v_mov_b32_e32 v42, 0
	v_mov_b32_e32 v41, 0
	v_mov_b32_e32 v40, 0
	v_mov_b32_e32 v39, 0
	v_mov_b32_e32 v38, 0
	v_mov_b32_e32 v37, 0
	v_mov_b32_e32 v36, 0
	v_mov_b32_e32 v35, 0
	v_mov_b32_e32 v34, 0
	v_mov_b32_e32 v33, 0
	v_mov_b32_e32 v32, 0
	v_mov_b32_e32 v31, 0
	v_mov_b32_e32 v30, 0
	v_mov_b32_e32 v29, 0
	v_mov_b32_e32 v28, 0
	v_mov_b32_e32 v27, 0
	v_mov_b32_e32 v26, 0
	v_mov_b32_e32 v25, 0
	v_mov_b32_e32 v24, 0
	v_mov_b32_e32 v23, 0
	v_mov_b32_e32 v22, 0
	v_mov_b32_e32 v21, 0
	v_mov_b32_e32 v20, 0
	v_mov_b32_e32 v19, 0
	v_mov_b32_e32 v18, 0
	v_mov_b32_e32 v17, 0
	v_mov_b32_e32 v16, 0
	v_mov_b32_e32 v15, 0
	v_mov_b32_e32 v14, 0
	v_mov_b32_e32 v13, 0
	v_mov_b32_e32 v12, 0
	v_mov_b32_e32 v11, 0
	v_mov_b32_e32 v10, 0
	v_mov_b32_e32 v9, 0
	v_mov_b32_e32 v8, 0
	v_mov_b32_e32 v7, 0
	v_mov_b32_e32 v6, 0
	v_mov_b32_e32 v5, 0
	v_mov_b32_e32 v4, 0
	v_mov_b32_e32 v3, 0
	v_mov_b32_e32 v2, 0
	s_cbranch_vccnz .LBB3_10
	v_lshlrev_b32_e32 v5, 6, v0
	v_lshrrev_b32_e32 v2, 5, v1
	v_bfe_u32 v3, v0, 2, 2
	v_and_b32_e32 v5, 0x7c0, v5
	s_add_u32 s10, s28, s36
	v_bitop3_b32 v4, v2, v201, 3 bitop3:0x78
	v_lshl_or_b32 v6, v197, 13, v5
	v_lshl_or_b32 v5, v198, 12, v5
	v_bitop3_b32 v2, v2, v3, 2 bitop3:0x36
	s_addc_u32 s11, s29, s37
	v_lshlrev_b32_e32 v4, 4, v4
	v_or_b32_e32 v7, 0x800, v6
	v_or_b32_e32 v9, 0x1000, v6
	v_or_b32_e32 v11, 0x1800, v6
	v_or_b32_e32 v13, 0x800, v5
	v_lshlrev_b32_e32 v2, 4, v2
	s_add_u32 s38, s26, s30
	v_or_b32_e32 v118, v4, v6
	v_or_b32_e32 v8, v7, v4
	v_or_b32_e32 v10, v9, v4
	v_or_b32_e32 v12, v11, v4
	v_or_b32_e32 v119, v5, v4
	v_or_b32_e32 v120, v13, v4
	v_or_b32_e32 v121, v2, v6
	v_or_b32_e32 v4, v2, v7
	v_or_b32_e32 v6, v2, v9
	v_or_b32_e32 v7, v2, v11
	v_or_b32_e32 v122, v2, v5
	v_or_b32_e32 v123, v13, v2
	v_lshl_add_u64 v[2:3], s[10:11], 0, v[194:195]
	s_mov_b64 s[10:11], 0x200
	s_addc_u32 s39, s27, s31
	v_lshl_add_u64 v[114:115], v[2:3], 0, s[10:11]
	v_lshl_add_u64 v[2:3], s[38:39], 0, v[144:145]
	s_mov_b64 s[38:39], 0x100
	v_lshl_add_u64 v[116:117], v[2:3], 0, s[38:39]
	v_mov_b32_e32 v2, 0
	s_mov_b32 s7, 4
	s_mul_hi_i32 s11, s34, 0x300
	s_mul_i32 s10, s34, 0x300
	v_or_b32_e32 v124, 0x10000, v199
	v_or_b32_e32 v125, 0x12000, v199
	v_or_b32_e32 v126, 0x18000, v200
	v_or_b32_e32 v127, 0x1c000, v200
	v_or_b32_e32 v128, 0x19000, v200
	v_or_b32_e32 v129, 0x1d000, v200
	v_or_b32_e32 v194, 0x18000, v202
	v_or_b32_e32 v195, 0x1c000, v202
	v_or_b32_e32 v201, 0x1b000, v200
	v_or_b32_e32 v202, 0x1f000, v200
	v_or_b32_e32 v203, 0x10000, v8
	v_or_b32_e32 v204, 0x10000, v10
	v_or_b32_e32 v205, 0x10000, v12
	v_or_b32_e32 v206, 0x10000, v4
	v_or_b32_e32 v207, 0x10000, v6
	v_or_b32_e32 v208, 0x10000, v7
	s_mov_b64 s[40:41], 0x80
	v_mov_b32_e32 v3, v2
	v_mov_b32_e32 v4, v2
	v_mov_b32_e32 v5, v2
	v_mov_b32_e32 v6, v2
	v_mov_b32_e32 v7, v2
	v_mov_b32_e32 v8, v2
	v_mov_b32_e32 v9, v2
	v_mov_b32_e32 v10, v2
	v_mov_b32_e32 v11, v2
	v_mov_b32_e32 v12, v2
	v_mov_b32_e32 v13, v2
	v_mov_b32_e32 v14, v2
	v_mov_b32_e32 v15, v2
	v_mov_b32_e32 v16, v2
	v_mov_b32_e32 v17, v2
	v_mov_b32_e32 v18, v2
	v_mov_b32_e32 v19, v2
	v_mov_b32_e32 v20, v2
	v_mov_b32_e32 v21, v2
	v_mov_b32_e32 v22, v2
	v_mov_b32_e32 v23, v2
	v_mov_b32_e32 v24, v2
	v_mov_b32_e32 v25, v2
	v_mov_b32_e32 v26, v2
	v_mov_b32_e32 v27, v2
	v_mov_b32_e32 v28, v2
	v_mov_b32_e32 v29, v2
	v_mov_b32_e32 v30, v2
	v_mov_b32_e32 v31, v2
	v_mov_b32_e32 v32, v2
	v_mov_b32_e32 v33, v2
	v_mov_b32_e32 v34, v2
	v_mov_b32_e32 v35, v2
	v_mov_b32_e32 v36, v2
	v_mov_b32_e32 v37, v2
	v_mov_b32_e32 v38, v2
	v_mov_b32_e32 v39, v2
	v_mov_b32_e32 v40, v2
	v_mov_b32_e32 v41, v2
	v_mov_b32_e32 v42, v2
	v_mov_b32_e32 v43, v2
	v_mov_b32_e32 v44, v2
	v_mov_b32_e32 v45, v2
	v_mov_b32_e32 v46, v2
	v_mov_b32_e32 v47, v2
	v_mov_b32_e32 v48, v2
	v_mov_b32_e32 v49, v2
	v_mov_b32_e32 v50, v2
	v_mov_b32_e32 v51, v2
	v_mov_b32_e32 v52, v2
	v_mov_b32_e32 v53, v2
	v_mov_b32_e32 v54, v2
	v_mov_b32_e32 v55, v2
	v_mov_b32_e32 v56, v2
	v_mov_b32_e32 v57, v2
	v_mov_b32_e32 v58, v2
	v_mov_b32_e32 v59, v2
	v_mov_b32_e32 v60, v2
	v_mov_b32_e32 v61, v2
	v_mov_b32_e32 v62, v2
	v_mov_b32_e32 v63, v2
	v_mov_b32_e32 v64, v2
	v_mov_b32_e32 v65, v2
	v_mov_b32_e32 v66, v2
	v_mov_b32_e32 v67, v2
	v_mov_b32_e32 v68, v2
	v_mov_b32_e32 v69, v2
	v_mov_b32_e32 v70, v2
	v_mov_b32_e32 v71, v2
	v_mov_b32_e32 v72, v2
	v_mov_b32_e32 v73, v2
	v_mov_b32_e32 v74, v2
	v_mov_b32_e32 v75, v2
	v_mov_b32_e32 v76, v2
	v_mov_b32_e32 v77, v2
	v_mov_b32_e32 v78, v2
	v_mov_b32_e32 v79, v2
	v_mov_b32_e32 v80, v2
	v_mov_b32_e32 v81, v2
	v_mov_b32_e32 v82, v2
	v_mov_b32_e32 v83, v2
	v_mov_b32_e32 v84, v2
	v_mov_b32_e32 v85, v2
	v_mov_b32_e32 v86, v2
	v_mov_b32_e32 v87, v2
	v_mov_b32_e32 v88, v2
	v_mov_b32_e32 v89, v2
	v_mov_b32_e32 v90, v2
	v_mov_b32_e32 v91, v2
	v_mov_b32_e32 v92, v2
	v_mov_b32_e32 v93, v2
	v_mov_b32_e32 v94, v2
	v_mov_b32_e32 v95, v2
	v_mov_b32_e32 v96, v2
	v_mov_b32_e32 v97, v2
	v_mov_b32_e32 v98, v2
	v_mov_b32_e32 v99, v2
	v_mov_b32_e32 v100, v2
	v_mov_b32_e32 v101, v2
	v_mov_b32_e32 v102, v2
	v_mov_b32_e32 v103, v2
	v_mov_b32_e32 v104, v2
	v_mov_b32_e32 v105, v2
	v_mov_b32_e32 v106, v2
	v_mov_b32_e32 v107, v2
	v_mov_b32_e32 v108, v2
	v_mov_b32_e32 v109, v2
	v_mov_b32_e32 v110, v2
	v_mov_b32_e32 v111, v2
	v_mov_b32_e32 v112, v2
	v_mov_b32_e32 v113, v2
	v_mov_b32_e32 v130, v2
	v_mov_b32_e32 v131, v2
	v_mov_b32_e32 v132, v2
	v_mov_b32_e32 v133, v2
	v_mov_b32_e32 v134, v2
	v_mov_b32_e32 v135, v2
	v_mov_b32_e32 v136, v2
	v_mov_b32_e32 v137, v2
	v_mov_b32_e32 v138, v2
	v_mov_b32_e32 v139, v2
	v_mov_b32_e32 v140, v2
	v_mov_b32_e32 v141, v2
	v_mov_b32_e32 v142, v2
	v_mov_b32_e32 v143, v2
	v_mov_b32_e32 v144, v2
	v_mov_b32_e32 v145, v2
	s_waitcnt vmcnt(3)
	s_branch .LBB3_4

.LBB3_4:
	s_add_i32 s17, s7, -2
	s_cmp_lt_i32 s17, s15
	s_cbranch_scc1 .Lgk_hi_steady
	s_waitcnt vmcnt(0)
.Lgk_hi_steady:
	s_waitcnt vmcnt(6)
	v_cvt_f16_f32_e32 v209, v150
	v_cvt_f16_f32_e32 v211, v151
	v_cvt_pk_f16_f32 v210, v150, v151
	s_add_i32 s17, s7, -1
	v_cvt_f32_f16_e32 v209, v209
	v_cvt_f32_f16_e32 v214, v211
	v_cvt_pk_f16_f32 v211, v152, v153
	v_cvt_f32_f16_e32 v212, v211
	v_cvt_f32_f16_sdwa v213, v211 dst_sel:DWORD dst_unused:UNUSED_PAD src0_sel:WORD_1
	v_sub_f32_e32 v209, v150, v209
	v_sub_f32_e32 v214, v151, v214
	v_cvt_pk_f16_f32 v214, v209, v214
	ds_write_b64 v126, v[210:211]
	v_cvt_f16_f32_e32 v209, v154
	v_cvt_f16_f32_e32 v211, v155
	v_pk_add_f32 v[212:213], v[152:153], v[212:213] neg_lo:[0,1] neg_hi:[0,1]
	v_cvt_pk_f16_f32 v210, v154, v155
	v_cvt_pk_f16_f32 v215, v212, v213
	ds_write_b64 v127, v[214:215]
	v_cvt_f32_f16_e32 v209, v209
	v_cvt_f32_f16_e32 v214, v211
	v_cvt_pk_f16_f32 v211, v156, v157
	v_cvt_f32_f16_e32 v212, v211
	v_cvt_f32_f16_sdwa v213, v211 dst_sel:DWORD dst_unused:UNUSED_PAD src0_sel:WORD_1
	v_sub_f32_e32 v209, v154, v209
	v_sub_f32_e32 v214, v155, v214
	v_cvt_pk_f16_f32 v214, v209, v214
	ds_write_b64 v128, v[210:211]
	v_cvt_f16_f32_e32 v209, v158
	v_cvt_f16_f32_e32 v211, v159
	v_pk_add_f32 v[212:213], v[156:157], v[212:213] neg_lo:[0,1] neg_hi:[0,1]
	v_cvt_pk_f16_f32 v210, v158, v159
	v_cvt_pk_f16_f32 v215, v212, v213
	ds_write_b64 v129, v[214:215]
	v_cvt_f32_f16_e32 v209, v209
	v_cvt_f32_f16_e32 v214, v211
	v_cvt_pk_f16_f32 v211, v160, v161
	v_cvt_f32_f16_e32 v212, v211
	v_cvt_f32_f16_sdwa v213, v211 dst_sel:DWORD dst_unused:UNUSED_PAD src0_sel:WORD_1
	v_sub_f32_e32 v209, v158, v209
	v_sub_f32_e32 v214, v159, v214
	ds_write_b64 v194, v[210:211]
	v_cvt_f16_f32_e32 v211, v179
	v_cvt_pk_f16_f32 v214, v209, v214
	v_cvt_f16_f32_e32 v209, v178
	v_pk_add_f32 v[212:213], v[160:161], v[212:213] neg_lo:[0,1] neg_hi:[0,1]
	v_cvt_pk_f16_f32 v210, v178, v179
	v_cvt_pk_f16_f32 v215, v212, v213
	ds_write_b64 v195, v[214:215]
	v_cvt_f32_f16_e32 v214, v211
	v_cvt_pk_f16_f32 v211, v180, v181
	v_cvt_f32_f16_e32 v209, v209
	v_cvt_f32_f16_e32 v212, v211
	v_cvt_f32_f16_sdwa v213, v211 dst_sel:DWORD dst_unused:UNUSED_PAD src0_sel:WORD_1
	v_sub_f32_e32 v214, v179, v214
	v_sub_f32_e32 v209, v178, v209
	v_cvt_pk_f16_f32 v214, v209, v214
	v_pk_add_f32 v[212:213], v[180:181], v[212:213] neg_lo:[0,1] neg_hi:[0,1]
	s_cmp_ge_i32 s17, s15
	v_cvt_pk_f16_f32 v215, v212, v213
	ds_write_b128 v124, v[146:149]
	ds_write_b128 v125, v[162:165]
	ds_write_b64 v201, v[210:211]
	ds_write_b64 v202, v[214:215]
	s_cbranch_scc1 .LBB3_6
	v_lshl_add_u64 v[150:151], v[116:117], 0, s[20:21]
	v_lshl_add_u64 v[154:155], v[114:115], 0, s[22:23]
	v_lshl_add_u64 v[158:159], v[114:115], 0, s[24:25]
	v_lshl_add_u64 v[178:179], v[114:115], 0, s[10:11]
	global_load_dwordx4 v[146:149], v[116:117], off offset:-64
	global_load_dwordx4 v[162:165], v[150:151], off offset:-64
	s_nop 0
	global_load_dwordx4 v[150:153], v[114:115], off offset:-128 nt
	s_nop 0
	global_load_dwordx4 v[154:157], v[154:155], off offset:-128 nt
	s_nop 0
	global_load_dwordx4 v[158:161], v[158:159], off offset:-128 nt
	s_nop 0
	global_load_dwordx4 v[178:181], v[178:179], off offset:-128 nt
.LBB3_6:
	ds_read_b128 v[210:213], v118
	ds_read_b128 v[214:217], v118 offset:2048
	ds_read_b128 v[218:221], v118 offset:4096
	ds_read_b128 v[222:225], v118 offset:6144
	ds_read_b128 v[230:233], v119 offset:49152
	ds_read_b128 v[226:229], v119 offset:32768
	s_add_i32 s17, s7, -2
	s_cmp_ge_i32 s17, s15
	s_waitcnt lgkmcnt(1)
	v_mfma_f32_32x32x16_f16 v[130:145], v[210:213], v[230:233], v[130:145]
	ds_read_b128 v[238:241], v119 offset:51200
	ds_read_b128 v[234:237], v119 offset:34816
	s_waitcnt lgkmcnt(2)
	v_mfma_f32_32x32x16_f16 v[130:145], v[210:213], v[226:229], v[130:145]
	s_waitcnt lgkmcnt(1)
	v_mfma_f32_32x32x16_f16 v[98:113], v[210:213], v[238:241], v[98:113]
	s_waitcnt lgkmcnt(0)
	v_mfma_f32_32x32x16_f16 v[98:113], v[210:213], v[234:237], v[98:113]
	ds_read_b128 v[210:213], v121
	v_mfma_f32_32x32x16_f16 v[82:97], v[214:217], v[230:233], v[82:97]
	v_mfma_f32_32x32x16_f16 v[82:97], v[214:217], v[226:229], v[82:97]
	v_mfma_f32_32x32x16_f16 v[66:81], v[214:217], v[238:241], v[66:81]
	v_mfma_f32_32x32x16_f16 v[66:81], v[214:217], v[234:237], v[66:81]
	ds_read_b128 v[214:217], v121 offset:2048
	v_mfma_f32_32x32x16_f16 v[50:65], v[218:221], v[230:233], v[50:65]
	v_mfma_f32_32x32x16_f16 v[50:65], v[218:221], v[226:229], v[50:65]
	v_mfma_f32_32x32x16_f16 v[34:49], v[218:221], v[238:241], v[34:49]
	v_mfma_f32_32x32x16_f16 v[34:49], v[218:221], v[234:237], v[34:49]
	ds_read_b128 v[218:221], v121 offset:4096
	v_mfma_f32_32x32x16_f16 v[18:33], v[222:225], v[230:233], v[18:33]
	ds_read_b128 v[230:233], v122 offset:49152
	v_mfma_f32_32x32x16_f16 v[18:33], v[222:225], v[226:229], v[18:33]
	ds_read_b128 v[226:229], v122 offset:32768
	v_mfma_f32_32x32x16_f16 v[2:17], v[222:225], v[238:241], v[2:17]
	ds_read_b128 v[238:241], v122 offset:51200
	v_mfma_f32_32x32x16_f16 v[2:17], v[222:225], v[234:237], v[2:17]
	ds_read_b128 v[222:225], v121 offset:6144
	ds_read_b128 v[234:237], v122 offset:34816
	s_waitcnt lgkmcnt(0)
	s_barrier
	v_mfma_f32_32x32x16_f16 v[130:145], v[210:213], v[230:233], v[130:145]
	v_mfma_f32_32x32x16_f16 v[130:145], v[210:213], v[226:229], v[130:145]
	v_mfma_f32_32x32x16_f16 v[98:113], v[210:213], v[238:241], v[98:113]
	v_mfma_f32_32x32x16_f16 v[98:113], v[210:213], v[234:237], v[98:113]
	v_mfma_f32_32x32x16_f16 v[82:97], v[214:217], v[230:233], v[82:97]
	v_mfma_f32_32x32x16_f16 v[82:97], v[214:217], v[226:229], v[82:97]
	v_mfma_f32_32x32x16_f16 v[66:81], v[214:217], v[238:241], v[66:81]
	v_mfma_f32_32x32x16_f16 v[66:81], v[214:217], v[234:237], v[66:81]
	v_mfma_f32_32x32x16_f16 v[50:65], v[218:221], v[230:233], v[50:65]
	v_mfma_f32_32x32x16_f16 v[50:65], v[218:221], v[226:229], v[50:65]
	v_mfma_f32_32x32x16_f16 v[34:49], v[218:221], v[238:241], v[34:49]
	v_mfma_f32_32x32x16_f16 v[34:49], v[218:221], v[234:237], v[34:49]
	v_mfma_f32_32x32x16_f16 v[18:33], v[222:225], v[230:233], v[18:33]
	v_mfma_f32_32x32x16_f16 v[18:33], v[222:225], v[226:229], v[18:33]
	v_mfma_f32_32x32x16_f16 v[2:17], v[222:225], v[238:241], v[2:17]
	v_mfma_f32_32x32x16_f16 v[2:17], v[222:225], v[234:237], v[2:17]
	s_cbranch_scc1 .LBB3_3
	s_waitcnt vmcnt(6)
	v_cvt_f16_f32_e32 v209, v174
	v_cvt_f16_f32_e32 v211, v175
	v_cvt_f16_f32_e32 v216, v183
	v_cvt_pk_f16_f32 v210, v174, v175
	v_cvt_f32_f16_e32 v209, v209
	v_cvt_f32_f16_e32 v214, v211
	v_cvt_pk_f16_f32 v211, v176, v177
	v_cvt_f32_f16_e32 v212, v211
	v_sub_f32_e32 v209, v174, v209
	v_sub_f32_e32 v214, v175, v214
	v_cvt_pk_f16_f32 v214, v209, v214
	v_cvt_f16_f32_e32 v209, v182
	v_cvt_f32_f16_sdwa v213, v211 dst_sel:DWORD dst_unused:UNUSED_PAD src0_sel:WORD_1
	v_cvt_f32_f16_e32 v218, v216
	s_cmp_ge_i32 s7, s15
	v_cvt_f32_f16_e32 v209, v209
	v_pk_add_f32 v[212:213], v[176:177], v[212:213] neg_lo:[0,1] neg_hi:[0,1]
	v_sub_f32_e32 v218, v183, v218
	v_cvt_pk_f16_f32 v215, v212, v213
	v_cvt_pk_f16_f32 v213, v184, v185
	v_cvt_f32_f16_e32 v216, v213
	v_cvt_f32_f16_sdwa v217, v213 dst_sel:DWORD dst_unused:UNUSED_PAD src0_sel:WORD_1
	v_cvt_pk_f16_f32 v212, v182, v183
	v_sub_f32_e32 v209, v182, v209
	v_cvt_pk_f16_f32 v218, v209, v218
	ds_write2st64_b64 v200, v[210:211], v[212:213] offset0:64 offset1:72
	v_cvt_f16_f32_e32 v209, v186
	v_cvt_f16_f32_e32 v211, v187
	v_pk_add_f32 v[216:217], v[184:185], v[216:217] neg_lo:[0,1] neg_hi:[0,1]
	v_cvt_pk_f16_f32 v210, v186, v187
	v_cvt_pk_f16_f32 v219, v216, v217
	ds_write2st64_b64 v200, v[214:215], v[218:219] offset0:96 offset1:104
	v_cvt_f32_f16_e32 v209, v209
	v_cvt_f32_f16_e32 v214, v211
	v_cvt_pk_f16_f32 v211, v188, v189
	v_cvt_f32_f16_e32 v212, v211
	v_cvt_f32_f16_sdwa v213, v211 dst_sel:DWORD dst_unused:UNUSED_PAD src0_sel:WORD_1
	v_sub_f32_e32 v209, v186, v209
	v_sub_f32_e32 v214, v187, v214
	v_cvt_pk_f16_f32 v214, v209, v214
	v_cvt_f16_f32_e32 v209, v190
	v_cvt_f16_f32_e32 v216, v191
	v_pk_add_f32 v[212:213], v[188:189], v[212:213] neg_lo:[0,1] neg_hi:[0,1]
	ds_write_b128 v199, v[166:169]
	v_cvt_pk_f16_f32 v215, v212, v213
	v_cvt_pk_f16_f32 v213, v192, v193
	v_cvt_f32_f16_e32 v209, v209
	v_cvt_f32_f16_e32 v218, v216
	v_cvt_f32_f16_e32 v216, v213
	v_cvt_f32_f16_sdwa v217, v213 dst_sel:DWORD dst_unused:UNUSED_PAD src0_sel:WORD_1
	v_sub_f32_e32 v209, v190, v209
	v_sub_f32_e32 v218, v191, v218
	v_cvt_pk_f16_f32 v212, v190, v191
	v_pk_add_f32 v[216:217], v[192:193], v[216:217] neg_lo:[0,1] neg_hi:[0,1]
	v_cvt_pk_f16_f32 v218, v209, v218
	v_cvt_pk_f16_f32 v219, v216, v217
	ds_write_b128 v199, v[170:173] offset:8192
	ds_write2st64_b64 v200, v[210:211], v[212:213] offset0:80 offset1:88
	ds_write2st64_b64 v200, v[214:215], v[218:219] offset0:112 offset1:120
	s_cbranch_scc1 .LBB3_3
	v_lshl_add_u64 v[170:171], v[116:117], 0, s[20:21]
	v_lshl_add_u64 v[182:183], v[114:115], 0, s[22:23]
	v_lshl_add_u64 v[186:187], v[114:115], 0, s[24:25]
	v_lshl_add_u64 v[190:191], v[114:115], 0, s[10:11]
	global_load_dwordx4 v[166:169], v[116:117], off
	s_nop 0
	global_load_dwordx4 v[170:173], v[170:171], off
	s_nop 0
	global_load_dwordx4 v[174:177], v[114:115], off nt
	s_nop 0
	global_load_dwordx4 v[182:185], v[182:183], off nt
	s_nop 0
	global_load_dwordx4 v[186:189], v[186:187], off nt
	s_nop 0
	global_load_dwordx4 v[190:193], v[190:191], off nt
	s_branch .LBB3_3

.LBB3_11:
	s_or_saveexec_b64 s[38:39], s[8:9]
	s_load_dwordx4 s[8:11], s[0:1], 0x20
	s_ashr_i32 s7, s33, 31
	s_ashr_i32 s17, s16, 31
	s_xor_b64 exec, exec, s[38:39]
	s_cbranch_execz .LBB3_20
	v_mov_b32_e32 v129, 0
	s_and_b64 vcc, exec, s[4:5]
	v_mov_b32_e32 v128, v129
	v_mov_b32_e32 v127, v129
	v_mov_b32_e32 v126, v129
	v_mov_b32_e32 v125, v129
	v_mov_b32_e32 v124, v129
	v_mov_b32_e32 v123, v129
	v_mov_b32_e32 v122, v129
	v_mov_b32_e32 v121, v129
	v_mov_b32_e32 v120, v129
	v_mov_b32_e32 v119, v129
	v_mov_b32_e32 v118, v129
	v_mov_b32_e32 v117, v129
	v_mov_b32_e32 v116, v129
	v_mov_b32_e32 v115, v129
	v_mov_b32_e32 v114, v129
	v_mov_b32_e32 v113, v129
	v_mov_b32_e32 v112, v129
	v_mov_b32_e32 v111, v129
	v_mov_b32_e32 v110, v129
	v_mov_b32_e32 v109, v129
	v_mov_b32_e32 v108, v129
	v_mov_b32_e32 v107, v129
	v_mov_b32_e32 v106, v129
	v_mov_b32_e32 v105, v129
	v_mov_b32_e32 v104, v129
	v_mov_b32_e32 v103, v129
	v_mov_b32_e32 v102, v129
	v_mov_b32_e32 v101, v129
	v_mov_b32_e32 v100, v129
	v_mov_b32_e32 v99, v129
	v_mov_b32_e32 v98, v129
	v_mov_b32_e32 v97, v129
	v_mov_b32_e32 v96, v129
	v_mov_b32_e32 v95, v129
	v_mov_b32_e32 v94, v129
	v_mov_b32_e32 v93, v129
	v_mov_b32_e32 v92, v129
	v_mov_b32_e32 v91, v129
	v_mov_b32_e32 v90, v129
	v_mov_b32_e32 v89, v129
	v_mov_b32_e32 v88, v129
	v_mov_b32_e32 v87, v129
	v_mov_b32_e32 v86, v129
	v_mov_b32_e32 v85, v129
	v_mov_b32_e32 v84, v129
	v_mov_b32_e32 v83, v129
	v_mov_b32_e32 v82, v129
	v_mov_b32_e32 v81, v129
	v_mov_b32_e32 v80, v129
	v_mov_b32_e32 v79, v129
	v_mov_b32_e32 v78, v129
	v_mov_b32_e32 v77, v129
	v_mov_b32_e32 v76, v129
	v_mov_b32_e32 v75, v129
	v_mov_b32_e32 v74, v129
	v_mov_b32_e32 v73, v129
	v_mov_b32_e32 v72, v129
	v_mov_b32_e32 v71, v129
	v_mov_b32_e32 v70, v129
	v_mov_b32_e32 v69, v129
	v_mov_b32_e32 v68, v129
	v_mov_b32_e32 v67, v129
	v_mov_b32_e32 v66, v129
	v_mov_b32_e32 v65, v129
	v_mov_b32_e32 v64, v129
	v_mov_b32_e32 v63, v129
	v_mov_b32_e32 v62, v129
	v_mov_b32_e32 v61, v129
	v_mov_b32_e32 v60, v129
	v_mov_b32_e32 v59, v129
	v_mov_b32_e32 v58, v129
	v_mov_b32_e32 v57, v129
	v_mov_b32_e32 v56, v129
	v_mov_b32_e32 v55, v129
	v_mov_b32_e32 v54, v129
	v_mov_b32_e32 v53, v129
	v_mov_b32_e32 v52, v129
	v_mov_b32_e32 v51, v129
	v_mov_b32_e32 v50, v129
	v_mov_b32_e32 v49, v129
	v_mov_b32_e32 v48, v129
	v_mov_b32_e32 v47, v129
	v_mov_b32_e32 v46, v129
	v_mov_b32_e32 v45, v129
	v_mov_b32_e32 v44, v129
	v_mov_b32_e32 v43, v129
	v_mov_b32_e32 v42, v129
	v_mov_b32_e32 v41, v129
	v_mov_b32_e32 v40, v129
	v_mov_b32_e32 v39, v129
	v_mov_b32_e32 v38, v129
	v_mov_b32_e32 v37, v129
	v_mov_b32_e32 v36, v129
	v_mov_b32_e32 v35, v129
	v_mov_b32_e32 v34, v129
	v_mov_b32_e32 v33, v129
	v_mov_b32_e32 v32, v129
	v_mov_b32_e32 v31, v129
	v_mov_b32_e32 v30, v129
	v_mov_b32_e32 v29, v129
	v_mov_b32_e32 v28, v129
	v_mov_b32_e32 v27, v129
	v_mov_b32_e32 v26, v129
	v_mov_b32_e32 v25, v129
	v_mov_b32_e32 v24, v129
	v_mov_b32_e32 v23, v129
	v_mov_b32_e32 v22, v129
	v_mov_b32_e32 v21, v129
	v_mov_b32_e32 v20, v129
	v_mov_b32_e32 v19, v129
	v_mov_b32_e32 v18, v129
	v_mov_b32_e32 v17, v129
	v_mov_b32_e32 v16, v129
	v_mov_b32_e32 v15, v129
	v_mov_b32_e32 v14, v129
	v_mov_b32_e32 v13, v129
	v_mov_b32_e32 v12, v129
	v_mov_b32_e32 v11, v129
	v_mov_b32_e32 v10, v129
	v_mov_b32_e32 v9, v129
	v_mov_b32_e32 v8, v129
	v_mov_b32_e32 v7, v129
	v_mov_b32_e32 v6, v129
	v_mov_b32_e32 v5, v129
	v_mov_b32_e32 v4, v129
	v_mov_b32_e32 v3, v129
	v_mov_b32_e32 v2, v129
	s_cbranch_vccnz .LBB3_20
	v_lshlrev_b32_e32 v6, 6, v0
	v_lshrrev_b32_e32 v2, 6, v0
	v_lshrrev_b32_e32 v3, 5, v1
	v_bfe_u32 v4, v0, 2, 2
	v_and_b32_e32 v6, 0x7c0, v6
	s_add_u32 s0, s28, s36
	v_bitop3_b32 v5, v3, v201, 3 bitop3:0x78
	v_lshl_or_b32 v2, v2, 12, v6
	v_bitop3_b32 v3, v3, v4, 2 bitop3:0x36
	s_addc_u32 s1, s29, s37
	v_lshlrev_b32_e32 v5, 4, v5
	v_or_b32_e32 v7, 0x800, v6
	v_or_b32_e32 v9, 0x1000, v6
	v_or_b32_e32 v11, 0x1800, v6
	v_or_b32_e32 v13, 0x800, v2
	v_lshlrev_b32_e32 v3, 4, v3
	s_add_u32 s4, s26, s30
	v_or_b32_e32 v134, v5, v6
	v_or_b32_e32 v8, v5, v7
	v_or_b32_e32 v10, v5, v9
	v_or_b32_e32 v12, v5, v11
	v_or_b32_e32 v135, v5, v2
	v_or_b32_e32 v136, v13, v5
	v_or_b32_e32 v137, v3, v6
	v_or_b32_e32 v4, v3, v7
	v_or_b32_e32 v5, v3, v9
	v_or_b32_e32 v6, v3, v11
	v_or_b32_e32 v138, v3, v2
	v_or_b32_e32 v139, v3, v13
	v_lshl_add_u64 v[2:3], s[0:1], 0, v[194:195]
	s_mov_b64 s[0:1], 0x200
	s_addc_u32 s5, s27, s31
	v_lshl_add_u64 v[130:131], v[2:3], 0, s[0:1]
	v_lshl_add_u64 v[2:3], s[4:5], 0, v[144:145]
	s_mov_b64 s[4:5], 0x100
	v_lshl_add_u64 v[132:133], v[2:3], 0, s[4:5]
	v_mov_b32_e32 v2, 0
	s_mov_b32 s35, 4
	s_mul_hi_i32 s1, s34, 0x300
	s_mul_i32 s0, s34, 0x300
	v_or_b32_e32 v140, 0x10000, v199
	v_or_b32_e32 v141, 0x12000, v199
	v_or_b32_e32 v142, 0x18000, v200
	v_or_b32_e32 v143, 0x1c000, v200
	v_or_b32_e32 v144, 0x19000, v200
	v_or_b32_e32 v145, 0x1d000, v200
	v_or_b32_e32 v194, 0x18000, v202
	v_or_b32_e32 v195, 0x1c000, v202
	v_or_b32_e32 v201, 0x1b000, v200
	v_or_b32_e32 v202, 0x1f000, v200
	v_or_b32_e32 v203, 0x10000, v8
	v_or_b32_e32 v204, 0x10000, v10
	v_or_b32_e32 v205, 0x10000, v12
	v_or_b32_e32 v206, 0x10000, v4
	v_or_b32_e32 v207, 0x10000, v5
	v_or_b32_e32 v208, 0x10000, v6
	s_mov_b64 s[26:27], 0x80
	v_mov_b32_e32 v3, v2
	v_mov_b32_e32 v4, v2
	v_mov_b32_e32 v5, v2
	v_mov_b32_e32 v6, v2
	v_mov_b32_e32 v7, v2
	v_mov_b32_e32 v8, v2
	v_mov_b32_e32 v9, v2
	v_mov_b32_e32 v10, v2
	v_mov_b32_e32 v11, v2
	v_mov_b32_e32 v12, v2
	v_mov_b32_e32 v13, v2
	v_mov_b32_e32 v14, v2
	v_mov_b32_e32 v15, v2
	v_mov_b32_e32 v16, v2
	v_mov_b32_e32 v17, v2
	v_mov_b32_e32 v18, v2
	v_mov_b32_e32 v19, v2
	v_mov_b32_e32 v20, v2
	v_mov_b32_e32 v21, v2
	v_mov_b32_e32 v22, v2
	v_mov_b32_e32 v23, v2
	v_mov_b32_e32 v24, v2
	v_mov_b32_e32 v25, v2
	v_mov_b32_e32 v26, v2
	v_mov_b32_e32 v27, v2
	v_mov_b32_e32 v28, v2
	v_mov_b32_e32 v29, v2
	v_mov_b32_e32 v30, v2
	v_mov_b32_e32 v31, v2
	v_mov_b32_e32 v32, v2
	v_mov_b32_e32 v33, v2
	v_mov_b32_e32 v34, v2
	v_mov_b32_e32 v35, v2
	v_mov_b32_e32 v36, v2
	v_mov_b32_e32 v37, v2
	v_mov_b32_e32 v38, v2
	v_mov_b32_e32 v39, v2
	v_mov_b32_e32 v40, v2
	v_mov_b32_e32 v41, v2
	v_mov_b32_e32 v42, v2
	v_mov_b32_e32 v43, v2
	v_mov_b32_e32 v44, v2
	v_mov_b32_e32 v45, v2
	v_mov_b32_e32 v46, v2
	v_mov_b32_e32 v47, v2
	v_mov_b32_e32 v48, v2
	v_mov_b32_e32 v49, v2
	v_mov_b32_e32 v50, v2
	v_mov_b32_e32 v51, v2
	v_mov_b32_e32 v52, v2
	v_mov_b32_e32 v53, v2
	v_mov_b32_e32 v54, v2
	v_mov_b32_e32 v55, v2
	v_mov_b32_e32 v56, v2
	v_mov_b32_e32 v57, v2
	v_mov_b32_e32 v58, v2
	v_mov_b32_e32 v59, v2
	v_mov_b32_e32 v60, v2
	v_mov_b32_e32 v61, v2
	v_mov_b32_e32 v62, v2
	v_mov_b32_e32 v63, v2
	v_mov_b32_e32 v64, v2
	v_mov_b32_e32 v65, v2
	v_mov_b32_e32 v66, v2
	v_mov_b32_e32 v67, v2
	v_mov_b32_e32 v68, v2
	v_mov_b32_e32 v69, v2
	v_mov_b32_e32 v70, v2
	v_mov_b32_e32 v71, v2
	v_mov_b32_e32 v72, v2
	v_mov_b32_e32 v73, v2
	v_mov_b32_e32 v74, v2
	v_mov_b32_e32 v75, v2
	v_mov_b32_e32 v76, v2
	v_mov_b32_e32 v77, v2
	v_mov_b32_e32 v78, v2
	v_mov_b32_e32 v79, v2
	v_mov_b32_e32 v80, v2
	v_mov_b32_e32 v81, v2
	v_mov_b32_e32 v82, v2
	v_mov_b32_e32 v83, v2
	v_mov_b32_e32 v84, v2
	v_mov_b32_e32 v85, v2
	v_mov_b32_e32 v86, v2
	v_mov_b32_e32 v87, v2
	v_mov_b32_e32 v88, v2
	v_mov_b32_e32 v89, v2
	v_mov_b32_e32 v90, v2
	v_mov_b32_e32 v91, v2
	v_mov_b32_e32 v92, v2
	v_mov_b32_e32 v93, v2
	v_mov_b32_e32 v94, v2
	v_mov_b32_e32 v95, v2
	v_mov_b32_e32 v96, v2
	v_mov_b32_e32 v97, v2
	v_mov_b32_e32 v98, v2
	v_mov_b32_e32 v99, v2
	v_mov_b32_e32 v100, v2
	v_mov_b32_e32 v101, v2
	v_mov_b32_e32 v102, v2
	v_mov_b32_e32 v103, v2
	v_mov_b32_e32 v104, v2
	v_mov_b32_e32 v105, v2
	v_mov_b32_e32 v106, v2
	v_mov_b32_e32 v107, v2
	v_mov_b32_e32 v108, v2
	v_mov_b32_e32 v109, v2
	v_mov_b32_e32 v110, v2
	v_mov_b32_e32 v111, v2
	v_mov_b32_e32 v112, v2
	v_mov_b32_e32 v113, v2
	v_mov_b32_e32 v114, v2
	v_mov_b32_e32 v115, v2
	v_mov_b32_e32 v116, v2
	v_mov_b32_e32 v117, v2
	v_mov_b32_e32 v118, v2
	v_mov_b32_e32 v119, v2
	v_mov_b32_e32 v120, v2
	v_mov_b32_e32 v121, v2
	v_mov_b32_e32 v122, v2
	v_mov_b32_e32 v123, v2
	v_mov_b32_e32 v124, v2
	v_mov_b32_e32 v125, v2
	v_mov_b32_e32 v126, v2
	v_mov_b32_e32 v127, v2
	v_mov_b32_e32 v128, v2
	v_mov_b32_e32 v129, v2
	s_waitcnt vmcnt(3)
	s_branch .LBB3_15

.LBB3_15:
	ds_read_b128 v[210:213], v134
	ds_read_b128 v[214:217], v134 offset:2048
	ds_read_b128 v[218:221], v134 offset:4096
	ds_read_b128 v[222:225], v134 offset:6144
	ds_read_b128 v[230:233], v135 offset:49152
	ds_read_b128 v[226:229], v135 offset:32768
	s_add_i32 s28, s35, -2
	s_cmp_lt_i32 s28, s15
	s_cbranch_scc1 .Lgk_lo_steady
	s_waitcnt vmcnt(0)
.Lgk_lo_steady:
	s_waitcnt vmcnt(6)
	v_cvt_f16_f32_e32 v209, v150
	s_add_i32 s28, s35, -1
	s_cmp_ge_i32 s28, s15
	s_waitcnt lgkmcnt(0)
	v_mfma_f32_32x32x16_f16 v[114:129], v[210:213], v[230:233], v[114:129]
	ds_read_b128 v[238:241], v135 offset:51200
	ds_read_b128 v[234:237], v135 offset:34816
	v_cvt_f32_f16_e32 v209, v209
	v_sub_f32_e32 v209, v150, v209
	v_mfma_f32_32x32x16_f16 v[114:129], v[210:213], v[226:229], v[114:129]
	s_waitcnt lgkmcnt(1)
	v_mfma_f32_32x32x16_f16 v[98:113], v[210:213], v[238:241], v[98:113]
	s_waitcnt lgkmcnt(0)
	v_mfma_f32_32x32x16_f16 v[98:113], v[210:213], v[234:237], v[98:113]
	ds_read_b128 v[210:213], v137
	v_mfma_f32_32x32x16_f16 v[82:97], v[214:217], v[230:233], v[82:97]
	v_mfma_f32_32x32x16_f16 v[82:97], v[214:217], v[226:229], v[82:97]
	v_mfma_f32_32x32x16_f16 v[66:81], v[214:217], v[238:241], v[66:81]
	v_mfma_f32_32x32x16_f16 v[66:81], v[214:217], v[234:237], v[66:81]
	ds_read_b128 v[214:217], v137 offset:2048
	v_mfma_f32_32x32x16_f16 v[50:65], v[218:221], v[230:233], v[50:65]
	v_mfma_f32_32x32x16_f16 v[50:65], v[218:221], v[226:229], v[50:65]
	v_mfma_f32_32x32x16_f16 v[34:49], v[218:221], v[238:241], v[34:49]
	v_mfma_f32_32x32x16_f16 v[34:49], v[218:221], v[234:237], v[34:49]
	ds_read_b128 v[218:221], v137 offset:4096
	v_mfma_f32_32x32x16_f16 v[18:33], v[222:225], v[230:233], v[18:33]
	ds_read_b128 v[230:233], v138 offset:49152
	v_mfma_f32_32x32x16_f16 v[18:33], v[222:225], v[226:229], v[18:33]
	ds_read_b128 v[226:229], v138 offset:32768
	v_mfma_f32_32x32x16_f16 v[2:17], v[222:225], v[238:241], v[2:17]
	ds_read_b128 v[238:241], v138 offset:51200
	v_mfma_f32_32x32x16_f16 v[2:17], v[222:225], v[234:237], v[2:17]
	ds_read_b128 v[222:225], v137 offset:6144
	ds_read_b128 v[234:237], v138 offset:34816
	s_waitcnt lgkmcnt(4)
	v_mfma_f32_32x32x16_f16 v[114:129], v[210:213], v[230:233], v[114:129]
	ds_write_b128 v140, v[146:149]
	ds_write_b128 v141, v[162:165]
	s_waitcnt lgkmcnt(5)
	v_mfma_f32_32x32x16_f16 v[114:129], v[210:213], v[226:229], v[114:129]
	s_waitcnt lgkmcnt(4)
	v_mfma_f32_32x32x16_f16 v[98:113], v[210:213], v[238:241], v[98:113]
	s_waitcnt lgkmcnt(2)
	v_mfma_f32_32x32x16_f16 v[98:113], v[210:213], v[234:237], v[98:113]
	v_cvt_f16_f32_e32 v211, v151
	v_cvt_pk_f16_f32 v210, v150, v151
	v_cvt_f32_f16_e32 v211, v211
	v_sub_f32_e32 v211, v151, v211
	v_cvt_pk_f16_f32 v212, v209, v211
	v_cvt_pk_f16_f32 v211, v152, v153
	ds_write_b64 v142, v[210:211]
	v_mfma_f32_32x32x16_f16 v[82:97], v[214:217], v[230:233], v[82:97]
	v_cvt_f16_f32_e32 v209, v154
	v_cvt_pk_f16_f32 v210, v154, v155
	v_cvt_f32_f16_e32 v209, v209
	v_sub_f32_e32 v209, v154, v209
	v_mfma_f32_32x32x16_f16 v[82:97], v[214:217], v[226:229], v[82:97]
	v_mfma_f32_32x32x16_f16 v[66:81], v[214:217], v[238:241], v[66:81]
	v_mfma_f32_32x32x16_f16 v[66:81], v[214:217], v[234:237], v[66:81]
	v_cvt_f32_f16_e32 v214, v211
	v_cvt_f32_f16_sdwa v215, v211 dst_sel:DWORD dst_unused:UNUSED_PAD src0_sel:WORD_1
	v_cvt_f16_f32_e32 v211, v155
	v_add_f32_e64 v214, v152, -v214
	v_add_f32_e64 v215, v153, -v215
	v_cvt_f32_f16_e32 v211, v211
	v_cvt_pk_f16_f32 v213, v214, v215
	ds_write_b64 v143, v[212:213]
	v_sub_f32_e32 v211, v155, v211
	v_cvt_pk_f16_f32 v212, v209, v211
	v_cvt_pk_f16_f32 v211, v156, v157
	v_cvt_f32_f16_e32 v214, v211
	v_cvt_f32_f16_sdwa v215, v211 dst_sel:DWORD dst_unused:UNUSED_PAD src0_sel:WORD_1
	ds_write_b64 v144, v[210:211]
	v_cvt_f16_f32_e32 v209, v158
	v_cvt_f16_f32_e32 v211, v159
	v_pk_add_f32 v[214:215], v[156:157], v[214:215] neg_lo:[0,1] neg_hi:[0,1]
	v_mfma_f32_32x32x16_f16 v[50:65], v[218:221], v[230:233], v[50:65]
	v_cvt_f32_f16_e32 v209, v209
	v_cvt_f32_f16_e32 v211, v211
	v_cvt_pk_f16_f32 v213, v214, v215
	ds_write_b64 v145, v[212:213]
	v_sub_f32_e32 v209, v158, v209
	v_sub_f32_e32 v211, v159, v211
	v_cvt_pk_f16_f32 v210, v158, v159
	v_cvt_pk_f16_f32 v212, v209, v211
	v_cvt_pk_f16_f32 v211, v160, v161
	v_cvt_f32_f16_e32 v214, v211
	v_cvt_f32_f16_sdwa v215, v211 dst_sel:DWORD dst_unused:UNUSED_PAD src0_sel:WORD_1
	ds_write_b64 v194, v[210:211]
	v_cvt_f16_f32_e32 v209, v178
	v_cvt_f16_f32_e32 v211, v179
	v_pk_add_f32 v[214:215], v[160:161], v[214:215] neg_lo:[0,1] neg_hi:[0,1]
	v_mfma_f32_32x32x16_f16 v[50:65], v[218:221], v[226:229], v[50:65]
	v_cvt_f32_f16_e32 v209, v209
	v_cvt_f32_f16_e32 v211, v211
	v_cvt_pk_f16_f32 v213, v214, v215
	ds_write_b64 v195, v[212:213]
	v_sub_f32_e32 v209, v178, v209
	v_sub_f32_e32 v211, v179, v211
	v_cvt_pk_f16_f32 v210, v178, v179
	v_cvt_pk_f16_f32 v212, v209, v211
	v_cvt_pk_f16_f32 v211, v180, v181
	ds_write_b64 v201, v[210:211]
	v_mfma_f32_32x32x16_f16 v[34:49], v[218:221], v[238:241], v[34:49]
	v_cvt_f32_f16_e32 v214, v211
	v_cvt_f32_f16_sdwa v215, v211 dst_sel:DWORD dst_unused:UNUSED_PAD src0_sel:WORD_1
	v_add_f32_e64 v214, v180, -v214
	v_add_f32_e64 v215, v181, -v215
	v_cvt_pk_f16_f32 v213, v214, v215
	ds_write_b64 v202, v[212:213]
	v_mfma_f32_32x32x16_f16 v[34:49], v[218:221], v[234:237], v[34:49]
	v_mfma_f32_32x32x16_f16 v[18:33], v[222:225], v[230:233], v[18:33]
	v_mfma_f32_32x32x16_f16 v[18:33], v[222:225], v[226:229], v[18:33]
	v_mfma_f32_32x32x16_f16 v[2:17], v[222:225], v[238:241], v[2:17]
	v_mfma_f32_32x32x16_f16 v[2:17], v[222:225], v[234:237], v[2:17]
	s_cbranch_scc1 .LBB3_17
	v_lshl_add_u64 v[150:151], v[132:133], 0, s[20:21]
	v_lshl_add_u64 v[154:155], v[130:131], 0, s[22:23]
	v_lshl_add_u64 v[158:159], v[130:131], 0, s[24:25]
	v_lshl_add_u64 v[178:179], v[130:131], 0, s[0:1]
	global_load_dwordx4 v[146:149], v[132:133], off offset:-64
	global_load_dwordx4 v[162:165], v[150:151], off offset:-64
	s_nop 0
	global_load_dwordx4 v[150:153], v[130:131], off offset:-128 nt
	s_nop 0
	global_load_dwordx4 v[154:157], v[154:155], off offset:-128 nt
	s_nop 0
	global_load_dwordx4 v[158:161], v[158:159], off offset:-128 nt
	s_nop 0
	global_load_dwordx4 v[178:181], v[178:179], off offset:-128 nt
.LBB3_17:
	v_or_b32_e32 v209, 0x10000, v134
	s_waitcnt lgkmcnt(0)
	s_barrier
	ds_read_b128 v[210:213], v209
	v_or_b32_e32 v209, 0x18000, v135
	ds_read_b128 v[214:217], v203
	ds_read_b128 v[218:221], v204
	ds_read_b128 v[222:225], v205
	ds_read_b128 v[226:229], v209
	v_add_u32_e32 v209, 0x1c000, v135
	ds_read_b128 v[230:233], v209
	s_waitcnt lgkmcnt(0)
	v_mfma_f32_32x32x16_f16 v[114:129], v[210:213], v[230:233], v[114:129]
	v_or_b32_e32 v209, 0x18000, v136
	ds_read_b128 v[234:237], v209
	v_add_u32_e32 v209, 0x1c000, v136
	ds_read_b128 v[238:241], v209
	v_or_b32_e32 v209, 0x10000, v137
	s_add_i32 s28, s35, -2
	s_cmp_ge_i32 s28, s15
	v_mfma_f32_32x32x16_f16 v[114:129], v[210:213], v[226:229], v[114:129]
	s_waitcnt lgkmcnt(0)
	v_mfma_f32_32x32x16_f16 v[98:113], v[210:213], v[238:241], v[98:113]
	v_mfma_f32_32x32x16_f16 v[98:113], v[210:213], v[234:237], v[98:113]
	ds_read_b128 v[210:213], v209
	v_or_b32_e32 v209, 0x18000, v138
	v_mfma_f32_32x32x16_f16 v[82:97], v[214:217], v[230:233], v[82:97]
	v_mfma_f32_32x32x16_f16 v[82:97], v[214:217], v[226:229], v[82:97]
	v_mfma_f32_32x32x16_f16 v[66:81], v[214:217], v[238:241], v[66:81]
	v_mfma_f32_32x32x16_f16 v[66:81], v[214:217], v[234:237], v[66:81]
	ds_read_b128 v[214:217], v206
	v_mfma_f32_32x32x16_f16 v[50:65], v[218:221], v[230:233], v[50:65]
	v_mfma_f32_32x32x16_f16 v[50:65], v[218:221], v[226:229], v[50:65]
	v_mfma_f32_32x32x16_f16 v[34:49], v[218:221], v[238:241], v[34:49]
	v_mfma_f32_32x32x16_f16 v[34:49], v[218:221], v[234:237], v[34:49]
	ds_read_b128 v[218:221], v207
	v_mfma_f32_32x32x16_f16 v[18:33], v[222:225], v[230:233], v[18:33]
	v_mfma_f32_32x32x16_f16 v[18:33], v[222:225], v[226:229], v[18:33]
	ds_read_b128 v[226:229], v209
	v_add_u32_e32 v209, 0x1c000, v138
	ds_read_b128 v[230:233], v209
	v_or_b32_e32 v209, 0x18000, v139
	v_mfma_f32_32x32x16_f16 v[2:17], v[222:225], v[238:241], v[2:17]
	v_mfma_f32_32x32x16_f16 v[2:17], v[222:225], v[234:237], v[2:17]
	ds_read_b128 v[222:225], v208
	ds_read_b128 v[234:237], v209
	v_add_u32_e32 v209, 0x1c000, v139
	s_waitcnt lgkmcnt(2)
	v_mfma_f32_32x32x16_f16 v[114:129], v[210:213], v[230:233], v[114:129]
	ds_read_b128 v[238:241], v209
	v_mfma_f32_32x32x16_f16 v[114:129], v[210:213], v[226:229], v[114:129]
	s_waitcnt lgkmcnt(0)
	v_mfma_f32_32x32x16_f16 v[98:113], v[210:213], v[238:241], v[98:113]
	v_mfma_f32_32x32x16_f16 v[98:113], v[210:213], v[234:237], v[98:113]
	v_mfma_f32_32x32x16_f16 v[82:97], v[214:217], v[230:233], v[82:97]
	v_mfma_f32_32x32x16_f16 v[82:97], v[214:217], v[226:229], v[82:97]
	v_mfma_f32_32x32x16_f16 v[66:81], v[214:217], v[238:241], v[66:81]
	v_mfma_f32_32x32x16_f16 v[66:81], v[214:217], v[234:237], v[66:81]
	v_mfma_f32_32x32x16_f16 v[50:65], v[218:221], v[230:233], v[50:65]
	v_mfma_f32_32x32x16_f16 v[50:65], v[218:221], v[226:229], v[50:65]
	v_mfma_f32_32x32x16_f16 v[34:49], v[218:221], v[238:241], v[34:49]
	v_mfma_f32_32x32x16_f16 v[34:49], v[218:221], v[234:237], v[34:49]
	v_mfma_f32_32x32x16_f16 v[18:33], v[222:225], v[230:233], v[18:33]
	v_mfma_f32_32x32x16_f16 v[18:33], v[222:225], v[226:229], v[18:33]
	v_mfma_f32_32x32x16_f16 v[2:17], v[222:225], v[238:241], v[2:17]
	v_mfma_f32_32x32x16_f16 v[2:17], v[222:225], v[234:237], v[2:17]
	s_cbranch_scc1 .LBB3_14
	s_waitcnt vmcnt(6)
	v_cvt_f16_f32_e32 v209, v174
	v_cvt_f16_f32_e32 v211, v175
	v_cvt_f16_f32_e32 v216, v183
	v_cvt_pk_f16_f32 v210, v174, v175
	v_cvt_f32_f16_e32 v209, v209
	v_cvt_f32_f16_e32 v214, v211
	v_cvt_pk_f16_f32 v211, v176, v177
	v_cvt_f32_f16_e32 v212, v211
	v_sub_f32_e32 v209, v174, v209
	v_sub_f32_e32 v214, v175, v214
	v_cvt_pk_f16_f32 v214, v209, v214
	v_cvt_f16_f32_e32 v209, v182
	v_cvt_f32_f16_sdwa v213, v211 dst_sel:DWORD dst_unused:UNUSED_PAD src0_sel:WORD_1
	v_cvt_f32_f16_e32 v218, v216
	s_cmp_ge_i32 s35, s15
	v_cvt_f32_f16_e32 v209, v209
	v_pk_add_f32 v[212:213], v[176:177], v[212:213] neg_lo:[0,1] neg_hi:[0,1]
	v_sub_f32_e32 v218, v183, v218
	v_cvt_pk_f16_f32 v215, v212, v213
	v_cvt_pk_f16_f32 v213, v184, v185
	v_cvt_f32_f16_e32 v216, v213
	v_cvt_f32_f16_sdwa v217, v213 dst_sel:DWORD dst_unused:UNUSED_PAD src0_sel:WORD_1
	v_cvt_pk_f16_f32 v212, v182, v183
	v_sub_f32_e32 v209, v182, v209
	v_cvt_pk_f16_f32 v218, v209, v218
	ds_write2st64_b64 v200, v[210:211], v[212:213] offset0:64 offset1:72
	v_cvt_f16_f32_e32 v209, v186
	v_cvt_f16_f32_e32 v211, v187
	v_pk_add_f32 v[216:217], v[184:185], v[216:217] neg_lo:[0,1] neg_hi:[0,1]
	v_cvt_pk_f16_f32 v210, v186, v187
	v_cvt_pk_f16_f32 v219, v216, v217
	ds_write2st64_b64 v200, v[214:215], v[218:219] offset0:96 offset1:104
	v_cvt_f32_f16_e32 v209, v209
	v_cvt_f32_f16_e32 v214, v211
	v_cvt_pk_f16_f32 v211, v188, v189
	v_cvt_f32_f16_e32 v212, v211
	v_cvt_f32_f16_sdwa v213, v211 dst_sel:DWORD dst_unused:UNUSED_PAD src0_sel:WORD_1
	v_sub_f32_e32 v209, v186, v209
	v_sub_f32_e32 v214, v187, v214
	v_cvt_pk_f16_f32 v214, v209, v214
	v_cvt_f16_f32_e32 v209, v190
	v_cvt_f16_f32_e32 v216, v191
	v_pk_add_f32 v[212:213], v[188:189], v[212:213] neg_lo:[0,1] neg_hi:[0,1]
	ds_write_b128 v199, v[166:169]
	v_cvt_pk_f16_f32 v215, v212, v213
	v_cvt_pk_f16_f32 v213, v192, v193
	v_cvt_f32_f16_e32 v209, v209
	v_cvt_f32_f16_e32 v218, v216
	v_cvt_f32_f16_e32 v216, v213
	v_cvt_f32_f16_sdwa v217, v213 dst_sel:DWORD dst_unused:UNUSED_PAD src0_sel:WORD_1
	v_sub_f32_e32 v209, v190, v209
	v_sub_f32_e32 v218, v191, v218
	v_cvt_pk_f16_f32 v212, v190, v191
	v_pk_add_f32 v[216:217], v[192:193], v[216:217] neg_lo:[0,1] neg_hi:[0,1]
	v_cvt_pk_f16_f32 v218, v209, v218
	v_cvt_pk_f16_f32 v219, v216, v217
	ds_write_b128 v199, v[170:173] offset:8192
	ds_write2st64_b64 v200, v[210:211], v[212:213] offset0:80 offset1:88
	ds_write2st64_b64 v200, v[214:215], v[218:219] offset0:112 offset1:120
	s_cbranch_scc1 .LBB3_14
	v_lshl_add_u64 v[170:171], v[132:133], 0, s[20:21]
	v_lshl_add_u64 v[182:183], v[130:131], 0, s[22:23]
	v_lshl_add_u64 v[186:187], v[130:131], 0, s[24:25]
	v_lshl_add_u64 v[190:191], v[130:131], 0, s[0:1]
	global_load_dwordx4 v[166:169], v[132:133], off
	s_nop 0
	global_load_dwordx4 v[170:173], v[170:171], off
	s_nop 0
	global_load_dwordx4 v[174:177], v[130:131], off nt
	s_nop 0
	global_load_dwordx4 v[182:185], v[182:183], off nt
	s_nop 0
	global_load_dwordx4 v[186:189], v[186:187], off nt
	s_nop 0
	global_load_dwordx4 v[190:193], v[190:191], off nt
	s_branch .LBB3_14

.LBB3_56:
	s_endpgm
	.p2align	8

	.text
	.p2alignl 6, 3212836864
	.fill 256, 4, 3212836864
	.p2align	8

amdhsa.kernels:
  - .agpr_count:     16
    .args:
      - .actual_access:  read_only
        .address_space:  global
        .offset:         0
        .size:           8
        .value_kind:     global_buffer
      - .actual_access:  read_only
        .address_space:  global
        .offset:         8
        .size:           8
        .value_kind:     global_buffer
      - .actual_access:  read_only
        .address_space:  global
        .offset:         16
        .size:           8
        .value_kind:     global_buffer
      - .actual_access:  read_only
        .address_space:  global
        .offset:         24
        .size:           8
        .value_kind:     global_buffer
      - .actual_access:  write_only
        .address_space:  global
        .offset:         32
        .size:           8
        .value_kind:     global_buffer
      - .actual_access:  read_only
        .address_space:  global
        .offset:         40
        .size:           8
        .value_kind:     global_buffer
      - .actual_access:  write_only
        .address_space:  global
        .offset:         48
        .size:           8
        .value_kind:     global_buffer
      - .actual_access:  write_only
        .address_space:  global
        .offset:         56
        .size:           8
        .value_kind:     global_buffer
      - .actual_access:  write_only
        .address_space:  global
        .offset:         64
        .size:           8
        .value_kind:     global_buffer
    .group_segment_fixed_size: 18432
    .kernarg_segment_align: 8
    .kernarg_segment_size: 72
    .language:       OpenCL C
    .language_version:
      - 2
      - 0
    .max_flat_workgroup_size: 64
    .name:           _Z6prep_kPKfS0_S0_S0_PDF16_S1_S1_PfS2_
    .private_segment_fixed_size: 0
    .sgpr_count:     22
    .sgpr_spill_count: 0
    .symbol:         _Z6prep_kPKfS0_S0_S0_PDF16_S1_S1_PfS2_.kd
    .uniform_work_group_size: 1
    .uses_dynamic_stack: false
    .vgpr_count:     168
    .vgpr_spill_count: 0
    .wavefront_size: 64
  - .agpr_count:     0
    .args:
      - .address_space:  global
        .offset:         0
        .size:           8
        .value_kind:     global_buffer
      - .address_space:  global
        .offset:         8
        .size:           8
        .value_kind:     global_buffer
      - .actual_access:  write_only
        .address_space:  global
        .offset:         16
        .size:           8
        .value_kind:     global_buffer
      - .actual_access:  read_only
        .address_space:  global
        .offset:         24
        .size:           8
        .value_kind:     global_buffer
      - .offset:         32
        .size:           4
        .value_kind:     by_value
    .group_segment_fixed_size: 131072
    .kernarg_segment_align: 8
    .kernarg_segment_size: 36
    .language:       OpenCL C
    .language_version:
      - 2
      - 0
    .max_flat_workgroup_size: 512
    .name:           _ZN2g817gemm_256sq_8phaseEPKDF16_S1_PfPKff
    .private_segment_fixed_size: 0
    .sgpr_count:     31
    .sgpr_spill_count: 0
    .symbol:         _ZN2g817gemm_256sq_8phaseEPKDF16_S1_PfPKff.kd
    .uniform_work_group_size: 1
    .uses_dynamic_stack: false
    .vgpr_count:     248
    .vgpr_spill_count: 0
    .wavefront_size: 64
  - .agpr_count:     0
    .args:
      - .actual_access:  read_only
        .address_space:  global
        .offset:         0
        .size:           8
        .value_kind:     global_buffer
      - .actual_access:  read_only
        .address_space:  global
        .offset:         8
        .size:           8
        .value_kind:     global_buffer
      - .actual_access:  write_only
        .address_space:  global
        .offset:         16
        .size:           8
        .value_kind:     global_buffer
      - .actual_access:  read_only
        .address_space:  global
        .offset:         24
        .size:           8
        .value_kind:     global_buffer
      - .offset:         32
        .size:           4
        .value_kind:     by_value
    .group_segment_fixed_size: 131072
    .kernarg_segment_align: 8
    .kernarg_segment_size: 36
    .language:       OpenCL C
    .language_version:
      - 2
      - 0
    .max_flat_workgroup_size: 512
    .name:           _ZN3r147gemm_q2ILi64EEEvPKfPKDF16_PDF16_S2_f
    .private_segment_fixed_size: 0
    .sgpr_count:     26
    .sgpr_spill_count: 0
    .symbol:         _ZN3r147gemm_q2ILi64EEEvPKfPKDF16_PDF16_S2_f.kd
    .uniform_work_group_size: 1
    .uses_dynamic_stack: false
    .vgpr_count:     246
    .vgpr_spill_count: 0
    .wavefront_size: 64
  - .agpr_count:     0
    .args:
      - .actual_access:  read_only
        .address_space:  global
        .offset:         0
        .size:           8
        .value_kind:     global_buffer
      - .actual_access:  read_only
        .address_space:  global
        .offset:         8
        .size:           8
        .value_kind:     global_buffer
      - .actual_access:  read_only
        .address_space:  global
        .offset:         16
        .size:           8
        .value_kind:     global_buffer
      - .actual_access:  read_only
        .address_space:  global
        .offset:         24
        .size:           8
        .value_kind:     global_buffer
      - .actual_access:  write_only
        .address_space:  global
        .offset:         32
        .size:           8
        .value_kind:     global_buffer
      - .actual_access:  write_only
        .address_space:  global
        .offset:         40
        .size:           8
        .value_kind:     global_buffer
      - .actual_access:  read_only
        .address_space:  global
        .offset:         48
        .size:           8
        .value_kind:     global_buffer
      - .offset:         56
        .size:           4
        .value_kind:     by_value
      - .offset:         60
        .size:           4
        .value_kind:     by_value
      - .offset:         64
        .size:           4
        .value_kind:     by_value
      - .offset:         68
        .size:           4
        .value_kind:     by_value
      - .offset:         72
        .size:           4
        .value_kind:     by_value
      - .offset:         76
        .size:           4
        .value_kind:     by_value
      - .offset:         80
        .size:           8
        .value_kind:     by_value
      - .offset:         88
        .size:           8
        .value_kind:     by_value
      - .offset:         96
        .size:           8
        .value_kind:     by_value
      - .offset:         104
        .size:           4
        .value_kind:     by_value
      - .offset:         112
        .size:           4
        .value_kind:     hidden_block_count_x
      - .offset:         116
        .size:           4
        .value_kind:     hidden_block_count_y
      - .offset:         120
        .size:           4
        .value_kind:     hidden_block_count_z
      - .offset:         124
        .size:           2
        .value_kind:     hidden_group_size_x
      - .offset:         126
        .size:           2
        .value_kind:     hidden_group_size_y
      - .offset:         128
        .size:           2
        .value_kind:     hidden_group_size_z
      - .offset:         130
        .size:           2
        .value_kind:     hidden_remainder_x
      - .offset:         132
        .size:           2
        .value_kind:     hidden_remainder_y
      - .offset:         134
        .size:           2
        .value_kind:     hidden_remainder_z
      - .offset:         152
        .size:           8
        .value_kind:     hidden_global_offset_x
      - .offset:         160
        .size:           8
        .value_kind:     hidden_global_offset_y
      - .offset:         168
        .size:           8
        .value_kind:     hidden_global_offset_z
      - .offset:         176
        .size:           2
        .value_kind:     hidden_grid_dims
    .group_segment_fixed_size: 131072
    .kernarg_segment_align: 8
    .kernarg_segment_size: 368
    .language:       OpenCL C
    .language_version:
      - 2
      - 0
    .max_flat_workgroup_size: 512
    .name:           _Z6gemm_kILi1ELi0ELi2ELi3EEvPKvS1_S1_S1_PvS2_PKfiiiiiilllf
    .private_segment_fixed_size: 0
    .sgpr_count:     48
    .sgpr_spill_count: 0
    .symbol:         _Z6gemm_kILi1ELi0ELi2ELi3EEvPKvS1_S1_S1_PvS2_PKfiiiiiilllf.kd
    .uniform_work_group_size: 1
    .uses_dynamic_stack: false
    .vgpr_count:     242
    .vgpr_spill_count: 0
    .wavefront_size: 64
  - .agpr_count:     0
    .args:
      - .actual_access:  read_only
        .address_space:  global
        .offset:         0
        .size:           8
        .value_kind:     global_buffer
      - .actual_access:  read_only
        .address_space:  global
        .offset:         8
        .size:           8
        .value_kind:     global_buffer
      - .actual_access:  write_only
        .address_space:  global
        .offset:         16
        .size:           8
        .value_kind:     global_buffer
      - .address_space:  global
        .offset:         24
        .size:           8
        .value_kind:     global_buffer
      - .actual_access:  read_only
        .address_space:  global
        .offset:         32
        .size:           8
        .value_kind:     global_buffer
      - .offset:         40
        .size:           4
        .value_kind:     by_value
      - .offset:         44
        .size:           4
        .value_kind:     by_value
      - .offset:         48
        .size:           4
        .value_kind:     by_value
      - .offset:         52
        .size:           4
        .value_kind:     by_value
      - .offset:         56
        .size:           4
        .value_kind:     by_value
      - .offset:         60
        .size:           4
        .value_kind:     by_value
      - .offset:         64
        .size:           8
        .value_kind:     by_value
      - .offset:         72
        .size:           8
        .value_kind:     by_value
      - .offset:         80
        .size:           8
        .value_kind:     by_value
      - .offset:         88
        .size:           4
        .value_kind:     by_value
    .group_segment_fixed_size: 131072
    .kernarg_segment_align: 8
    .kernarg_segment_size: 92
    .language:       OpenCL C
    .language_version:
      - 2
      - 0
    .max_flat_workgroup_size: 512
    .name:           _Z7gemm2_kILi5ELi3ELi1EEvPKvS1_PvS2_PKfiiiiiilllf
    .private_segment_fixed_size: 0
    .sgpr_count:     44
    .sgpr_spill_count: 0
    .symbol:         _Z7gemm2_kILi5ELi3ELi1EEvPKvS1_PvS2_PKfiiiiiilllf.kd
    .uniform_work_group_size: 1
    .uses_dynamic_stack: false
    .vgpr_count:     234
    .vgpr_spill_count: 0
    .wavefront_size: 64
